# plus LayerNorm/rms wave sums and router top-4 butterflies on DPP / permlane swaps instead of ds_bpermute chains (bit-identical)
# speedup vs baseline: 1.0115x; 1.0026x over previous
; #define IN(k) ((const float*)gptr(ldp(PT, k)))
; __device__ __forceinline__ void ln_rows_pre(f32x4 (&v)[4], const LnAff& a) {
;     float s = 0.f;
; #pragma unroll
;     for (int j = 0; j < 4; ++j) s += (v[j][0] + v[j][1]) + (v[j][2] + v[j][3]);
;     const float mean = wave_sum(s) * (1.f / D); float s2 = 0.f;
; #pragma unroll
;     for (int j = 0; j < 4; ++j) { v[j] = v[j] - mean; s2 += (v[j][0] * v[j][0] + v[j][1] * v[j][1]) + (v[j][2] * v[j][2] + v[j][3] * v[j][3]); }
;     const float rstd = 1.f / sqrtf(wave_sum(s2) * (1.f / D) + LN_EPS);
; __global__ void __launch_bounds__(NWAVES * 64, 2) fwd(Args args) {
;     ...
;         for (int m = F.gw; m < M; m += F.NGW) { const float* xp = IN(0) + (size_t)m * D; f32x4 v[4];
; #pragma unroll
;             for (int j = 0; j < 4; ++j) v[j] = *(const f32x4*)(xp + 4 * lane + 256 * j);
;             ln_rows_pre(v, aff0); store_row_f32_bf16(v, nullptr, Hf + (size_t)m * D, lane); store_row_fp8(v, (unsigned char*)Hb + (size_t)m * D, lane); }
.LBB0_250:
	ds_read_b64 v[38:39], v44
	v_lshl_add_u64 v[40:41], s[58:59], 0, v[34:35]
	v_add_co_u32_e32 v42, vcc, s13, v40
	v_lshl_add_u64 v[48:49], s[58:59], 0, v[32:33]
	s_nop 0
	v_addc_co_u32_e32 v43, vcc, 0, v41, vcc
	s_waitcnt lgkmcnt(0)
	v_readfirstlane_b32 s1, v39
	v_readfirstlane_b32 s0, v38
	v_add_co_u32_e32 v40, vcc, s16, v48
	s_nop 0
	v_lshl_add_u64 v[38:39], s[0:1], 0, v[36:37]
	v_addc_co_u32_e32 v41, vcc, 0, v49, vcc
	global_load_dwordx4 v[48:51], v[38:39], off
	global_load_dwordx4 v[52:55], v[38:39], off offset:1024
	global_load_dwordx4 v[56:59], v[38:39], off offset:2048
	global_load_dwordx4 v[60:63], v[38:39], off offset:3072
	v_mov_b32_e32 v65, v80
	v_mov_b32_e32 v66, v80
	s_add_i32 s6, s6, s8
	v_lshlrev_b32_e32 v38, 2, v65
	v_lshlrev_b32_e32 v39, 2, v66
	v_xor_b32_e32 v65, 4, v38
	v_xor_b32_e32 v78, 8, v38
	v_xor_b32_e32 v79, 16, v38
	v_xor_b32_e32 v81, 32, v38
	v_xor_b32_e32 v82, 64, v38
	v_xor_b32_e32 v83, 0x80, v38
	v_xor_b32_e32 v84, 4, v39
	v_xor_b32_e32 v85, 8, v39
	v_xor_b32_e32 v86, 16, v39
	v_xor_b32_e32 v87, 32, v39
	v_xor_b32_e32 v88, 64, v39
	v_xor_b32_e32 v89, 0x80, v39
	v_lshl_add_u64 v[32:33], v[32:33], 0, s[2:3]
	v_lshl_add_u64 v[34:35], v[34:35], 0, s[4:5]
	s_cmpk_gt_i32 s6, 0x3fff
	v_lshl_add_u64 v[36:37], v[36:37], 0, s[10:11]
	s_waitcnt vmcnt(3)
	v_mov_b32_e32 v38, v49
	v_mov_b32_e32 v39, v50
	v_mov_b32_e32 v66, v48
	v_mov_b32_e32 v67, v51
	s_waitcnt vmcnt(2)
	v_mov_b32_e32 v68, v53
	v_mov_b32_e32 v69, v54
	v_mov_b32_e32 v70, v52
	v_mov_b32_e32 v71, v55
	v_pk_add_f32 v[38:39], v[38:39], v[66:67]
	v_pk_add_f32 v[66:67], v[68:69], v[70:71]
	v_add_f32_e32 v70, v38, v39
	v_pk_add_f32 v[38:39], v[66:67], v[66:67] op_sel:[0,1] op_sel_hi:[1,0]
	s_waitcnt vmcnt(1)
	v_add_f32_e32 v72, v56, v57
	v_add_f32_e32 v74, v58, v59
	s_waitcnt vmcnt(0)
	v_mov_b32_e32 v77, v60
	v_mov_b32_e32 v73, v62
	v_mov_b32_e32 v75, v63
	v_add_f32_e32 v76, 0, v70
	v_mov_b32_e32 v39, v61
	v_pk_add_f32 v[68:69], v[72:73], v[74:75]
	v_pk_add_f32 v[38:39], v[76:77], v[38:39]
	s_nop 0
	v_pk_add_f32 v[38:39], v[38:39], v[68:69]
	s_nop 0
	v_add_f32_e32 v38, v38, v39
	s_nop 1
	v_add_f32_dpp v38, v38, v38 quad_perm:[1,0,3,2] row_mask:0xf bank_mask:0xf
	s_nop 1
	v_add_f32_dpp v38, v38, v38 quad_perm:[2,3,0,1] row_mask:0xf bank_mask:0xf
	s_nop 1
	v_add_f32_dpp v38, v38, v38 row_half_mirror row_mask:0xf bank_mask:0xf
	s_nop 1
	v_add_f32_dpp v38, v38, v38 row_mirror row_mask:0xf bank_mask:0xf
	v_mov_b32_e32 v39, v38
	v_mov_b32_e32 v83, v38
	s_nop 1
	v_permlane16_swap_b32 v39, v83
	v_add_f32_e32 v38, v39, v83
	v_mov_b32_e32 v39, v38
	v_mov_b32_e32 v83, v38
	s_nop 1
	v_permlane32_swap_b32 v39, v83
	v_add_f32_e32 v65, v39, v83
	v_fmamk_f32 v39, v65, 0xba800000, v49
	v_fmamk_f32 v38, v65, 0xba800000, v48
	v_fmamk_f32 v51, v65, 0xba800000, v51
	v_fmac_f32_e32 v50, 0xba800000, v65
	v_fmamk_f32 v49, v65, 0xba800000, v53
	v_fmamk_f32 v48, v65, 0xba800000, v52
	v_fmamk_f32 v55, v65, 0xba800000, v55
	v_fmac_f32_e32 v54, 0xba800000, v65
	v_fmamk_f32 v53, v65, 0xba800000, v57
	v_fmamk_f32 v52, v65, 0xba800000, v56
	v_fmamk_f32 v57, v65, 0xba800000, v63
	v_fmamk_f32 v56, v65, 0xba800000, v62
	v_pk_mul_f32 v[62:63], v[50:51], v[50:51]
	v_pk_mul_f32 v[66:67], v[38:39], v[38:39]
	v_pk_mul_f32 v[68:69], v[54:55], v[54:55]
	v_pk_mul_f32 v[70:71], v[48:49], v[48:49]
	v_fmac_f32_e32 v58, 0xba800000, v65
	v_pk_mov_b32 v[76:77], v[66:67], v[62:63] op_sel:[1,0]
	v_mov_b32_e32 v67, v63
	v_pk_mov_b32 v[62:63], v[70:71], v[68:69] op_sel:[1,0]
	v_mov_b32_e32 v71, v69
	v_fmamk_f32 v59, v65, 0xba800000, v59
	v_mul_f32_e32 v72, v52, v52
	v_mul_f32_e32 v74, v58, v58
	v_pk_add_f32 v[66:67], v[76:77], v[66:67]
	v_pk_add_f32 v[62:63], v[62:63], v[70:71]
	v_fmamk_f32 v61, v65, 0xba800000, v61
	v_fmac_f32_e32 v60, 0xba800000, v65
	v_pk_fma_f32 v[68:69], v[52:53], v[52:53], v[72:73] op_sel_hi:[1,1,0]
	v_pk_fma_f32 v[72:73], v[58:59], v[58:59], v[74:75] op_sel_hi:[1,1,0]
	v_pk_add_f32 v[66:67], v[66:67], v[66:67] op_sel_hi:[0,1]
	v_pk_add_f32 v[62:63], v[62:63], v[62:63] op_sel_hi:[0,1]
	v_mul_f32_e32 v68, v60, v60
	v_mul_f32_e32 v72, v61, v61
	v_mul_f32_e32 v66, v56, v56
	v_mul_f32_e32 v62, v57, v57
	v_pk_add_f32 v[68:69], v[68:69], v[72:73]
	v_pk_add_f32 v[62:63], v[66:67], v[62:63]
	s_nop 0
	v_pk_add_f32 v[62:63], v[68:69], v[62:63]
	s_nop 0
	v_add_f32_e32 v62, v62, v63
	ds_bpermute_b32 v63, v84, v62
	s_waitcnt lgkmcnt(0)
	v_add_f32_e32 v62, v62, v63
	ds_bpermute_b32 v63, v85, v62
	s_waitcnt lgkmcnt(0)
	v_add_f32_e32 v62, v62, v63
	ds_bpermute_b32 v63, v86, v62
	s_waitcnt lgkmcnt(0)
	v_add_f32_e32 v62, v62, v63
	ds_bpermute_b32 v63, v87, v62
	s_waitcnt lgkmcnt(0)
	v_add_f32_e32 v62, v62, v63
	ds_bpermute_b32 v63, v88, v62
	s_waitcnt lgkmcnt(0)
	v_add_f32_e32 v62, v62, v63
	ds_bpermute_b32 v63, v89, v62
	s_waitcnt lgkmcnt(0)
; __device__ __forceinline__ unsigned pk2(float lo, float hi) { return f2bf(lo) | (f2bf(hi) << 16); }
; __device__ __forceinline__ unsigned q8x4(float a, float b, float c, float d, float s) { return q8_(a, s) | (q8_(b, s) << 8) | (q8_(c, s) << 16) | (q8_(d, s) << 24); }
; __device__ __forceinline__ void ln_rows_pre(f32x4 (&v)[4], const LnAff& a) {
;     ...
;     const float rstd = 1.f / sqrtf(wave_sum(s2) * (1.f / D) + LN_EPS);
; #pragma unroll
;     for (int j = 0; j < 4; ++j) v[j] = v[j] * rstd * a.g[j] + a.b[j];
; }
; __device__ __forceinline__ void store_row_f32_bf16(const f32x4 (&v)[4], float* of, bf16* ob, int lane) {
; #pragma unroll
;     for (int j = 0; j < 4; ++j) { if (of) *(f32x4*)(of + 4 * lane + 256 * j) = v[j];
;         if (ob) { v2u w; w.x = pk2(v[j][0], v[j][1]); w.y = pk2(v[j][2], v[j][3]); *(v2u*)(ob + 4 * lane + 256 * j) = w; } }
; __device__ __forceinline__ void store_row_fp8(const f32x4 (&v)[4], unsigned char* o8, int lane) {
; #pragma unroll
;     for (int j = 0; j < 4; ++j) *(unsigned*)(o8 + 4 * lane + 256 * j) = q8x4(v[j][0], v[j][1], v[j][2], v[j][3], QS_H);
; }
	v_add_f32_e32 v62, v62, v63
	v_fmamk_f32 v62, v62, 0x3a800000, v45
	v_mul_f32_e32 v63, 0x4f800000, v62
	v_cmp_gt_f32_e32 vcc, s7, v62
	s_nop 1
	v_cndmask_b32_e32 v62, v62, v63, vcc
	v_sqrt_f32_e32 v63, v62
	s_nop 0
	v_add_u32_e32 v65, -1, v63
	v_add_u32_e32 v66, 1, v63
	v_fma_f32 v67, -v65, v63, v62
	v_fma_f32 v68, -v66, v63, v62
	v_cmp_ge_f32_e64 s[0:1], 0, v67
	s_nop 1
	v_cndmask_b32_e64 v63, v63, v65, s[0:1]
	v_cmp_lt_f32_e64 s[0:1], 0, v68
	s_nop 1
	v_cndmask_b32_e64 v63, v63, v66, s[0:1]
	v_mul_f32_e32 v65, 0x37800000, v63
	v_cndmask_b32_e32 v63, v63, v65, vcc
	v_cmp_class_f32_e32 vcc, v62, v46
	s_nop 1
	v_cndmask_b32_e32 v62, v63, v62, vcc
	v_div_scale_f32 v63, s[0:1], v62, v62, 1.0
	v_rcp_f32_e32 v66, v63
	v_div_scale_f32 v65, vcc, 1.0, v62, 1.0
	v_fma_f32 v67, -v63, v66, 1.0
	v_fmac_f32_e32 v66, v67, v66
	v_mul_f32_e32 v67, v65, v66
	v_fma_f32 v68, -v63, v67, v65
	v_fmac_f32_e32 v67, v68, v66
	v_fma_f32 v63, -v63, v67, v65
	v_div_fmas_f32 v63, v63, v66, v67
	v_div_fixup_f32 v62, v63, v62, 1.0
	v_pk_mul_f32 v[38:39], v[38:39], v[62:63] op_sel_hi:[1,0]
	v_pk_mul_f32 v[48:49], v[48:49], v[62:63] op_sel_hi:[1,0]
	v_pk_mul_f32 v[54:55], v[54:55], v[62:63] op_sel_hi:[1,0]
	v_pk_mul_f32 v[50:51], v[50:51], v[62:63] op_sel_hi:[1,0]
	v_pk_mul_f32 v[52:53], v[52:53], v[62:63] op_sel_hi:[1,0]
	v_pk_mul_f32 v[58:59], v[58:59], v[62:63] op_sel_hi:[1,0]
	v_pk_mul_f32 v[60:61], v[60:61], v[62:63] op_sel_hi:[1,0]
	v_pk_mul_f32 v[56:57], v[56:57], v[62:63] op_sel_hi:[1,0]
	v_pk_fma_f32 v[38:39], v[0:1], v[38:39], v[8:9]
	v_pk_fma_f32 v[54:55], v[6:7], v[54:55], v[14:15]
	v_pk_fma_f32 v[48:49], v[4:5], v[48:49], v[12:13]
	v_pk_fma_f32 v[50:51], v[2:3], v[50:51], v[10:11]
	v_pk_fma_f32 v[58:59], v[18:19], v[58:59], v[26:27]
	v_pk_fma_f32 v[52:53], v[16:17], v[52:53], v[24:25]
	v_pk_fma_f32 v[56:57], v[22:23], v[56:57], v[30:31]
	v_pk_fma_f32 v[60:61], v[20:21], v[60:61], v[28:29]
	v_bfe_u32 v63, v39, 16, 1
	v_bfe_u32 v67, v48, 16, 1
	v_bfe_u32 v69, v54, 16, 1
	v_mul_f32_e32 v81, 0x41cb3333, v39
	v_bfe_u32 v62, v38, 16, 1
	v_bfe_u32 v65, v50, 16, 1
	v_bfe_u32 v66, v51, 16, 1
	v_bfe_u32 v68, v49, 16, 1
	v_bfe_u32 v70, v55, 16, 1
	v_bfe_u32 v71, v52, 16, 1
	v_bfe_u32 v72, v53, 16, 1
	v_bfe_u32 v73, v58, 16, 1
	v_bfe_u32 v76, v61, 16, 1
	v_bfe_u32 v77, v56, 16, 1
	v_mul_f32_e32 v79, 0x41cb3333, v38
	v_mul_f32_e32 v82, 0x41cb3333, v50
	v_mul_f32_e32 v83, 0x41cb3333, v51
	v_mul_f32_e32 v84, 0x41cb3333, v48
	v_mul_f32_e32 v85, 0x41cb3333, v49
	v_mul_f32_e32 v86, 0x41cb3333, v54
	v_mul_f32_e32 v89, 0x41cb3333, v53
	v_mul_f32_e32 v93, 0x41cb3333, v61
	v_add3_u32 v39, v39, v63, s9
	v_add3_u32 v48, v48, v67, s9
	v_add3_u32 v54, v54, v69, s9
	v_med3_f32 v63, v81, s14, v47
	v_bfe_u32 v74, v59, 16, 1
	v_bfe_u32 v75, v60, 16, 1
	v_bfe_u32 v78, v57, 16, 1
	v_mul_f32_e32 v87, 0x41cb3333, v55
	v_mul_f32_e32 v88, 0x41cb3333, v52
	v_mul_f32_e32 v90, 0x41cb3333, v58
	v_mul_f32_e32 v91, 0x41cb3333, v59
	v_mul_f32_e32 v92, 0x41cb3333, v60
	v_mul_f32_e32 v94, 0x41cb3333, v56
	v_mul_f32_e32 v95, 0x41cb3333, v57
	v_add3_u32 v38, v38, v62, s9
	v_add3_u32 v50, v50, v65, s9
	v_add3_u32 v51, v51, v66, s9
	v_add3_u32 v49, v49, v68, s9
	v_add3_u32 v55, v55, v70, s9
	v_add3_u32 v52, v52, v71, s9
	v_add3_u32 v53, v53, v72, s9
	v_add3_u32 v58, v58, v73, s9
	v_add3_u32 v61, v61, v76, s9
	v_add3_u32 v56, v56, v77, s9
	v_med3_f32 v62, v79, s14, v47
	v_med3_f32 v65, v82, s14, v47
	v_med3_f32 v66, v83, s14, v47
	v_med3_f32 v68, v85, s14, v47
	v_med3_f32 v72, v89, s14, v47
	v_med3_f32 v76, v93, s14, v47
	v_lshrrev_b32_e32 v48, 16, v48
	v_lshrrev_b32_e32 v54, 16, v54
	v_rndne_f32_e32 v63, v63
	v_add3_u32 v59, v59, v74, s9
	v_add3_u32 v60, v60, v75, s9
	v_add3_u32 v57, v57, v78, s9
	v_med3_f32 v67, v84, s14, v47
	v_med3_f32 v69, v86, s14, v47
	v_med3_f32 v70, v87, s14, v47
	v_med3_f32 v71, v88, s14, v47
	v_med3_f32 v73, v90, s14, v47
	v_med3_f32 v74, v91, s14, v47
	v_med3_f32 v75, v92, s14, v47
	v_med3_f32 v77, v94, s14, v47
	v_med3_f32 v78, v95, s14, v47
	v_lshrrev_b32_e32 v38, 16, v38
	v_lshrrev_b32_e32 v50, 16, v50
	v_lshrrev_b32_e32 v52, 16, v52
	v_lshrrev_b32_e32 v58, 16, v58
	v_lshrrev_b32_e32 v56, 16, v56
	v_rndne_f32_e32 v62, v62
	v_rndne_f32_e32 v65, v65
	v_rndne_f32_e32 v66, v66
	v_rndne_f32_e32 v68, v68
	v_rndne_f32_e32 v72, v72
	v_rndne_f32_e32 v76, v76
	v_and_or_b32 v48, v49, s12, v48
	v_and_or_b32 v49, v55, s12, v54
	v_cvt_i32_f32_e32 v55, v63
	v_lshrrev_b32_e32 v60, 16, v60
	v_rndne_f32_e32 v67, v67
	v_rndne_f32_e32 v69, v69
	v_rndne_f32_e32 v70, v70
	v_rndne_f32_e32 v71, v71
	v_rndne_f32_e32 v73, v73
	v_rndne_f32_e32 v74, v74
	v_rndne_f32_e32 v75, v75
	v_rndne_f32_e32 v77, v77
	v_rndne_f32_e32 v78, v78
	v_and_or_b32 v38, v39, s12, v38
	v_and_or_b32 v39, v51, s12, v50
	v_and_or_b32 v50, v53, s12, v52
	v_and_or_b32 v51, v59, s12, v58
	v_and_or_b32 v53, v57, s12, v56
	v_cvt_i32_f32_e32 v54, v62
	v_cvt_i32_f32_sdwa v56, v65 dst_sel:WORD_1 dst_unused:UNUSED_PAD src0_sel:DWORD
	v_cvt_i32_f32_e32 v57, v66
	v_cvt_i32_f32_e32 v59, v68
	v_cvt_i32_f32_e32 v63, v72
	v_cvt_i32_f32_e32 v68, v76
	v_and_or_b32 v52, v61, s12, v60
	v_cvt_i32_f32_e32 v58, v67
	v_cvt_i32_f32_sdwa v60, v69 dst_sel:WORD_1 dst_unused:UNUSED_PAD src0_sel:DWORD
	v_cvt_i32_f32_e32 v61, v70
	v_cvt_i32_f32_e32 v62, v71
	v_cvt_i32_f32_sdwa v65, v73 dst_sel:WORD_1 dst_unused:UNUSED_PAD src0_sel:DWORD
	v_cvt_i32_f32_e32 v66, v74
	v_cvt_i32_f32_e32 v67, v75
	v_cvt_i32_f32_sdwa v69, v77 dst_sel:WORD_1 dst_unused:UNUSED_PAD src0_sel:DWORD
	v_cvt_i32_f32_e32 v70, v78
	global_store_dwordx2 v[42:43], v[38:39], off
	global_store_dwordx2 v[42:43], v[48:49], off offset:512
	global_store_dwordx2 v[42:43], v[50:51], off offset:1024
	global_store_dwordx2 v[42:43], v[52:53], off offset:1536
	v_lshlrev_b32_e32 v38, 8, v55
	v_and_b32_e32 v39, 0xff0000, v56
	v_perm_b32 v42, v57, v54, s15
	v_lshlrev_b32_e32 v43, 8, v59
	v_lshlrev_b32_e32 v50, 8, v63
	v_lshlrev_b32_e32 v53, 8, v68
	v_and_b32_e32 v38, 0xff00, v38
	v_and_b32_e32 v48, 0xff0000, v60
	v_perm_b32 v49, v61, v58, s15
	v_and_b32_e32 v51, 0xff0000, v65
	v_perm_b32 v52, v66, v62, s15
	v_and_b32_e32 v54, 0xff0000, v69
	v_perm_b32 v55, v70, v67, s15
	v_and_b32_e32 v43, 0xff00, v43
	v_and_b32_e32 v50, 0xff00, v50
	v_and_b32_e32 v53, 0xff00, v53
	v_or3_b32 v38, v42, v38, v39
	v_or3_b32 v39, v49, v43, v48
	v_or3_b32 v42, v52, v50, v51
	v_or3_b32 v43, v55, v53, v54
	global_store_dword v[40:41], v38, off
	global_store_dword v[40:41], v39, off offset:256
	global_store_dword v[40:41], v42, off offset:512
	global_store_dword v[40:41], v43, off offset:768
	s_cbranch_scc0 .LBB0_250

; __global__ void __launch_bounds__(NWAVES * 64, 2) fwd(Args args) {
;     ...
;               for (int mb = gw2_; mb < M; mb += 4 * ngw2_) {
;                 unsigned cw2[4], kx[4]; v4u uu[4][3], gc[4][3], gb[4];
; #pragma unroll
;                 for (int q = 0; q < 4; ++q) { int m = mb + q * ngw2_; m = m < M ? m : mb; const bf16* pr = PROJ + (size_t)m * NP; const int tl = m & (T - 1);
;                     cw2[q] = *(const unsigned*)(pr + PC_CKV + 2 * lane); kx[q] = *(const unsigned*)(pr + PC_KIDX + 2 * (lane & 15)); gb[q] = *(const v4u*)(pr + PC_GB + 8 * lane);
; #pragma unroll
;                     for (int k = 0; k < 3; ++k) { const int back = 2 - k; const bf16* pp = pr - (size_t)(tl >= back ? back : 0) * NP;
;                         uu[q][k] = *(const v4u*)(pp + PC_CU + 8 * lane); gc[q][k] = *(const v4u*)(pp + PC_GC + 8 * lane); } }
.LBB0_544:
	s_add_i32 s6, s28, s29
	s_and_b32 s22, s6, 0x1fff
	s_cmp_gt_u32 s22, 1
	s_cselect_b64 s[24:25], -1, 0
	s_cmp_lt_u32 s22, 2
	s_cselect_b32 s2, 0, 0xffff8000
	s_cselect_b32 s3, 0, -1
	s_add_u32 s2, s8, s2
	v_lshl_add_u64 v[0:1], s[8:9], 0, v[150:151]
	s_addc_u32 s3, s9, s3
	global_load_dword v112, v[0:1], off
	v_lshl_add_u64 v[0:1], s[8:9], 0, v[148:149]
	s_cmp_lg_u32 s22, 0
	v_add_co_u32_e32 v2, vcc, 0x3ce01000, v0
	s_cselect_b64 s[20:21], -1, 0
	s_cmp_eq_u32 s22, 0
	v_addc_co_u32_e32 v3, vcc, 0, v1, vcc
	v_lshl_add_u64 v[4:5], s[2:3], 0, v[148:149]
	s_cselect_b32 s2, 0, 0xffffc000
	v_add_co_u32_e32 v6, vcc, s37, v4
	s_cselect_b32 s3, 0, -1
	s_add_u32 s2, s8, s2
	v_addc_co_u32_e32 v7, vcc, 0, v5, vcc
	s_addc_u32 s3, s9, s3
	s_add_i32 s76, s28, s31
	v_add_co_u32_e32 v4, vcc, s35, v4
	s_cmpk_lt_i32 s76, 0x4000
	s_nop 0
	v_addc_co_u32_e32 v5, vcc, 0, v5, vcc
	s_cselect_b64 s[78:79], -1, 0
	global_load_dwordx4 v[84:87], v[2:3], off
	global_load_dwordx4 v[104:107], v[4:5], off offset:1024
	v_lshl_add_u64 v[4:5], s[2:3], 0, v[148:149]
	s_and_b64 s[2:3], s[78:79], exec
	s_cselect_b32 s2, s76, s6
	global_load_dwordx4 v[108:111], v[6:7], off offset:3072
	v_add_co_u32_e32 v6, vcc, s37, v4
	s_ashr_i32 s3, s2, 31
	s_nop 0
	v_addc_co_u32_e32 v7, vcc, 0, v5, vcc
	s_lshl_b64 s[26:27], s[2:3], 14
	v_add_co_u32_e32 v4, vcc, s35, v4
	s_add_u32 s26, s4, s26
	s_nop 0
	v_addc_co_u32_e32 v5, vcc, 0, v5, vcc
	s_addc_u32 s27, s5, s27
	s_and_b32 s22, s2, 0x1fff
	v_add_co_u32_e32 v0, vcc, s37, v0
	s_cmp_lt_u32 s22, 2
	s_nop 0
	v_addc_co_u32_e32 v1, vcc, 0, v1, vcc
	v_mov_b32_e32 v153, v128
	s_cselect_b32 s2, 0, 0xffff8000
	global_load_dwordx4 v[100:103], v[6:7], off offset:3072
	global_load_dwordx4 v[96:99], v[4:5], off offset:1024
	global_load_dwordx4 v[92:95], v[0:1], off offset:3072
	global_load_dwordx4 v[88:91], v[2:3], off offset:1024
	v_lshl_add_u64 v[0:1], s[26:27], 0, v[152:153]
	s_cselect_b32 s3, 0, -1
	s_add_u32 s2, s26, s2
	v_add_co_u32_e32 v0, vcc, s34, v0
	s_addc_u32 s3, s27, s3
	s_nop 0
	v_addc_co_u32_e32 v1, vcc, 0, v1, vcc
	s_cmp_eq_u32 s22, 0
	global_load_dword v160, v123, s[26:27] offset:2048
	global_load_dword v159, v154, s[26:27] offset:2304
	global_load_dwordx4 v[56:59], v[0:1], off
	global_load_dwordx4 v[80:83], v152, s[2:3] offset:3072
	v_lshl_add_u64 v[2:3], s[2:3], 0, v[152:153]
	s_cselect_b32 s2, 0, 0xffffc000
	v_add_co_u32_e32 v2, vcc, s34, v2
	s_cselect_b32 s3, 0, -1
	s_add_u32 s2, s26, s2
	v_addc_co_u32_e32 v3, vcc, 0, v3, vcc
	s_addc_u32 s3, s27, s3
	global_load_dwordx4 v[76:79], v[2:3], off offset:1024
	global_load_dwordx4 v[68:71], v152, s[2:3] offset:3072
	v_lshl_add_u64 v[2:3], s[2:3], 0, v[152:153]
	v_add_co_u32_e32 v2, vcc, s34, v2
	s_add_i32 s70, s28, s11
	s_nop 0
	v_addc_co_u32_e32 v3, vcc, 0, v3, vcc
	global_load_dwordx4 v[72:75], v[2:3], off offset:1024
	global_load_dwordx4 v[64:67], v152, s[26:27] offset:3072
	global_load_dwordx4 v[60:63], v[0:1], off offset:1024
	v_lshl_add_u64 v[0:1], s[8:9], 0, v[146:147]
	global_load_dword v113, v[0:1], off
	s_cmpk_lt_i32 s70, 0x4000
	s_cselect_b64 s[74:75], -1, 0
	s_and_b64 s[2:3], s[74:75], exec
	s_cselect_b32 s26, s70, s6
	s_ashr_i32 s27, s26, 31
	s_lshl_b64 s[2:3], s[26:27], 14
	s_add_u32 s2, s4, s2
	s_addc_u32 s3, s5, s3
	s_and_b32 s22, s26, 0x1fff
	s_cmp_lt_u32 s22, 2
	s_cselect_b32 s26, 0, 0xffff8000
	v_lshl_add_u64 v[0:1], s[2:3], 0, v[152:153]
	s_cselect_b32 s27, 0, -1
	s_add_u32 s26, s2, s26
	v_add_co_u32_e32 v0, vcc, s34, v0
	s_addc_u32 s27, s3, s27
	s_nop 0
	v_addc_co_u32_e32 v1, vcc, 0, v1, vcc
	s_cmp_eq_u32 s22, 0
	global_load_dword v158, v123, s[2:3] offset:2048
	global_load_dword v157, v154, s[2:3] offset:2304
	global_load_dwordx4 v[28:31], v[0:1], off
	global_load_dwordx4 v[52:55], v152, s[26:27] offset:3072
	v_lshl_add_u64 v[2:3], s[26:27], 0, v[152:153]
	s_cselect_b32 s26, 0, 0xffffc000
	v_add_co_u32_e32 v2, vcc, s34, v2
	s_cselect_b32 s22, 0, -1
	s_add_u32 s26, s2, s26
	v_addc_co_u32_e32 v3, vcc, 0, v3, vcc
	s_addc_u32 s27, s3, s22
	global_load_dwordx4 v[48:51], v[2:3], off offset:1024
	global_load_dwordx4 v[44:47], v152, s[26:27] offset:3072
	v_lshl_add_u64 v[2:3], s[26:27], 0, v[152:153]
	s_add_i32 s68, s28, s30
	v_add_co_u32_e32 v2, vcc, s34, v2
	s_cmpk_lt_i32 s68, 0x4000
	s_nop 0
	v_addc_co_u32_e32 v3, vcc, 0, v3, vcc
	s_cselect_b64 s[72:73], -1, 0
	global_load_dwordx4 v[40:43], v[2:3], off offset:1024
	global_load_dwordx4 v[36:39], v152, s[2:3] offset:3072
	global_load_dwordx4 v[32:35], v[0:1], off offset:1024
	s_and_b64 s[2:3], s[72:73], exec
	s_cselect_b32 s2, s68, s6
	s_ashr_i32 s3, s2, 31
	s_lshl_b64 s[26:27], s[2:3], 14
	s_add_u32 s26, s4, s26
	s_addc_u32 s27, s5, s27
	s_and_b32 s6, s2, 0x1fff
	s_cmp_lt_u32 s6, 2
	s_cselect_b32 s2, 0, 0xffff8000
	v_lshl_add_u64 v[0:1], s[26:27], 0, v[152:153]
	s_cselect_b32 s3, 0, -1
	s_add_u32 s2, s26, s2
	v_add_co_u32_e32 v4, vcc, s34, v0
	s_addc_u32 s3, s27, s3
	s_nop 0
	v_addc_co_u32_e32 v5, vcc, 0, v1, vcc
	s_cmp_eq_u32 s6, 0
	global_load_dword v156, v123, s[26:27] offset:2048
	global_load_dword v155, v154, s[26:27] offset:2304
	global_load_dwordx4 v[0:3], v[4:5], off
	global_load_dwordx4 v[24:27], v152, s[2:3] offset:3072
	v_lshl_add_u64 v[6:7], s[2:3], 0, v[152:153]
	s_cselect_b32 s2, 0, 0xffffc000
	v_add_co_u32_e32 v6, vcc, s34, v6
	s_cselect_b32 s3, 0, -1
	s_add_u32 s2, s26, s2
	v_addc_co_u32_e32 v7, vcc, 0, v7, vcc
	s_addc_u32 s3, s27, s3
	global_load_dwordx4 v[20:23], v[6:7], off offset:1024
	global_load_dwordx4 v[16:19], v152, s[2:3] offset:3072
	v_lshl_add_u64 v[6:7], s[2:3], 0, v[152:153]
	v_add_co_u32_e32 v6, vcc, s34, v6
	s_waitcnt vmcnt(0)
; __device__ __forceinline__ unsigned pk2(float lo, float hi) { return f2bf(lo) | (f2bf(hi) << 16); }
; __device__ __forceinline__ int lane_op() { int l = (int)__builtin_amdgcn_mbcnt_hi(~0u, __builtin_amdgcn_mbcnt_lo(~0u, 0u)); asm volatile("" : "+v"(l)); return l; }
; #define SHX(v, m, l) bperm_((l) ^ (m), (v))
; __device__ __forceinline__ float wave_sum(float v) { const int l = lane_op();
; #pragma unroll
;     for (int o = 1; o < 64; o <<= 1) v += SHX(v, o, l);
;     return v;
; __global__ void __launch_bounds__(NWAVES * 64, 2) fwd(Args args) {
;     ...
;                 for (int q = 0; q < 4; ++q) { const int m = mb + q * ngw2_; if (m < M) { const int tl = m & (T - 1);
;                     const float c0 = bflo(cw2[q]), c1 = bfhi(cw2[q]);
;                     const float rs = 1.f / sqrtf(wave_sum(c0 * c0 + c1 * c1) * (1.f / 128.f) + LN_EPS);
;                     *(unsigned*)(KVN + (size_t)m * 128 + 2 * lane) = pk2(c0 * rs * kg0, c1 * rs * kg1);
;                     if (lane < 16) *(unsigned*)(KIDX + (size_t)m * 32 + 2 * lane) = kx[q];
	v_lshlrev_b32_e32 v114, 16, v113
	v_addc_co_u32_e32 v7, vcc, 0, v7, vcc
	global_load_dwordx4 v[12:15], v[6:7], off offset:1024
	global_load_dwordx4 v[8:11], v152, s[26:27] offset:3072
	s_nop 0
	global_load_dwordx4 v[4:7], v[4:5], off offset:1024
	v_and_b32_e32 v115, 0xffff0000, v113
	v_mov_b32_e32 v113, v251
	v_pk_mul_f32 v[116:117], v[114:115], v[114:115]
	v_lshlrev_b32_e32 v113, 2, v113
	v_xor_b32_e32 v118, 4, v113
	v_add_f32_e32 v116, v116, v117
	v_xor_b32_e32 v118, 8, v113
	v_xor_b32_e32 v118, 16, v113
	v_xor_b32_e32 v118, 32, v113
	v_xor_b32_e32 v118, 64, v113
	v_xor_b32_e32 v113, 0x80, v113
	s_nop 1
	v_add_f32_dpp v116, v116, v116 quad_perm:[1,0,3,2] row_mask:0xf bank_mask:0xf
	s_nop 1
	v_add_f32_dpp v116, v116, v116 quad_perm:[2,3,0,1] row_mask:0xf bank_mask:0xf
	s_nop 1
	v_add_f32_dpp v116, v116, v116 row_half_mirror row_mask:0xf bank_mask:0xf
	s_nop 1
	v_add_f32_dpp v116, v116, v116 row_mirror row_mask:0xf bank_mask:0xf
	v_mov_b32_e32 v113, v116
	v_mov_b32_e32 v117, v116
	s_nop 1
	v_permlane16_swap_b32 v113, v117
	v_add_f32_e32 v116, v113, v117
	v_mov_b32_e32 v113, v116
	v_mov_b32_e32 v117, v116
	s_nop 1
	v_permlane32_swap_b32 v113, v117
	v_add_f32_e32 v113, v113, v117
	v_fmamk_f32 v113, v113, 0x3c000000, v249
	v_cmp_gt_f32_e32 vcc, s52, v113
	v_mul_f32_e32 v116, 0x4f800000, v113
	s_nop 0
	v_cndmask_b32_e32 v113, v113, v116, vcc
	v_sqrt_f32_e32 v116, v113
	s_nop 0
	v_add_u32_e32 v117, -1, v116
	v_fma_f32 v118, -v117, v116, v113
	v_cmp_ge_f32_e64 s[2:3], 0, v118
	v_add_u32_e32 v118, 1, v116
	s_nop 0
	v_cndmask_b32_e64 v117, v116, v117, s[2:3]
	v_fma_f32 v116, -v118, v116, v113
	v_cmp_lt_f32_e64 s[2:3], 0, v116
	s_nop 1
	v_cndmask_b32_e64 v116, v117, v118, s[2:3]
	v_mul_f32_e32 v117, 0x37800000, v116
	v_cndmask_b32_e32 v116, v116, v117, vcc
	v_cmp_class_f32_e32 vcc, v113, v250
	s_nop 1
	v_cndmask_b32_e32 v113, v116, v113, vcc
	v_div_scale_f32 v116, s[2:3], v113, v113, 1.0
	v_rcp_f32_e32 v117, v116
	s_nop 0
	v_fma_f32 v118, -v116, v117, 1.0
	v_fmac_f32_e32 v117, v118, v117
	v_div_scale_f32 v118, vcc, 1.0, v113, 1.0
	v_mul_f32_e32 v119, v118, v117
	v_fma_f32 v153, -v116, v119, v118
	v_fmac_f32_e32 v119, v153, v117
	v_fma_f32 v116, -v116, v119, v118
	v_div_fmas_f32 v116, v116, v117, v119
	v_div_fixup_f32 v116, v116, v113, 1.0
	v_pk_mul_f32 v[114:115], v[116:117], v[114:115] op_sel_hi:[0,1]
	v_pk_mul_f32 v[114:115], v[124:125], v[114:115]
	s_nop 0
	v_and_b32_sdwa v116, v114, v248 dst_sel:DWORD dst_unused:UNUSED_PAD src0_sel:WORD_1 src1_sel:DWORD
	v_and_b32_sdwa v113, v115, v248 dst_sel:DWORD dst_unused:UNUSED_PAD src0_sel:WORD_1 src1_sel:DWORD
	v_add3_u32 v114, v114, v116, s55
	v_add3_u32 v113, v115, v113, s55
	v_lshrrev_b32_e32 v114, 16, v114
	v_and_or_b32 v113, v113, s53, v114
	v_lshl_add_u64 v[114:115], s[8:9], 0, v[140:141]
	global_store_dword v[114:115], v113, off
	s_and_saveexec_b64 s[2:3], s[0:1]
	s_cbranch_execz .LBB0_546
	v_lshl_add_u64 v[114:115], s[8:9], 0, v[142:143]
	global_store_dword v[114:115], v112, off

; __device__ __forceinline__ unsigned pk2(float lo, float hi) { return f2bf(lo) | (f2bf(hi) << 16); }
; __device__ __forceinline__ int lane_op() { int l = (int)__builtin_amdgcn_mbcnt_hi(~0u, __builtin_amdgcn_mbcnt_lo(~0u, 0u)); asm volatile("" : "+v"(l)); return l; }
; #define SHX(v, m, l) bperm_((l) ^ (m), (v))
; __device__ __forceinline__ float wave_sum(float v) { const int l = lane_op();
; #pragma unroll
;     for (int o = 1; o < 64; o <<= 1) v += SHX(v, o, l);
;     return v;
; __global__ void __launch_bounds__(NWAVES * 64, 2) fwd(Args args) {
;     ...
;                 for (int q = 0; q < 4; ++q) { const int m = mb + q * ngw2_; if (m < M) { const int tl = m & (T - 1);
;                     const float c0 = bflo(cw2[q]), c1 = bfhi(cw2[q]);
;                     const float rs = 1.f / sqrtf(wave_sum(c0 * c0 + c1 * c1) * (1.f / 128.f) + LN_EPS);
;                     *(unsigned*)(KVN + (size_t)m * 128 + 2 * lane) = pk2(c0 * rs * kg0, c1 * rs * kg1);
;                     if (lane < 16) *(unsigned*)(KIDX + (size_t)m * 32 + 2 * lane) = kx[q];
.LBB0_553:
	s_nop 0
	v_mov_b32_e32 v86, v251
	v_lshlrev_b32_e32 v84, 16, v160
	v_and_b32_e32 v85, 0xffff0000, v160
	v_lshlrev_b32_e32 v86, 2, v86
	v_xor_b32_e32 v88, 4, v86
	v_xor_b32_e32 v89, 8, v86
	v_xor_b32_e32 v90, 16, v86
	v_xor_b32_e32 v91, 32, v86
	v_xor_b32_e32 v92, 64, v86
	v_xor_b32_e32 v93, 0x80, v86
	v_pk_mul_f32 v[86:87], v[84:85], v[84:85]
	s_ashr_i32 s77, s76, 31
	v_add_f32_e32 v86, v86, v87
	s_nop 1
	v_add_f32_dpp v86, v86, v86 quad_perm:[1,0,3,2] row_mask:0xf bank_mask:0xf
	s_nop 1
	v_add_f32_dpp v86, v86, v86 quad_perm:[2,3,0,1] row_mask:0xf bank_mask:0xf
	s_nop 1
	v_add_f32_dpp v86, v86, v86 row_half_mirror row_mask:0xf bank_mask:0xf
	s_nop 1
	v_add_f32_dpp v86, v86, v86 row_mirror row_mask:0xf bank_mask:0xf
	v_mov_b32_e32 v87, v86
	v_mov_b32_e32 v91, v86
	s_nop 1
	v_permlane16_swap_b32 v87, v91
	v_add_f32_e32 v86, v87, v91
	v_mov_b32_e32 v87, v86
	v_mov_b32_e32 v91, v86
	s_nop 1
	v_permlane32_swap_b32 v87, v91
	v_add_f32_e32 v86, v87, v91
	v_fmamk_f32 v86, v86, 0x3c000000, v249
	v_cmp_gt_f32_e32 vcc, s52, v86
	v_mul_f32_e32 v87, 0x4f800000, v86
	s_nop 0
	v_cndmask_b32_e32 v86, v86, v87, vcc
	v_sqrt_f32_e32 v87, v86
	s_nop 0
	v_add_u32_e32 v88, -1, v87
	v_fma_f32 v89, -v88, v87, v86
	v_cmp_ge_f32_e64 s[2:3], 0, v89
	v_add_u32_e32 v89, 1, v87
	s_nop 0
	v_cndmask_b32_e64 v88, v87, v88, s[2:3]
	v_fma_f32 v87, -v89, v87, v86
	v_cmp_lt_f32_e64 s[2:3], 0, v87
	s_nop 1
	v_cndmask_b32_e64 v87, v88, v89, s[2:3]
	v_mul_f32_e32 v88, 0x37800000, v87
	v_cndmask_b32_e32 v87, v87, v88, vcc
	v_cmp_class_f32_e32 vcc, v86, v250
	s_nop 1
	v_cndmask_b32_e32 v86, v87, v86, vcc
	v_div_scale_f32 v87, s[2:3], v86, v86, 1.0
	v_rcp_f32_e32 v88, v87
	s_lshl_b64 s[2:3], s[76:77], 8
	v_fma_f32 v89, -v87, v88, 1.0
	v_fmac_f32_e32 v88, v89, v88
	v_div_scale_f32 v89, vcc, 1.0, v86, 1.0
	v_mul_f32_e32 v90, v89, v88
	v_fma_f32 v91, -v87, v90, v89
	v_fmac_f32_e32 v90, v91, v88
	v_fma_f32 v87, -v87, v90, v89
	v_div_fmas_f32 v87, v87, v88, v90
	v_div_fixup_f32 v86, v87, v86, 1.0
	v_pk_mul_f32 v[84:85], v[86:87], v[84:85] op_sel_hi:[0,1]
	v_pk_mul_f32 v[84:85], v[124:125], v[84:85]
	s_nop 0
	v_and_b32_sdwa v87, v84, v248 dst_sel:DWORD dst_unused:UNUSED_PAD src0_sel:WORD_1 src1_sel:DWORD
	v_and_b32_sdwa v86, v85, v248 dst_sel:DWORD dst_unused:UNUSED_PAD src0_sel:WORD_1 src1_sel:DWORD
	v_add3_u32 v84, v84, v87, s55
	v_add3_u32 v85, v85, v86, s55
	v_lshrrev_b32_e32 v84, 16, v84
	v_and_or_b32 v86, v85, s53, v84
	v_lshl_add_u64 v[84:85], v[126:127], 0, s[2:3]
	global_store_dword v[84:85], v86, off
	s_and_saveexec_b64 s[2:3], s[0:1]
	s_cbranch_execz .LBB0_555
	s_lshl_b64 s[20:21], s[76:77], 6
	v_lshl_add_u64 v[84:85], v[130:131], 0, s[20:21]
	global_store_dword v[84:85], v159, off

; __device__ __forceinline__ unsigned pk2(float lo, float hi) { return f2bf(lo) | (f2bf(hi) << 16); }
; __device__ __forceinline__ int lane_op() { int l = (int)__builtin_amdgcn_mbcnt_hi(~0u, __builtin_amdgcn_mbcnt_lo(~0u, 0u)); asm volatile("" : "+v"(l)); return l; }
; #define SHX(v, m, l) bperm_((l) ^ (m), (v))
; __device__ __forceinline__ float wave_sum(float v) { const int l = lane_op();
; #pragma unroll
;     for (int o = 1; o < 64; o <<= 1) v += SHX(v, o, l);
;     return v;
; __global__ void __launch_bounds__(NWAVES * 64, 2) fwd(Args args) {
;     ...
;                 for (int q = 0; q < 4; ++q) { const int m = mb + q * ngw2_; if (m < M) { const int tl = m & (T - 1);
;                     const float c0 = bflo(cw2[q]), c1 = bfhi(cw2[q]);
;                     const float rs = 1.f / sqrtf(wave_sum(c0 * c0 + c1 * c1) * (1.f / 128.f) + LN_EPS);
;                     *(unsigned*)(KVN + (size_t)m * 128 + 2 * lane) = pk2(c0 * rs * kg0, c1 * rs * kg1);
;                     if (lane < 16) *(unsigned*)(KIDX + (size_t)m * 32 + 2 * lane) = kx[q];
.LBB0_560:
	v_mov_b32_e32 v58, v251
	v_lshlrev_b32_e32 v56, 16, v158
	v_and_b32_e32 v57, 0xffff0000, v158
	v_lshlrev_b32_e32 v58, 2, v58
	v_xor_b32_e32 v60, 4, v58
	v_xor_b32_e32 v61, 8, v58
	v_xor_b32_e32 v62, 16, v58
	v_xor_b32_e32 v63, 32, v58
	v_xor_b32_e32 v64, 64, v58
	v_xor_b32_e32 v65, 0x80, v58
	v_pk_mul_f32 v[58:59], v[56:57], v[56:57]
	s_ashr_i32 s71, s70, 31
	v_add_f32_e32 v58, v58, v59
	s_nop 1
	v_add_f32_dpp v58, v58, v58 quad_perm:[1,0,3,2] row_mask:0xf bank_mask:0xf
	s_nop 1
	v_add_f32_dpp v58, v58, v58 quad_perm:[2,3,0,1] row_mask:0xf bank_mask:0xf
	s_nop 1
	v_add_f32_dpp v58, v58, v58 row_half_mirror row_mask:0xf bank_mask:0xf
	s_nop 1
	v_add_f32_dpp v58, v58, v58 row_mirror row_mask:0xf bank_mask:0xf
	v_mov_b32_e32 v59, v58
	v_mov_b32_e32 v63, v58
	s_nop 1
	v_permlane16_swap_b32 v59, v63
	v_add_f32_e32 v58, v59, v63
	v_mov_b32_e32 v59, v58
	v_mov_b32_e32 v63, v58
	s_nop 1
	v_permlane32_swap_b32 v59, v63
	v_add_f32_e32 v58, v59, v63
	v_fmamk_f32 v58, v58, 0x3c000000, v249
	v_cmp_gt_f32_e32 vcc, s52, v58
	v_mul_f32_e32 v59, 0x4f800000, v58
	s_nop 0
	v_cndmask_b32_e32 v58, v58, v59, vcc
	v_sqrt_f32_e32 v59, v58
	s_nop 0
	v_add_u32_e32 v60, -1, v59
	v_fma_f32 v61, -v60, v59, v58
	v_cmp_ge_f32_e64 s[2:3], 0, v61
	v_add_u32_e32 v61, 1, v59
	s_nop 0
	v_cndmask_b32_e64 v60, v59, v60, s[2:3]
	v_fma_f32 v59, -v61, v59, v58
	v_cmp_lt_f32_e64 s[2:3], 0, v59
	s_nop 1
	v_cndmask_b32_e64 v59, v60, v61, s[2:3]
	v_mul_f32_e32 v60, 0x37800000, v59
	v_cndmask_b32_e32 v59, v59, v60, vcc
	v_cmp_class_f32_e32 vcc, v58, v250
	s_nop 1
	v_cndmask_b32_e32 v58, v59, v58, vcc
	v_div_scale_f32 v59, s[2:3], v58, v58, 1.0
	v_rcp_f32_e32 v60, v59
	s_lshl_b64 s[2:3], s[70:71], 8
	v_fma_f32 v61, -v59, v60, 1.0
	v_fmac_f32_e32 v60, v61, v60
	v_div_scale_f32 v61, vcc, 1.0, v58, 1.0
	v_mul_f32_e32 v62, v61, v60
	v_fma_f32 v63, -v59, v62, v61
	v_fmac_f32_e32 v62, v63, v60
	v_fma_f32 v59, -v59, v62, v61
	v_div_fmas_f32 v59, v59, v60, v62
	v_div_fixup_f32 v58, v59, v58, 1.0
	v_pk_mul_f32 v[56:57], v[58:59], v[56:57] op_sel_hi:[0,1]
	v_pk_mul_f32 v[56:57], v[124:125], v[56:57]
	s_nop 0
	v_and_b32_sdwa v59, v56, v248 dst_sel:DWORD dst_unused:UNUSED_PAD src0_sel:WORD_1 src1_sel:DWORD
	v_and_b32_sdwa v58, v57, v248 dst_sel:DWORD dst_unused:UNUSED_PAD src0_sel:WORD_1 src1_sel:DWORD
	v_add3_u32 v56, v56, v59, s55
	v_add3_u32 v57, v57, v58, s55
	v_lshrrev_b32_e32 v56, 16, v56
	v_and_or_b32 v58, v57, s53, v56
	v_lshl_add_u64 v[56:57], v[126:127], 0, s[2:3]
	global_store_dword v[56:57], v58, off
	s_and_saveexec_b64 s[2:3], s[0:1]
	s_cbranch_execz .LBB0_562
	s_lshl_b64 s[20:21], s[70:71], 6
	v_lshl_add_u64 v[56:57], v[130:131], 0, s[20:21]
	global_store_dword v[56:57], v157, off

; __device__ __forceinline__ unsigned pk2(float lo, float hi) { return f2bf(lo) | (f2bf(hi) << 16); }
; __device__ __forceinline__ int lane_op() { int l = (int)__builtin_amdgcn_mbcnt_hi(~0u, __builtin_amdgcn_mbcnt_lo(~0u, 0u)); asm volatile("" : "+v"(l)); return l; }
; #define SHX(v, m, l) bperm_((l) ^ (m), (v))
; __device__ __forceinline__ float wave_sum(float v) { const int l = lane_op();
; #pragma unroll
;     for (int o = 1; o < 64; o <<= 1) v += SHX(v, o, l);
;     return v;
; __global__ void __launch_bounds__(NWAVES * 64, 2) fwd(Args args) {
;     ...
;                 for (int q = 0; q < 4; ++q) { const int m = mb + q * ngw2_; if (m < M) { const int tl = m & (T - 1);
;                     const float c0 = bflo(cw2[q]), c1 = bfhi(cw2[q]);
;                     const float rs = 1.f / sqrtf(wave_sum(c0 * c0 + c1 * c1) * (1.f / 128.f) + LN_EPS);
;                     *(unsigned*)(KVN + (size_t)m * 128 + 2 * lane) = pk2(c0 * rs * kg0, c1 * rs * kg1);
;                     if (lane < 16) *(unsigned*)(KIDX + (size_t)m * 32 + 2 * lane) = kx[q];
.LBB0_567:
	v_mov_b32_e32 v30, v251
	v_lshlrev_b32_e32 v28, 16, v156
	v_and_b32_e32 v29, 0xffff0000, v156
	s_ashr_i32 s69, s68, 31
	v_lshlrev_b32_e32 v32, 2, v30
	v_pk_mul_f32 v[30:31], v[28:29], v[28:29]
	v_xor_b32_e32 v33, 4, v32
	v_add_f32_e32 v30, v30, v31
	v_xor_b32_e32 v33, 8, v32
	v_xor_b32_e32 v33, 16, v32
	v_xor_b32_e32 v33, 32, v32
	v_xor_b32_e32 v33, 64, v32
	v_xor_b32_e32 v32, 0x80, v32
	s_nop 1
	v_add_f32_dpp v30, v30, v30 quad_perm:[1,0,3,2] row_mask:0xf bank_mask:0xf
	s_nop 1
	v_add_f32_dpp v30, v30, v30 quad_perm:[2,3,0,1] row_mask:0xf bank_mask:0xf
	s_nop 1
	v_add_f32_dpp v30, v30, v30 row_half_mirror row_mask:0xf bank_mask:0xf
	s_nop 1
	v_add_f32_dpp v30, v30, v30 row_mirror row_mask:0xf bank_mask:0xf
	v_mov_b32_e32 v31, v30
	v_mov_b32_e32 v32, v30
	s_nop 1
	v_permlane16_swap_b32 v31, v32
	v_add_f32_e32 v30, v31, v32
	v_mov_b32_e32 v31, v30
	v_mov_b32_e32 v32, v30
	s_nop 1
	v_permlane32_swap_b32 v31, v32
	v_add_f32_e32 v30, v31, v32
	v_fmamk_f32 v30, v30, 0x3c000000, v249
	v_mul_f32_e32 v31, 0x4f800000, v30
	v_cmp_gt_f32_e32 vcc, s52, v30
	s_nop 1
	v_cndmask_b32_e32 v30, v30, v31, vcc
	v_sqrt_f32_e32 v31, v30
	s_nop 0
	v_add_u32_e32 v32, -1, v31
	v_add_u32_e32 v33, 1, v31
	v_fma_f32 v34, -v32, v31, v30
	v_fma_f32 v35, -v33, v31, v30
	v_cmp_ge_f32_e64 s[2:3], 0, v34
	s_nop 1
	v_cndmask_b32_e64 v31, v31, v32, s[2:3]
	v_cmp_lt_f32_e64 s[2:3], 0, v35
	s_nop 1
	v_cndmask_b32_e64 v31, v31, v33, s[2:3]
	v_mul_f32_e32 v32, 0x37800000, v31
	v_cndmask_b32_e32 v31, v31, v32, vcc
	v_cmp_class_f32_e32 vcc, v30, v250
	s_nop 1
	v_cndmask_b32_e32 v30, v31, v30, vcc
	v_div_scale_f32 v31, s[2:3], v30, v30, 1.0
	v_rcp_f32_e32 v32, v31
	v_div_scale_f32 v33, vcc, 1.0, v30, 1.0
	s_lshl_b64 s[2:3], s[68:69], 8
	v_fma_f32 v34, -v31, v32, 1.0
	v_fmac_f32_e32 v32, v34, v32
	v_mul_f32_e32 v34, v33, v32
	v_fma_f32 v35, -v31, v34, v33
	v_fmac_f32_e32 v34, v35, v32
	v_fma_f32 v31, -v31, v34, v33
	v_div_fmas_f32 v31, v31, v32, v34
	v_div_fixup_f32 v30, v31, v30, 1.0
	v_pk_mul_f32 v[28:29], v[30:31], v[28:29] op_sel_hi:[0,1]
	v_pk_mul_f32 v[28:29], v[124:125], v[28:29]
	s_nop 0
	v_and_b32_sdwa v31, v28, v248 dst_sel:DWORD dst_unused:UNUSED_PAD src0_sel:WORD_1 src1_sel:DWORD
	v_and_b32_sdwa v30, v29, v248 dst_sel:DWORD dst_unused:UNUSED_PAD src0_sel:WORD_1 src1_sel:DWORD
	v_add3_u32 v28, v28, v31, s55
	v_add3_u32 v29, v29, v30, s55
	v_lshrrev_b32_e32 v28, 16, v28
	v_and_or_b32 v30, v29, s53, v28
	v_lshl_add_u64 v[28:29], v[126:127], 0, s[2:3]
	global_store_dword v[28:29], v30, off
	s_and_saveexec_b64 s[2:3], s[0:1]
	s_cbranch_execz .LBB0_569
	s_lshl_b64 s[20:21], s[68:69], 6
	v_lshl_add_u64 v[28:29], v[130:131], 0, s[20:21]
	global_store_dword v[28:29], v155, off

; __device__ __forceinline__ void ln_rows_pre(f32x4 (&v)[4], const LnAff& a) {
;     float s = 0.f;
; #pragma unroll
;     for (int j = 0; j < 4; ++j) s += (v[j][0] + v[j][1]) + (v[j][2] + v[j][3]);
;     const float mean = wave_sum(s) * (1.f / D); float s2 = 0.f;
; #pragma unroll
;     for (int j = 0; j < 4; ++j) { v[j] = v[j] - mean; s2 += (v[j][0] * v[j][0] + v[j][1] * v[j][1]) + (v[j][2] * v[j][2] + v[j][3] * v[j][3]); }
;     const float rstd = 1.f / sqrtf(wave_sum(s2) * (1.f / D) + LN_EPS);
; #pragma unroll
;     for (int j = 0; j < 4; ++j) v[j] = v[j] * rstd * a.g[j] + a.b[j];
; }
; __global__ void __launch_bounds__(NWAVES * 64, 2) fwd(Args args) {
;     ...
;                     for (int tk = 0; tk < 2; ++tk) { f32x4 v[4];
; #pragma unroll
;                         for (int j = 0; j < 4; ++j) v[j] = (f32x4){bflo(raw[tk][j].x), bfhi(raw[tk][j].x), bflo(raw[tk][j].y), bfhi(raw[tk][j].y)};
;                         ln_rows_pre(v, aff1); store_row_f32_bf16(v, nullptr, H1 + (size_t)(m0 + tk) * D, lane); store_row_fp8(v, (unsigned char*)H1B + (size_t)(m0 + tk) * D, lane);
.LBB0_3066:
	s_waitcnt vmcnt(7)
	v_lshlrev_b32_e32 v135, 16, v117
	v_lshlrev_b32_e32 v134, 16, v116
	v_and_b32_e32 v137, 0xffff0000, v117
	v_and_b32_e32 v136, 0xffff0000, v116
	v_pk_add_f32 v[138:139], v[134:135], v[136:137]
	s_waitcnt vmcnt(6)
	v_and_b32_e32 v159, 0xffff0000, v119
	v_add_f32_e32 v138, v138, v139
	v_add_f32_e32 v157, 0, v138
	v_lshlrev_b32_e32 v139, 16, v119
	v_lshlrev_b32_e32 v138, 16, v118
	v_and_b32_e32 v158, 0xffff0000, v118
	s_waitcnt vmcnt(5)
	v_lshlrev_b32_e32 v96, 16, v120
	v_and_b32_e32 v97, 0xffff0000, v120
	v_lshlrev_b32_e32 v98, 16, v121
	v_and_b32_e32 v99, 0xffff0000, v121
	v_pk_add_f32 v[160:161], v[138:139], v[158:159]
	s_waitcnt vmcnt(4)
	v_lshlrev_b32_e32 v150, 16, v122
	v_and_b32_e32 v152, 0xffff0000, v122
	v_pk_add_f32 v[160:161], v[160:161], v[160:161] op_sel_hi:[0,1]
	v_add_f32_e32 v151, v96, v97
	v_add_f32_e32 v153, v98, v99
	v_lshlrev_b32_e32 v154, 16, v123
	s_waitcnt lgkmcnt(0)
	v_and_b32_e32 v156, 0xffff0000, v123
	v_pk_add_f32 v[162:163], v[150:151], v[152:153]
	v_mov_b32_e32 v155, v161
	v_mov_b32_e32 v153, v251
	v_pk_add_f32 v[160:161], v[154:155], v[156:157]
	s_lshl_b32 s26, s19, 4
	v_pk_add_f32 v[160:161], v[162:163], v[160:161]
	v_lshlrev_b32_e32 v153, 2, v153
	v_add_f32_e32 v151, v160, v161
	v_xor_b32_e32 v155, 4, v153
	s_add_i32 s24, s18, s26
	s_ashr_i32 s25, s24, 31
	s_lshl_b64 s[20:21], s[24:25], 11
	v_xor_b32_e32 v155, 8, v153
	v_xor_b32_e32 v155, 16, v153
	v_xor_b32_e32 v155, 32, v153
	v_xor_b32_e32 v155, 64, v153
	v_xor_b32_e32 v153, 0x80, v153
	s_nop 1
	v_add_f32_dpp v151, v151, v151 quad_perm:[1,0,3,2] row_mask:0xf bank_mask:0xf
	s_nop 1
	v_add_f32_dpp v151, v151, v151 quad_perm:[2,3,0,1] row_mask:0xf bank_mask:0xf
	s_nop 1
	v_add_f32_dpp v151, v151, v151 row_half_mirror row_mask:0xf bank_mask:0xf
	s_nop 1
	v_add_f32_dpp v151, v151, v151 row_mirror row_mask:0xf bank_mask:0xf
	v_mov_b32_e32 v153, v151
	v_mov_b32_e32 v155, v151
	s_nop 1
	v_permlane16_swap_b32 v153, v155
	v_add_f32_e32 v151, v153, v155
	v_mov_b32_e32 v153, v151
	v_mov_b32_e32 v155, v151
	s_nop 1
	v_permlane32_swap_b32 v153, v155
	v_add_f32_e32 v151, v153, v155
	v_fmac_f32_e32 v136, 0xba800000, v151
	v_fmac_f32_e32 v137, 0xba800000, v151
	v_fmac_f32_e32 v135, 0xba800000, v151
	v_fmac_f32_e32 v134, 0xba800000, v151
	v_mov_b32_e32 v160, v135
	v_mov_b32_e32 v161, v137
	v_mov_b32_e32 v135, v136
	v_pk_mul_f32 v[162:163], v[160:161], v[160:161]
	v_pk_mul_f32 v[136:137], v[134:135], v[134:135]
	v_fmac_f32_e32 v158, 0xba800000, v151
	v_pk_mov_b32 v[164:165], v[136:137], v[162:163] op_sel:[1,0]
	v_mov_b32_e32 v137, v163
	v_fmac_f32_e32 v159, 0xba800000, v151
	v_fmac_f32_e32 v139, 0xba800000, v151
	v_pk_add_f32 v[136:137], v[164:165], v[136:137]
	v_fmac_f32_e32 v138, 0xba800000, v151
	v_mov_b32_e32 v162, v139
	v_mov_b32_e32 v163, v159
	v_mov_b32_e32 v139, v158
	v_pk_add_f32 v[136:137], v[136:137], v[136:137] op_sel_hi:[0,1]
	v_pk_mul_f32 v[164:165], v[162:163], v[162:163]
	v_pk_mul_f32 v[158:159], v[138:139], v[138:139]
	v_fmac_f32_e32 v96, 0xba800000, v151
	v_pk_mov_b32 v[166:167], v[158:159], v[164:165] op_sel:[1,0]
	v_mov_b32_e32 v159, v165
	v_fmac_f32_e32 v97, 0xba800000, v151
	v_fmac_f32_e32 v98, 0xba800000, v151
	v_mul_f32_e32 v136, v96, v96
	v_pk_add_f32 v[158:159], v[166:167], v[158:159]
	v_fmac_f32_e32 v99, 0xba800000, v151
	v_pk_fma_f32 v[164:165], v[96:97], v[96:97], v[136:137] op_sel_hi:[1,1,0]
	v_mul_f32_e32 v136, v98, v98
	v_pk_add_f32 v[158:159], v[158:159], v[158:159] op_sel_hi:[0,1]
	v_pk_fma_f32 v[166:167], v[98:99], v[98:99], v[136:137] op_sel_hi:[1,1,0]
	v_fmac_f32_e32 v156, 0xba800000, v151
	v_fmac_f32_e32 v154, 0xba800000, v151
	v_fmac_f32_e32 v152, 0xba800000, v151
	v_fmac_f32_e32 v150, 0xba800000, v151
	v_mul_f32_e32 v164, v150, v150
	v_mul_f32_e32 v166, v152, v152
	v_mul_f32_e32 v136, v154, v154
	v_mul_f32_e32 v158, v156, v156
	v_pk_add_f32 v[164:165], v[164:165], v[166:167]
	v_pk_add_f32 v[136:137], v[136:137], v[158:159]
	s_nop 0
	v_pk_add_f32 v[136:137], v[164:165], v[136:137]
	s_nop 0
	v_add_f32_e32 v136, v136, v137
	v_mov_b32_e32 v137, v251
	s_nop 0
	v_lshlrev_b32_e32 v137, 2, v137
	v_xor_b32_e32 v151, 4, v137
	v_xor_b32_e32 v151, 8, v137
	v_xor_b32_e32 v151, 16, v137
	v_xor_b32_e32 v151, 32, v137
	v_xor_b32_e32 v151, 64, v137
	v_xor_b32_e32 v137, 0x80, v137
	s_nop 1
	v_add_f32_dpp v136, v136, v136 quad_perm:[1,0,3,2] row_mask:0xf bank_mask:0xf
	s_nop 1
	v_add_f32_dpp v136, v136, v136 quad_perm:[2,3,0,1] row_mask:0xf bank_mask:0xf
	s_nop 1
	v_add_f32_dpp v136, v136, v136 row_half_mirror row_mask:0xf bank_mask:0xf
	s_nop 1
	v_add_f32_dpp v136, v136, v136 row_mirror row_mask:0xf bank_mask:0xf
	v_mov_b32_e32 v137, v136
	v_mov_b32_e32 v151, v136
	s_nop 1
	v_permlane16_swap_b32 v137, v151
	v_add_f32_e32 v136, v137, v151
	v_mov_b32_e32 v137, v136
	v_mov_b32_e32 v151, v136
	s_nop 1
	v_permlane32_swap_b32 v137, v151
	v_add_f32_e32 v136, v137, v151
	v_fmamk_f32 v136, v136, 0x3a800000, v249
	v_mul_f32_e32 v137, 0x4f800000, v136
	v_cmp_gt_f32_e32 vcc, s52, v136
	s_nop 1
	v_cndmask_b32_e32 v136, v136, v137, vcc
	v_sqrt_f32_e32 v137, v136
	s_nop 0
	v_add_u32_e32 v151, -1, v137
	v_fma_f32 v153, -v151, v137, v136
	v_cmp_ge_f32_e64 s[12:13], 0, v153
	v_add_u32_e32 v153, 1, v137
	s_nop 0
	v_cndmask_b32_e64 v151, v137, v151, s[12:13]
	v_fma_f32 v137, -v153, v137, v136
	v_cmp_lt_f32_e64 s[12:13], 0, v137
	s_nop 1
	v_cndmask_b32_e64 v137, v151, v153, s[12:13]
	v_mul_f32_e32 v151, 0x37800000, v137
	v_cndmask_b32_e32 v137, v137, v151, vcc
	v_cmp_class_f32_e32 vcc, v136, v250
	s_nop 1
	v_cndmask_b32_e32 v136, v137, v136, vcc
	v_div_scale_f32 v137, s[12:13], v136, v136, 1.0
	v_rcp_f32_e32 v151, v137
	s_lshl_b64 s[12:13], s[24:25], 10
; #define LAS __attribute__((address_space(3)))
; __device__ __forceinline__ unsigned f2bf(float f) { unsigned u = __builtin_bit_cast(unsigned, f); return (u + 0x7fffu + ((u >> 16) & 1u)) >> 16; }
; __device__ __forceinline__ unsigned pk2(float lo, float hi) { return f2bf(lo) | (f2bf(hi) << 16); }
; __device__ __forceinline__ unsigned q8x4(float a, float b, float c, float d, float s) { return q8_(a, s) | (q8_(b, s) << 8) | (q8_(c, s) << 16) | (q8_(d, s) << 24); }
; __device__ __forceinline__ void store_row_fp8(const f32x4 (&v)[4], unsigned char* o8, int lane) {
; #pragma unroll
;     for (int j = 0; j < 4; ++j) *(unsigned*)(o8 + 4 * lane + 256 * j) = q8x4(v[j][0], v[j][1], v[j][2], v[j][3], QS_H);
; }
; __global__ void __launch_bounds__(NWAVES * 64, 2) fwd(Args args) {
;     ...
;                         for (int j = 0; j < 4; ++j) v[j] = (f32x4){bflo(raw[tk][j].x), bfhi(raw[tk][j].x), bflo(raw[tk][j].y), bfhi(raw[tk][j].y)};
;                         ln_rows_pre(v, aff1); store_row_f32_bf16(v, nullptr, H1 + (size_t)(m0 + tk) * D, lane); store_row_fp8(v, (unsigned char*)H1B + (size_t)(m0 + tk) * D, lane);
; #pragma unroll
;                         for (int j = 0; j < 4; ++j) { unsigned hh[4]; float rr[4];
; #pragma unroll
;                             for (int q = 0; q < 4; ++q) { hh[q] = f2bf(v[j][q]); rr[q] = v[j][q] - __builtin_bit_cast(float, hh[q] << 16); }
;                             const int o_ = (2 * wave + tk) * HP + (4 * lane + 256 * j) * 2;
;                             *(LAS v2u*)(hhi + o_) = (v2u){hh[0] | (hh[1] << 16), hh[2] | (hh[3] << 16)}; *(LAS v2u*)(hlo + o_) = (v2u){pk2(rr[0], rr[1]), pk2(rr[2], rr[3])}; } }
	v_fma_f32 v153, -v137, v151, 1.0
	v_fmac_f32_e32 v151, v153, v151
	v_div_scale_f32 v153, vcc, 1.0, v136, 1.0
	v_mul_f32_e32 v155, v153, v151
	v_fma_f32 v157, -v137, v155, v153
	v_fmac_f32_e32 v155, v157, v151
	v_fma_f32 v137, -v137, v155, v153
	v_div_fmas_f32 v137, v137, v151, v155
	v_div_fixup_f32 v158, v137, v136, 1.0
	v_pk_mul_f32 v[134:135], v[134:135], v[158:159] op_sel_hi:[1,0]
	v_mov_b32_e32 v151, v152
	v_pk_fma_f32 v[164:165], v[0:1], v[134:135], v[8:9]
	v_pk_mul_f32 v[136:137], v[160:161], v[158:159] op_sel_hi:[1,0]
	v_bfe_u32 v152, v164, 16, 1
	v_add3_u32 v152, v164, v152, s55
	v_bfe_u32 v153, v165, 16, 1
	v_pk_fma_f32 v[160:161], v[2:3], v[136:137], v[10:11]
	v_lshrrev_b32_e32 v152, 16, v152
	v_add3_u32 v153, v165, v153, s55
	v_pk_mul_f32 v[136:137], v[162:163], v[158:159] op_sel_hi:[1,0]
	v_pk_mul_f32 v[96:97], v[96:97], v[158:159] op_sel_hi:[1,0]
	v_mov_b32_e32 v155, v156
	v_and_or_b32 v152, v153, s53, v152
	v_bfe_u32 v153, v160, 16, 1
	v_pk_mul_f32 v[134:135], v[138:139], v[158:159] op_sel_hi:[1,0]
	v_pk_fma_f32 v[138:139], v[6:7], v[136:137], v[14:15]
	v_pk_fma_f32 v[136:137], v[16:17], v[96:97], v[24:25]
	v_pk_mul_f32 v[96:97], v[154:155], v[158:159] op_sel_hi:[1,0]
	v_add3_u32 v153, v160, v153, s55
	v_bfe_u32 v154, v161, 16, 1
	v_pk_mul_f32 v[98:99], v[98:99], v[158:159] op_sel_hi:[1,0]
	v_lshrrev_b32_e32 v153, 16, v153
	v_add3_u32 v154, v161, v154, s55
	v_pk_fma_f32 v[162:163], v[4:5], v[134:135], v[12:13]
	v_pk_fma_f32 v[134:135], v[18:19], v[98:99], v[26:27]
	v_pk_mul_f32 v[98:99], v[150:151], v[158:159] op_sel_hi:[1,0]
	v_lshl_add_u64 v[150:151], v[104:105], 0, s[20:21]
	v_and_or_b32 v153, v154, s53, v153
	global_store_dwordx2 v[150:151], v[152:153], off
	v_bfe_u32 v152, v162, 16, 1
	v_add3_u32 v152, v162, v152, s55
	v_bfe_u32 v153, v163, 16, 1
	v_lshrrev_b32_e32 v152, 16, v152
	v_add3_u32 v153, v163, v153, s55
	v_and_or_b32 v152, v153, s53, v152
	v_bfe_u32 v153, v138, 16, 1
	v_add3_u32 v153, v138, v153, s55
	v_bfe_u32 v154, v139, 16, 1
	v_lshrrev_b32_e32 v153, 16, v153
	v_add3_u32 v154, v139, v154, s55
	v_and_or_b32 v153, v154, s53, v153
	global_store_dwordx2 v[150:151], v[152:153], off offset:512
	v_bfe_u32 v152, v136, 16, 1
	v_add3_u32 v152, v136, v152, s55
	v_bfe_u32 v153, v137, 16, 1
	v_lshrrev_b32_e32 v152, 16, v152
	v_add3_u32 v153, v137, v153, s55
	v_and_or_b32 v152, v153, s53, v152
	v_bfe_u32 v153, v134, 16, 1
	v_add3_u32 v153, v134, v153, s55
	v_bfe_u32 v154, v135, 16, 1
	v_lshrrev_b32_e32 v153, 16, v153
	v_add3_u32 v154, v135, v154, s55
	v_pk_fma_f32 v[98:99], v[20:21], v[98:99], v[28:29]
	v_and_or_b32 v153, v154, s53, v153
	global_store_dwordx2 v[150:151], v[152:153], off offset:1024
	v_bfe_u32 v152, v98, 16, 1
	v_add3_u32 v152, v98, v152, s55
	v_bfe_u32 v153, v99, 16, 1
	v_pk_fma_f32 v[96:97], v[22:23], v[96:97], v[30:31]
	v_lshrrev_b32_e32 v152, 16, v152
	v_add3_u32 v153, v99, v153, s55
	v_and_or_b32 v152, v153, s53, v152
	v_bfe_u32 v153, v96, 16, 1
	v_add3_u32 v153, v96, v153, s55
	v_bfe_u32 v154, v97, 16, 1
	v_lshrrev_b32_e32 v153, 16, v153
	v_add3_u32 v154, v97, v154, s55
	v_and_or_b32 v153, v154, s53, v153
	global_store_dwordx2 v[150:151], v[152:153], off offset:1536
	v_mul_f32_e32 v153, 0x41cb3333, v165
	v_mul_f32_e32 v152, 0x41cb3333, v164
	v_med3_f32 v153, v153, s54, v213
	v_mul_f32_e32 v154, 0x41cb3333, v160
	v_mul_f32_e32 v155, 0x41cb3333, v161
	v_med3_f32 v152, v152, s54, v213
	v_rndne_f32_e32 v153, v153
	v_med3_f32 v154, v154, s54, v213
	v_med3_f32 v155, v155, s54, v213
	v_rndne_f32_e32 v152, v152
	v_cvt_i32_f32_e32 v153, v153
	v_rndne_f32_e32 v154, v154
	v_rndne_f32_e32 v155, v155
	v_cvt_i32_f32_e32 v152, v152
	v_cvt_i32_f32_sdwa v154, v154 dst_sel:WORD_1 dst_unused:UNUSED_PAD src0_sel:DWORD
	v_cvt_i32_f32_e32 v155, v155
	v_lshlrev_b32_e32 v153, 8, v153
	v_and_b32_e32 v153, 0xff00, v153
	v_and_b32_e32 v154, 0xff0000, v154
	v_perm_b32 v152, v155, v152, s65
	v_lshl_add_u64 v[150:151], v[110:111], 0, s[12:13]
	v_or3_b32 v152, v152, v153, v154
	v_mul_f32_e32 v153, 0x41cb3333, v163
	global_store_dword v[150:151], v152, off
	v_mul_f32_e32 v152, 0x41cb3333, v162
	v_med3_f32 v153, v153, s54, v213
	v_mul_f32_e32 v154, 0x41cb3333, v138
	v_mul_f32_e32 v155, 0x41cb3333, v139
	v_med3_f32 v152, v152, s54, v213
	v_rndne_f32_e32 v153, v153
	v_med3_f32 v154, v154, s54, v213
	v_med3_f32 v155, v155, s54, v213
	v_rndne_f32_e32 v152, v152
	v_cvt_i32_f32_e32 v153, v153
	v_rndne_f32_e32 v154, v154
	v_rndne_f32_e32 v155, v155
	v_cvt_i32_f32_e32 v152, v152
	v_cvt_i32_f32_sdwa v154, v154 dst_sel:WORD_1 dst_unused:UNUSED_PAD src0_sel:DWORD
	v_cvt_i32_f32_e32 v155, v155
	v_lshlrev_b32_e32 v153, 8, v153
	v_and_b32_e32 v153, 0xff00, v153
	v_and_b32_e32 v154, 0xff0000, v154
	v_perm_b32 v152, v155, v152, s65
	v_or3_b32 v152, v152, v153, v154
	v_mul_f32_e32 v153, 0x41cb3333, v137
	global_store_dword v[150:151], v152, off offset:256
	v_mul_f32_e32 v152, 0x41cb3333, v136
	v_med3_f32 v153, v153, s54, v213
	v_mul_f32_e32 v154, 0x41cb3333, v134
	v_mul_f32_e32 v155, 0x41cb3333, v135
	v_med3_f32 v152, v152, s54, v213
	v_rndne_f32_e32 v153, v153
	v_med3_f32 v154, v154, s54, v213
	v_med3_f32 v155, v155, s54, v213
	v_rndne_f32_e32 v152, v152
	v_cvt_i32_f32_e32 v153, v153
	v_rndne_f32_e32 v154, v154
	v_rndne_f32_e32 v155, v155
	v_cvt_i32_f32_e32 v152, v152
	v_cvt_i32_f32_sdwa v154, v154 dst_sel:WORD_1 dst_unused:UNUSED_PAD src0_sel:DWORD
	v_cvt_i32_f32_e32 v155, v155
	v_lshlrev_b32_e32 v153, 8, v153
	v_and_b32_e32 v153, 0xff00, v153
	v_and_b32_e32 v154, 0xff0000, v154
	v_perm_b32 v152, v155, v152, s65
	v_or3_b32 v152, v152, v153, v154
	v_mul_f32_e32 v153, 0x41cb3333, v99
	global_store_dword v[150:151], v152, off offset:512
; #define LAS __attribute__((address_space(3)))
; __device__ __forceinline__ unsigned f2bf(float f) { unsigned u = __builtin_bit_cast(unsigned, f); return (u + 0x7fffu + ((u >> 16) & 1u)) >> 16; }
; __device__ __forceinline__ unsigned pk2(float lo, float hi) { return f2bf(lo) | (f2bf(hi) << 16); }
; __device__ __forceinline__ unsigned q8x4(float a, float b, float c, float d, float s) { return q8_(a, s) | (q8_(b, s) << 8) | (q8_(c, s) << 16) | (q8_(d, s) << 24); }
; __device__ __forceinline__ void store_row_fp8(const f32x4 (&v)[4], unsigned char* o8, int lane) {
; #pragma unroll
;     for (int j = 0; j < 4; ++j) *(unsigned*)(o8 + 4 * lane + 256 * j) = q8x4(v[j][0], v[j][1], v[j][2], v[j][3], QS_H);
; }
; __global__ void __launch_bounds__(NWAVES * 64, 2) fwd(Args args) {
;     ...
;                         for (int j = 0; j < 4; ++j) { unsigned hh[4]; float rr[4];
; #pragma unroll
;                             for (int q = 0; q < 4; ++q) { hh[q] = f2bf(v[j][q]); rr[q] = v[j][q] - __builtin_bit_cast(float, hh[q] << 16); }
;                             const int o_ = (2 * wave + tk) * HP + (4 * lane + 256 * j) * 2;
;                             *(LAS v2u*)(hhi + o_) = (v2u){hh[0] | (hh[1] << 16), hh[2] | (hh[3] << 16)}; *(LAS v2u*)(hlo + o_) = (v2u){pk2(rr[0], rr[1]), pk2(rr[2], rr[3])}; } }
	v_mul_f32_e32 v152, 0x41cb3333, v98
	v_med3_f32 v153, v153, s54, v213
	v_mul_f32_e32 v154, 0x41cb3333, v96
	v_mul_f32_e32 v155, 0x41cb3333, v97
	v_med3_f32 v152, v152, s54, v213
	v_rndne_f32_e32 v153, v153
	v_med3_f32 v154, v154, s54, v213
	v_med3_f32 v155, v155, s54, v213
	v_rndne_f32_e32 v152, v152
	v_cvt_i32_f32_e32 v153, v153
	v_rndne_f32_e32 v154, v154
	v_rndne_f32_e32 v155, v155
	v_cvt_i32_f32_e32 v152, v152
	v_cvt_i32_f32_sdwa v154, v154 dst_sel:WORD_1 dst_unused:UNUSED_PAD src0_sel:DWORD
	v_cvt_i32_f32_e32 v155, v155
	v_lshlrev_b32_e32 v153, 8, v153
	v_and_b32_e32 v153, 0xff00, v153
	v_and_b32_e32 v154, 0xff0000, v154
	v_perm_b32 v152, v155, v152, s65
	v_or3_b32 v152, v152, v153, v154
	global_store_dword v[150:151], v152, off offset:768
	v_and_b32_sdwa v152, v160, v248 dst_sel:DWORD dst_unused:UNUSED_PAD src0_sel:WORD_1 src1_sel:DWORD
	v_and_b32_sdwa v153, v164, v248 dst_sel:DWORD dst_unused:UNUSED_PAD src0_sel:WORD_1 src1_sel:DWORD
	v_add3_u32 v156, v160, v152, s55
	v_and_b32_sdwa v152, v161, v248 dst_sel:DWORD dst_unused:UNUSED_PAD src0_sel:WORD_1 src1_sel:DWORD
	v_add3_u32 v158, v164, v153, s55
	v_and_b32_sdwa v153, v165, v248 dst_sel:DWORD dst_unused:UNUSED_PAD src0_sel:WORD_1 src1_sel:DWORD
	v_add3_u32 v152, v161, v152, s55
	v_add3_u32 v154, v165, v153, s55
	v_and_b32_e32 v153, 0xffff0000, v152
	v_mov_b32_e32 v150, v164
	v_mov_b32_e32 v151, v160
	v_or_b32_sdwa v155, v153, v156 dst_sel:DWORD dst_unused:UNUSED_PAD src0_sel:DWORD src1_sel:WORD_1
	v_and_b32_e32 v157, 0xffff0000, v156
	v_and_b32_e32 v156, 0xffff0000, v158
	v_mov_b32_e32 v160, v165
	v_and_b32_e32 v152, 0xffff0000, v154
	v_pk_add_f32 v[150:151], v[150:151], v[156:157] neg_lo:[0,1] neg_hi:[0,1]
	v_or_b32_sdwa v154, v152, v158 dst_sel:DWORD dst_unused:UNUSED_PAD src0_sel:DWORD src1_sel:WORD_1
	v_pk_add_f32 v[152:153], v[160:161], v[152:153] neg_lo:[0,1] neg_hi:[0,1]
	v_and_b32_sdwa v156, v151, v248 dst_sel:DWORD dst_unused:UNUSED_PAD src0_sel:WORD_1 src1_sel:DWORD
	v_and_b32_sdwa v157, v150, v248 dst_sel:DWORD dst_unused:UNUSED_PAD src0_sel:WORD_1 src1_sel:DWORD
	v_add3_u32 v150, v150, v157, s55
	v_add3_u32 v151, v151, v156, s55
	v_and_b32_sdwa v156, v153, v248 dst_sel:DWORD dst_unused:UNUSED_PAD src0_sel:WORD_1 src1_sel:DWORD
	v_and_b32_sdwa v157, v152, v248 dst_sel:DWORD dst_unused:UNUSED_PAD src0_sel:WORD_1 src1_sel:DWORD
	v_add3_u32 v153, v153, v156, s55
	v_add3_u32 v152, v152, v157, s55
	v_and_b32_sdwa v156, v138, v248 dst_sel:DWORD dst_unused:UNUSED_PAD src0_sel:WORD_1 src1_sel:DWORD
	v_and_b32_sdwa v157, v162, v248 dst_sel:DWORD dst_unused:UNUSED_PAD src0_sel:WORD_1 src1_sel:DWORD
	v_add3_u32 v160, v138, v156, s55
	v_add3_u32 v161, v162, v157, s55
	v_and_b32_sdwa v156, v139, v248 dst_sel:DWORD dst_unused:UNUSED_PAD src0_sel:WORD_1 src1_sel:DWORD
	v_and_b32_sdwa v157, v163, v248 dst_sel:DWORD dst_unused:UNUSED_PAD src0_sel:WORD_1 src1_sel:DWORD
	v_add3_u32 v156, v139, v156, s55
	v_add3_u32 v158, v163, v157, s55
	v_and_b32_e32 v157, 0xffff0000, v156
	v_and_b32_e32 v156, 0xffff0000, v158
	v_and_b32_e32 v153, 0xffff0000, v153
	v_and_b32_e32 v152, 0xffff0000, v152
	v_or_b32_sdwa v159, v157, v160 dst_sel:DWORD dst_unused:UNUSED_PAD src0_sel:DWORD src1_sel:WORD_1
	v_or_b32_sdwa v158, v156, v161 dst_sel:DWORD dst_unused:UNUSED_PAD src0_sel:DWORD src1_sel:WORD_1
	v_or_b32_sdwa v151, v153, v151 dst_sel:DWORD dst_unused:UNUSED_PAD src0_sel:DWORD src1_sel:WORD_1
	v_or_b32_sdwa v150, v152, v150 dst_sel:DWORD dst_unused:UNUSED_PAD src0_sel:DWORD src1_sel:WORD_1
	v_mov_b32_e32 v152, v162
	v_mov_b32_e32 v153, v138
	ds_write2st64_b64 v147, v[154:155], v[158:159] offset1:1
	v_and_b32_e32 v155, 0xffff0000, v160
	v_and_b32_e32 v154, 0xffff0000, v161
	v_mov_b32_e32 v138, v163
	v_pk_add_f32 v[152:153], v[152:153], v[154:155] neg_lo:[0,1] neg_hi:[0,1]
	v_pk_add_f32 v[138:139], v[138:139], v[156:157] neg_lo:[0,1] neg_hi:[0,1]
	v_and_b32_sdwa v154, v153, v248 dst_sel:DWORD dst_unused:UNUSED_PAD src0_sel:WORD_1 src1_sel:DWORD
	v_and_b32_sdwa v155, v152, v248 dst_sel:DWORD dst_unused:UNUSED_PAD src0_sel:WORD_1 src1_sel:DWORD
	v_add3_u32 v152, v152, v155, s55
	v_add3_u32 v153, v153, v154, s55
	v_and_b32_sdwa v154, v139, v248 dst_sel:DWORD dst_unused:UNUSED_PAD src0_sel:WORD_1 src1_sel:DWORD
	v_and_b32_sdwa v155, v138, v248 dst_sel:DWORD dst_unused:UNUSED_PAD src0_sel:WORD_1 src1_sel:DWORD
	v_add3_u32 v139, v139, v154, s55
	v_add3_u32 v138, v138, v155, s55
	v_and_b32_e32 v139, 0xffff0000, v139
	v_and_b32_e32 v138, 0xffff0000, v138
	v_or_b32_sdwa v139, v139, v153 dst_sel:DWORD dst_unused:UNUSED_PAD src0_sel:DWORD src1_sel:WORD_1
	v_or_b32_sdwa v138, v138, v152 dst_sel:DWORD dst_unused:UNUSED_PAD src0_sel:DWORD src1_sel:WORD_1
	v_add_u32_e32 v154, 0x100, v147
	ds_write2st64_b64 v154, v[150:151], v[138:139] offset0:64 offset1:65
	v_and_b32_sdwa v151, v136, v248 dst_sel:DWORD dst_unused:UNUSED_PAD src0_sel:WORD_1 src1_sel:DWORD
	v_mov_b32_e32 v138, v136
	v_and_b32_sdwa v150, v134, v248 dst_sel:DWORD dst_unused:UNUSED_PAD src0_sel:WORD_1 src1_sel:DWORD
	v_add3_u32 v155, v136, v151, s55
	v_and_b32_sdwa v136, v135, v248 dst_sel:DWORD dst_unused:UNUSED_PAD src0_sel:WORD_1 src1_sel:DWORD
	v_add3_u32 v152, v134, v150, s55
	v_and_b32_sdwa v150, v137, v248 dst_sel:DWORD dst_unused:UNUSED_PAD src0_sel:WORD_1 src1_sel:DWORD
	v_add3_u32 v136, v135, v136, s55
	v_mov_b32_e32 v139, v134
	v_mov_b32_e32 v134, v137
	v_add3_u32 v150, v137, v150, s55
	v_and_b32_e32 v137, 0xffff0000, v136
	v_or_b32_sdwa v151, v137, v152 dst_sel:DWORD dst_unused:UNUSED_PAD src0_sel:DWORD src1_sel:WORD_1
	v_and_b32_e32 v153, 0xffff0000, v152
	v_and_b32_e32 v152, 0xffff0000, v155
	v_and_b32_e32 v136, 0xffff0000, v150
; #define LAS __attribute__((address_space(3)))
; __device__ __forceinline__ unsigned f2bf(float f) { unsigned u = __builtin_bit_cast(unsigned, f); return (u + 0x7fffu + ((u >> 16) & 1u)) >> 16; }
; __device__ __forceinline__ unsigned pk2(float lo, float hi) { return f2bf(lo) | (f2bf(hi) << 16); }
; __device__ __forceinline__ void ln_rows_pre(f32x4 (&v)[4], const LnAff& a) {
;     float s = 0.f;
; #pragma unroll
;     for (int j = 0; j < 4; ++j) s += (v[j][0] + v[j][1]) + (v[j][2] + v[j][3]);
;     const float mean = wave_sum(s) * (1.f / D); float s2 = 0.f;
; #pragma unroll
;     for (int j = 0; j < 4; ++j) { v[j] = v[j] - mean; s2 += (v[j][0] * v[j][0] + v[j][1] * v[j][1]) + (v[j][2] * v[j][2] + v[j][3] * v[j][3]); }
;     const float rstd = 1.f / sqrtf(wave_sum(s2) * (1.f / D) + LN_EPS);
; __global__ void __launch_bounds__(NWAVES * 64, 2) fwd(Args args) {
;     ...
;                         for (int j = 0; j < 4; ++j) { unsigned hh[4]; float rr[4];
; #pragma unroll
;                             for (int q = 0; q < 4; ++q) { hh[q] = f2bf(v[j][q]); rr[q] = v[j][q] - __builtin_bit_cast(float, hh[q] << 16); }
;                             const int o_ = (2 * wave + tk) * HP + (4 * lane + 256 * j) * 2;
;                             *(LAS v2u*)(hhi + o_) = (v2u){hh[0] | (hh[1] << 16), hh[2] | (hh[3] << 16)}; *(LAS v2u*)(hlo + o_) = (v2u){pk2(rr[0], rr[1]), pk2(rr[2], rr[3])}; } }
	v_pk_add_f32 v[138:139], v[138:139], v[152:153] neg_lo:[0,1] neg_hi:[0,1]
	v_pk_add_f32 v[134:135], v[134:135], v[136:137] neg_lo:[0,1] neg_hi:[0,1]
	v_and_b32_sdwa v137, v138, v248 dst_sel:DWORD dst_unused:UNUSED_PAD src0_sel:WORD_1 src1_sel:DWORD
	v_or_b32_sdwa v150, v136, v155 dst_sel:DWORD dst_unused:UNUSED_PAD src0_sel:DWORD src1_sel:WORD_1
	v_and_b32_sdwa v136, v139, v248 dst_sel:DWORD dst_unused:UNUSED_PAD src0_sel:WORD_1 src1_sel:DWORD
	v_add3_u32 v137, v138, v137, s55
	v_and_b32_sdwa v138, v135, v248 dst_sel:DWORD dst_unused:UNUSED_PAD src0_sel:WORD_1 src1_sel:DWORD
	v_add3_u32 v136, v139, v136, s55
	v_and_b32_sdwa v139, v134, v248 dst_sel:DWORD dst_unused:UNUSED_PAD src0_sel:WORD_1 src1_sel:DWORD
	v_add3_u32 v135, v135, v138, s55
	v_add3_u32 v134, v134, v139, s55
	v_and_b32_e32 v135, 0xffff0000, v135
	v_and_b32_sdwa v138, v96, v248 dst_sel:DWORD dst_unused:UNUSED_PAD src0_sel:WORD_1 src1_sel:DWORD
	v_and_b32_sdwa v139, v98, v248 dst_sel:DWORD dst_unused:UNUSED_PAD src0_sel:WORD_1 src1_sel:DWORD
	v_or_b32_sdwa v135, v135, v136 dst_sel:DWORD dst_unused:UNUSED_PAD src0_sel:DWORD src1_sel:WORD_1
	v_mov_b32_e32 v136, v98
	v_add3_u32 v152, v96, v138, s55
	v_add3_u32 v153, v98, v139, s55
	v_and_b32_sdwa v98, v97, v248 dst_sel:DWORD dst_unused:UNUSED_PAD src0_sel:WORD_1 src1_sel:DWORD
	v_and_b32_sdwa v138, v99, v248 dst_sel:DWORD dst_unused:UNUSED_PAD src0_sel:WORD_1 src1_sel:DWORD
	v_and_b32_e32 v134, 0xffff0000, v134
	v_add3_u32 v98, v97, v98, s55
	v_add3_u32 v138, v99, v138, s55
	v_or_b32_sdwa v134, v134, v137 dst_sel:DWORD dst_unused:UNUSED_PAD src0_sel:DWORD src1_sel:WORD_1
	v_mov_b32_e32 v137, v96
	v_mov_b32_e32 v96, v99
	v_and_b32_e32 v99, 0xffff0000, v98
	v_and_b32_e32 v98, 0xffff0000, v138
	v_or_b32_sdwa v139, v99, v152 dst_sel:DWORD dst_unused:UNUSED_PAD src0_sel:DWORD src1_sel:WORD_1
	v_or_b32_sdwa v138, v98, v153 dst_sel:DWORD dst_unused:UNUSED_PAD src0_sel:DWORD src1_sel:WORD_1
	ds_write2st64_b64 v147, v[150:151], v[138:139] offset0:2 offset1:3
	v_and_b32_e32 v139, 0xffff0000, v152
	v_and_b32_e32 v138, 0xffff0000, v153
	v_pk_add_f32 v[136:137], v[136:137], v[138:139] neg_lo:[0,1] neg_hi:[0,1]
	v_pk_add_f32 v[96:97], v[96:97], v[98:99] neg_lo:[0,1] neg_hi:[0,1]
	v_and_b32_sdwa v98, v137, v248 dst_sel:DWORD dst_unused:UNUSED_PAD src0_sel:WORD_1 src1_sel:DWORD
	v_and_b32_sdwa v99, v136, v248 dst_sel:DWORD dst_unused:UNUSED_PAD src0_sel:WORD_1 src1_sel:DWORD
	v_add3_u32 v99, v136, v99, s55
	v_add3_u32 v98, v137, v98, s55
	v_and_b32_sdwa v136, v97, v248 dst_sel:DWORD dst_unused:UNUSED_PAD src0_sel:WORD_1 src1_sel:DWORD
	v_and_b32_sdwa v137, v96, v248 dst_sel:DWORD dst_unused:UNUSED_PAD src0_sel:WORD_1 src1_sel:DWORD
	v_add3_u32 v97, v97, v136, s55
	v_add3_u32 v96, v96, v137, s55
	v_and_b32_e32 v97, 0xffff0000, v97
	v_and_b32_e32 v96, 0xffff0000, v96
	v_or_b32_sdwa v97, v97, v98 dst_sel:DWORD dst_unused:UNUSED_PAD src0_sel:DWORD src1_sel:WORD_1
	v_or_b32_sdwa v96, v96, v99 dst_sel:DWORD dst_unused:UNUSED_PAD src0_sel:DWORD src1_sel:WORD_1
	ds_write2st64_b64 v154, v[134:135], v[96:97] offset0:66 offset1:67
	s_waitcnt vmcnt(11)
	v_lshlrev_b32_e32 v135, 16, v125
	v_lshlrev_b32_e32 v134, 16, v124
	v_and_b32_e32 v137, 0xffff0000, v125
	v_and_b32_e32 v136, 0xffff0000, v124
	v_pk_add_f32 v[138:139], v[134:135], v[136:137]
	s_waitcnt vmcnt(10)
	v_and_b32_e32 v159, 0xffff0000, v127
	v_add_f32_e32 v138, v138, v139
	v_add_f32_e32 v157, 0, v138
	v_lshlrev_b32_e32 v139, 16, v127
	v_lshlrev_b32_e32 v138, 16, v126
	v_and_b32_e32 v158, 0xffff0000, v126
	s_waitcnt vmcnt(9)
	v_lshlrev_b32_e32 v96, 16, v130
	v_and_b32_e32 v97, 0xffff0000, v130
	v_lshlrev_b32_e32 v98, 16, v131
	v_and_b32_e32 v99, 0xffff0000, v131
	v_pk_add_f32 v[160:161], v[138:139], v[158:159]
	s_waitcnt vmcnt(8)
	v_lshlrev_b32_e32 v150, 16, v132
	v_and_b32_e32 v152, 0xffff0000, v132
	v_pk_add_f32 v[160:161], v[160:161], v[160:161] op_sel_hi:[0,1]
	v_add_f32_e32 v151, v96, v97
	v_add_f32_e32 v153, v98, v99
	v_lshlrev_b32_e32 v154, 16, v133
	v_and_b32_e32 v156, 0xffff0000, v133
	v_pk_add_f32 v[162:163], v[150:151], v[152:153]
	v_mov_b32_e32 v155, v161
	v_mov_b32_e32 v153, v251
	v_pk_add_f32 v[160:161], v[154:155], v[156:157]
	s_nop 0
	v_pk_add_f32 v[160:161], v[162:163], v[160:161]
	v_lshlrev_b32_e32 v153, 2, v153
	v_add_f32_e32 v151, v160, v161
	v_xor_b32_e32 v155, 4, v153
	v_xor_b32_e32 v155, 8, v153
	v_xor_b32_e32 v155, 16, v153
	v_xor_b32_e32 v155, 32, v153
	v_xor_b32_e32 v155, 64, v153
	v_xor_b32_e32 v153, 0x80, v153
	s_nop 1
	v_add_f32_dpp v151, v151, v151 quad_perm:[1,0,3,2] row_mask:0xf bank_mask:0xf
	s_nop 1
	v_add_f32_dpp v151, v151, v151 quad_perm:[2,3,0,1] row_mask:0xf bank_mask:0xf
	s_nop 1
	v_add_f32_dpp v151, v151, v151 row_half_mirror row_mask:0xf bank_mask:0xf
	s_nop 1
	v_add_f32_dpp v151, v151, v151 row_mirror row_mask:0xf bank_mask:0xf
	v_mov_b32_e32 v153, v151
	v_mov_b32_e32 v155, v151
	s_nop 1
	v_permlane16_swap_b32 v153, v155
	v_add_f32_e32 v151, v153, v155
	v_mov_b32_e32 v153, v151
	v_mov_b32_e32 v155, v151
	s_nop 1
	v_permlane32_swap_b32 v153, v155
	v_add_f32_e32 v151, v153, v155
	v_fmac_f32_e32 v136, 0xba800000, v151
	v_fmac_f32_e32 v137, 0xba800000, v151
	v_fmac_f32_e32 v135, 0xba800000, v151
	v_fmac_f32_e32 v134, 0xba800000, v151
	v_mov_b32_e32 v160, v135
	v_mov_b32_e32 v161, v137
	v_mov_b32_e32 v135, v136
	v_pk_mul_f32 v[162:163], v[160:161], v[160:161]
	v_pk_mul_f32 v[136:137], v[134:135], v[134:135]
	v_fmac_f32_e32 v158, 0xba800000, v151
	v_pk_mov_b32 v[164:165], v[136:137], v[162:163] op_sel:[1,0]
	v_mov_b32_e32 v137, v163
	v_fmac_f32_e32 v159, 0xba800000, v151
	v_fmac_f32_e32 v139, 0xba800000, v151
	v_pk_add_f32 v[136:137], v[164:165], v[136:137]
; __device__ __forceinline__ void ln_rows_pre(f32x4 (&v)[4], const LnAff& a) {
;     float s = 0.f;
; #pragma unroll
;     for (int j = 0; j < 4; ++j) s += (v[j][0] + v[j][1]) + (v[j][2] + v[j][3]);
;     const float mean = wave_sum(s) * (1.f / D); float s2 = 0.f;
; #pragma unroll
;     for (int j = 0; j < 4; ++j) { v[j] = v[j] - mean; s2 += (v[j][0] * v[j][0] + v[j][1] * v[j][1]) + (v[j][2] * v[j][2] + v[j][3] * v[j][3]); }
;     const float rstd = 1.f / sqrtf(wave_sum(s2) * (1.f / D) + LN_EPS);
; #pragma unroll
;     for (int j = 0; j < 4; ++j) v[j] = v[j] * rstd * a.g[j] + a.b[j];
; }
; __global__ void __launch_bounds__(NWAVES * 64, 2) fwd(Args args) {
;     ...
;                     for (int tk = 0; tk < 2; ++tk) { f32x4 v[4];
; #pragma unroll
;                         for (int j = 0; j < 4; ++j) v[j] = (f32x4){bflo(raw[tk][j].x), bfhi(raw[tk][j].x), bflo(raw[tk][j].y), bfhi(raw[tk][j].y)};
;                         ln_rows_pre(v, aff1); store_row_f32_bf16(v, nullptr, H1 + (size_t)(m0 + tk) * D, lane); store_row_fp8(v, (unsigned char*)H1B + (size_t)(m0 + tk) * D, lane);
	v_fmac_f32_e32 v138, 0xba800000, v151
	v_mov_b32_e32 v162, v139
	v_mov_b32_e32 v163, v159
	v_mov_b32_e32 v139, v158
	v_pk_add_f32 v[136:137], v[136:137], v[136:137] op_sel_hi:[0,1]
	v_pk_mul_f32 v[164:165], v[162:163], v[162:163]
	v_pk_mul_f32 v[158:159], v[138:139], v[138:139]
	v_fmac_f32_e32 v96, 0xba800000, v151
	v_pk_mov_b32 v[166:167], v[158:159], v[164:165] op_sel:[1,0]
	v_mov_b32_e32 v159, v165
	v_fmac_f32_e32 v97, 0xba800000, v151
	v_fmac_f32_e32 v98, 0xba800000, v151
	v_mul_f32_e32 v136, v96, v96
	v_pk_add_f32 v[158:159], v[166:167], v[158:159]
	v_fmac_f32_e32 v99, 0xba800000, v151
	v_pk_fma_f32 v[164:165], v[96:97], v[96:97], v[136:137] op_sel_hi:[1,1,0]
	v_mul_f32_e32 v136, v98, v98
	v_pk_add_f32 v[158:159], v[158:159], v[158:159] op_sel_hi:[0,1]
	v_pk_fma_f32 v[166:167], v[98:99], v[98:99], v[136:137] op_sel_hi:[1,1,0]
	v_fmac_f32_e32 v156, 0xba800000, v151
	v_fmac_f32_e32 v154, 0xba800000, v151
	v_fmac_f32_e32 v152, 0xba800000, v151
	v_fmac_f32_e32 v150, 0xba800000, v151
	v_mul_f32_e32 v164, v150, v150
	v_mul_f32_e32 v166, v152, v152
	v_mul_f32_e32 v136, v154, v154
	v_mul_f32_e32 v158, v156, v156
	v_pk_add_f32 v[164:165], v[164:165], v[166:167]
	v_pk_add_f32 v[136:137], v[136:137], v[158:159]
	s_nop 0
	v_pk_add_f32 v[136:137], v[164:165], v[136:137]
	s_nop 0
	v_add_f32_e32 v136, v136, v137
	v_mov_b32_e32 v137, v251
	s_nop 0
	v_lshlrev_b32_e32 v137, 2, v137
	v_xor_b32_e32 v151, 4, v137
	v_xor_b32_e32 v151, 8, v137
	v_xor_b32_e32 v151, 16, v137
	v_xor_b32_e32 v151, 32, v137
	v_xor_b32_e32 v151, 64, v137
	v_xor_b32_e32 v137, 0x80, v137
	s_nop 1
	v_add_f32_dpp v136, v136, v136 quad_perm:[1,0,3,2] row_mask:0xf bank_mask:0xf
	s_nop 1
	v_add_f32_dpp v136, v136, v136 quad_perm:[2,3,0,1] row_mask:0xf bank_mask:0xf
	s_nop 1
	v_add_f32_dpp v136, v136, v136 row_half_mirror row_mask:0xf bank_mask:0xf
	s_nop 1
	v_add_f32_dpp v136, v136, v136 row_mirror row_mask:0xf bank_mask:0xf
	v_mov_b32_e32 v137, v136
	v_mov_b32_e32 v151, v136
	s_nop 1
	v_permlane16_swap_b32 v137, v151
	v_add_f32_e32 v136, v137, v151
	v_mov_b32_e32 v137, v136
	v_mov_b32_e32 v151, v136
	s_nop 1
	v_permlane32_swap_b32 v137, v151
	v_add_f32_e32 v136, v137, v151
	v_fmamk_f32 v136, v136, 0x3a800000, v249
	v_mul_f32_e32 v137, 0x4f800000, v136
	v_cmp_gt_f32_e32 vcc, s52, v136
	s_nop 1
	v_cndmask_b32_e32 v136, v136, v137, vcc
	v_sqrt_f32_e32 v137, v136
	s_nop 0
	v_add_u32_e32 v151, -1, v137
	v_fma_f32 v153, -v151, v137, v136
	v_cmp_ge_f32_e64 s[12:13], 0, v153
	v_add_u32_e32 v153, 1, v137
	s_nop 0
	v_cndmask_b32_e64 v151, v137, v151, s[12:13]
	v_fma_f32 v137, -v153, v137, v136
	v_cmp_lt_f32_e64 s[12:13], 0, v137
	s_nop 1
	v_cndmask_b32_e64 v137, v151, v153, s[12:13]
	v_mul_f32_e32 v151, 0x37800000, v137
	v_cndmask_b32_e32 v137, v137, v151, vcc
	v_cmp_class_f32_e32 vcc, v136, v250
	s_nop 1
	v_cndmask_b32_e32 v136, v137, v136, vcc
	v_div_scale_f32 v137, s[12:13], v136, v136, 1.0
	v_rcp_f32_e32 v151, v137
	s_or_b32 s12, s24, 1
	s_ashr_i32 s13, s12, 31
	s_lshl_b64 s[24:25], s[12:13], 10
	v_fma_f32 v153, -v137, v151, 1.0
	v_fmac_f32_e32 v151, v153, v151
	v_div_scale_f32 v153, vcc, 1.0, v136, 1.0
	v_mul_f32_e32 v155, v153, v151
	v_fma_f32 v157, -v137, v155, v153
	v_fmac_f32_e32 v155, v157, v151
	v_fma_f32 v137, -v137, v155, v153
	v_div_fmas_f32 v137, v137, v151, v155
	v_div_fixup_f32 v158, v137, v136, 1.0
	v_pk_mul_f32 v[134:135], v[134:135], v[158:159] op_sel_hi:[1,0]
	v_mov_b32_e32 v151, v152
	v_pk_fma_f32 v[164:165], v[0:1], v[134:135], v[8:9]
	v_pk_mul_f32 v[136:137], v[160:161], v[158:159] op_sel_hi:[1,0]
	v_bfe_u32 v152, v164, 16, 1
	v_add3_u32 v152, v164, v152, s55
	v_bfe_u32 v153, v165, 16, 1
	v_pk_fma_f32 v[160:161], v[2:3], v[136:137], v[10:11]
	v_lshrrev_b32_e32 v152, 16, v152
	v_add3_u32 v153, v165, v153, s55
	v_pk_mul_f32 v[136:137], v[162:163], v[158:159] op_sel_hi:[1,0]
	v_pk_mul_f32 v[96:97], v[96:97], v[158:159] op_sel_hi:[1,0]
	v_mov_b32_e32 v155, v156
	v_and_or_b32 v152, v153, s53, v152
	v_bfe_u32 v153, v160, 16, 1
	v_pk_mul_f32 v[134:135], v[138:139], v[158:159] op_sel_hi:[1,0]
	v_pk_fma_f32 v[138:139], v[6:7], v[136:137], v[14:15]
	v_pk_fma_f32 v[136:137], v[16:17], v[96:97], v[24:25]
	v_pk_mul_f32 v[96:97], v[154:155], v[158:159] op_sel_hi:[1,0]
	v_add3_u32 v153, v160, v153, s55
	v_bfe_u32 v154, v161, 16, 1
	v_pk_mul_f32 v[98:99], v[98:99], v[158:159] op_sel_hi:[1,0]
	s_lshl_b64 s[12:13], s[12:13], 11
	v_lshrrev_b32_e32 v153, 16, v153
	v_add3_u32 v154, v161, v154, s55
	v_pk_fma_f32 v[162:163], v[4:5], v[134:135], v[12:13]
	v_pk_fma_f32 v[134:135], v[18:19], v[98:99], v[26:27]
	v_pk_mul_f32 v[98:99], v[150:151], v[158:159] op_sel_hi:[1,0]
	v_lshl_add_u64 v[150:151], v[104:105], 0, s[12:13]
	v_and_or_b32 v153, v154, s53, v153
	global_store_dwordx2 v[150:151], v[152:153], off
	v_bfe_u32 v152, v162, 16, 1
	v_add3_u32 v152, v162, v152, s55
	v_bfe_u32 v153, v163, 16, 1
	v_lshrrev_b32_e32 v152, 16, v152
	v_add3_u32 v153, v163, v153, s55
	v_and_or_b32 v152, v153, s53, v152
	v_bfe_u32 v153, v138, 16, 1
	v_add3_u32 v153, v138, v153, s55
	v_bfe_u32 v154, v139, 16, 1
	v_lshrrev_b32_e32 v153, 16, v153
	v_add3_u32 v154, v139, v154, s55
	v_and_or_b32 v153, v154, s53, v153
	global_store_dwordx2 v[150:151], v[152:153], off offset:512
	v_bfe_u32 v152, v136, 16, 1
	v_add3_u32 v152, v136, v152, s55
	v_bfe_u32 v153, v137, 16, 1
	v_lshrrev_b32_e32 v152, 16, v152
	v_add3_u32 v153, v137, v153, s55
	v_and_or_b32 v152, v153, s53, v152
	v_bfe_u32 v153, v134, 16, 1
	v_add3_u32 v153, v134, v153, s55
	v_bfe_u32 v154, v135, 16, 1
	v_lshrrev_b32_e32 v153, 16, v153
	v_add3_u32 v154, v135, v154, s55
	v_pk_fma_f32 v[98:99], v[20:21], v[98:99], v[28:29]
	v_and_or_b32 v153, v154, s53, v153
; #define LAS __attribute__((address_space(3)))
; __device__ __forceinline__ unsigned f2bf(float f) { unsigned u = __builtin_bit_cast(unsigned, f); return (u + 0x7fffu + ((u >> 16) & 1u)) >> 16; }
; __device__ __forceinline__ unsigned pk2(float lo, float hi) { return f2bf(lo) | (f2bf(hi) << 16); }
; __device__ __forceinline__ unsigned q8x4(float a, float b, float c, float d, float s) { return q8_(a, s) | (q8_(b, s) << 8) | (q8_(c, s) << 16) | (q8_(d, s) << 24); }
; __device__ __forceinline__ void store_row_fp8(const f32x4 (&v)[4], unsigned char* o8, int lane) {
; #pragma unroll
;     for (int j = 0; j < 4; ++j) *(unsigned*)(o8 + 4 * lane + 256 * j) = q8x4(v[j][0], v[j][1], v[j][2], v[j][3], QS_H);
; }
; __global__ void __launch_bounds__(NWAVES * 64, 2) fwd(Args args) {
;     ...
;                         ln_rows_pre(v, aff1); store_row_f32_bf16(v, nullptr, H1 + (size_t)(m0 + tk) * D, lane); store_row_fp8(v, (unsigned char*)H1B + (size_t)(m0 + tk) * D, lane);
; #pragma unroll
;                         for (int j = 0; j < 4; ++j) { unsigned hh[4]; float rr[4];
; #pragma unroll
;                             for (int q = 0; q < 4; ++q) { hh[q] = f2bf(v[j][q]); rr[q] = v[j][q] - __builtin_bit_cast(float, hh[q] << 16); }
;                             const int o_ = (2 * wave + tk) * HP + (4 * lane + 256 * j) * 2;
;                             *(LAS v2u*)(hhi + o_) = (v2u){hh[0] | (hh[1] << 16), hh[2] | (hh[3] << 16)}; *(LAS v2u*)(hlo + o_) = (v2u){pk2(rr[0], rr[1]), pk2(rr[2], rr[3])}; } }
	global_store_dwordx2 v[150:151], v[152:153], off offset:1024
	v_bfe_u32 v152, v98, 16, 1
	v_add3_u32 v152, v98, v152, s55
	v_bfe_u32 v153, v99, 16, 1
	v_pk_fma_f32 v[96:97], v[22:23], v[96:97], v[30:31]
	v_lshrrev_b32_e32 v152, 16, v152
	v_add3_u32 v153, v99, v153, s55
	v_and_or_b32 v152, v153, s53, v152
	v_bfe_u32 v153, v96, 16, 1
	v_add3_u32 v153, v96, v153, s55
	v_bfe_u32 v154, v97, 16, 1
	v_lshrrev_b32_e32 v153, 16, v153
	v_add3_u32 v154, v97, v154, s55
	v_and_or_b32 v153, v154, s53, v153
	global_store_dwordx2 v[150:151], v[152:153], off offset:1536
	v_mul_f32_e32 v153, 0x41cb3333, v165
	v_mul_f32_e32 v152, 0x41cb3333, v164
	v_med3_f32 v153, v153, s54, v213
	v_mul_f32_e32 v154, 0x41cb3333, v160
	v_mul_f32_e32 v155, 0x41cb3333, v161
	v_med3_f32 v152, v152, s54, v213
	v_rndne_f32_e32 v153, v153
	v_med3_f32 v154, v154, s54, v213
	v_med3_f32 v155, v155, s54, v213
	v_rndne_f32_e32 v152, v152
	v_cvt_i32_f32_e32 v153, v153
	v_rndne_f32_e32 v154, v154
	v_rndne_f32_e32 v155, v155
	v_cvt_i32_f32_e32 v152, v152
	v_cvt_i32_f32_sdwa v154, v154 dst_sel:WORD_1 dst_unused:UNUSED_PAD src0_sel:DWORD
	v_cvt_i32_f32_e32 v155, v155
	v_lshlrev_b32_e32 v153, 8, v153
	v_and_b32_e32 v153, 0xff00, v153
	v_and_b32_e32 v154, 0xff0000, v154
	v_perm_b32 v152, v155, v152, s65
	v_lshl_add_u64 v[150:151], v[110:111], 0, s[24:25]
	v_or3_b32 v152, v152, v153, v154
	v_mul_f32_e32 v153, 0x41cb3333, v163
	global_store_dword v[150:151], v152, off
	v_mul_f32_e32 v152, 0x41cb3333, v162
	v_med3_f32 v153, v153, s54, v213
	v_mul_f32_e32 v154, 0x41cb3333, v138
	v_mul_f32_e32 v155, 0x41cb3333, v139
	v_med3_f32 v152, v152, s54, v213
	v_rndne_f32_e32 v153, v153
	v_med3_f32 v154, v154, s54, v213
	v_med3_f32 v155, v155, s54, v213
	v_rndne_f32_e32 v152, v152
	v_cvt_i32_f32_e32 v153, v153
	v_rndne_f32_e32 v154, v154
	v_rndne_f32_e32 v155, v155
	v_cvt_i32_f32_e32 v152, v152
	v_cvt_i32_f32_sdwa v154, v154 dst_sel:WORD_1 dst_unused:UNUSED_PAD src0_sel:DWORD
	v_cvt_i32_f32_e32 v155, v155
	v_lshlrev_b32_e32 v153, 8, v153
	v_and_b32_e32 v153, 0xff00, v153
	v_and_b32_e32 v154, 0xff0000, v154
	v_perm_b32 v152, v155, v152, s65
	v_or3_b32 v152, v152, v153, v154
	v_mul_f32_e32 v153, 0x41cb3333, v137
	global_store_dword v[150:151], v152, off offset:256
	v_mul_f32_e32 v152, 0x41cb3333, v136
	v_med3_f32 v153, v153, s54, v213
	v_mul_f32_e32 v154, 0x41cb3333, v134
	v_mul_f32_e32 v155, 0x41cb3333, v135
	v_med3_f32 v152, v152, s54, v213
	v_rndne_f32_e32 v153, v153
	v_med3_f32 v154, v154, s54, v213
	v_med3_f32 v155, v155, s54, v213
	v_rndne_f32_e32 v152, v152
	v_cvt_i32_f32_e32 v153, v153
	v_rndne_f32_e32 v154, v154
	v_rndne_f32_e32 v155, v155
	v_cvt_i32_f32_e32 v152, v152
	v_cvt_i32_f32_sdwa v154, v154 dst_sel:WORD_1 dst_unused:UNUSED_PAD src0_sel:DWORD
	v_cvt_i32_f32_e32 v155, v155
	v_lshlrev_b32_e32 v153, 8, v153
	v_and_b32_e32 v153, 0xff00, v153
	v_and_b32_e32 v154, 0xff0000, v154
	v_perm_b32 v152, v155, v152, s65
	v_or3_b32 v152, v152, v153, v154
	v_mul_f32_e32 v153, 0x41cb3333, v99
	global_store_dword v[150:151], v152, off offset:512
	v_mul_f32_e32 v152, 0x41cb3333, v98
	v_med3_f32 v153, v153, s54, v213
	v_mul_f32_e32 v154, 0x41cb3333, v96
	v_mul_f32_e32 v155, 0x41cb3333, v97
	v_med3_f32 v152, v152, s54, v213
	v_rndne_f32_e32 v153, v153
	v_med3_f32 v154, v154, s54, v213
	v_med3_f32 v155, v155, s54, v213
	v_rndne_f32_e32 v152, v152
	v_cvt_i32_f32_e32 v153, v153
	v_rndne_f32_e32 v154, v154
	v_rndne_f32_e32 v155, v155
	v_cvt_i32_f32_e32 v152, v152
	v_cvt_i32_f32_sdwa v154, v154 dst_sel:WORD_1 dst_unused:UNUSED_PAD src0_sel:DWORD
	v_cvt_i32_f32_e32 v155, v155
	v_lshlrev_b32_e32 v153, 8, v153
	v_and_b32_e32 v153, 0xff00, v153
	v_and_b32_e32 v154, 0xff0000, v154
	v_perm_b32 v152, v155, v152, s65
	v_or3_b32 v152, v152, v153, v154
	global_store_dword v[150:151], v152, off offset:768
	v_and_b32_sdwa v152, v160, v248 dst_sel:DWORD dst_unused:UNUSED_PAD src0_sel:WORD_1 src1_sel:DWORD
	v_and_b32_sdwa v153, v164, v248 dst_sel:DWORD dst_unused:UNUSED_PAD src0_sel:WORD_1 src1_sel:DWORD
	v_add3_u32 v156, v160, v152, s55
	v_and_b32_sdwa v152, v161, v248 dst_sel:DWORD dst_unused:UNUSED_PAD src0_sel:WORD_1 src1_sel:DWORD
	v_add3_u32 v158, v164, v153, s55
	v_and_b32_sdwa v153, v165, v248 dst_sel:DWORD dst_unused:UNUSED_PAD src0_sel:WORD_1 src1_sel:DWORD
	v_add3_u32 v152, v161, v152, s55
	v_add3_u32 v154, v165, v153, s55
	v_and_b32_e32 v153, 0xffff0000, v152
	v_mov_b32_e32 v150, v164
	v_mov_b32_e32 v151, v160
	v_or_b32_sdwa v155, v153, v156 dst_sel:DWORD dst_unused:UNUSED_PAD src0_sel:DWORD src1_sel:WORD_1
	v_and_b32_e32 v157, 0xffff0000, v156
	v_and_b32_e32 v156, 0xffff0000, v158
	v_mov_b32_e32 v160, v165
	v_and_b32_e32 v152, 0xffff0000, v154
	v_pk_add_f32 v[150:151], v[150:151], v[156:157] neg_lo:[0,1] neg_hi:[0,1]
	v_or_b32_sdwa v154, v152, v158 dst_sel:DWORD dst_unused:UNUSED_PAD src0_sel:DWORD src1_sel:WORD_1
	v_pk_add_f32 v[152:153], v[160:161], v[152:153] neg_lo:[0,1] neg_hi:[0,1]
	v_and_b32_sdwa v156, v151, v248 dst_sel:DWORD dst_unused:UNUSED_PAD src0_sel:WORD_1 src1_sel:DWORD
	v_and_b32_sdwa v157, v150, v248 dst_sel:DWORD dst_unused:UNUSED_PAD src0_sel:WORD_1 src1_sel:DWORD
	v_add3_u32 v150, v150, v157, s55
	v_add3_u32 v151, v151, v156, s55
	v_and_b32_sdwa v156, v153, v248 dst_sel:DWORD dst_unused:UNUSED_PAD src0_sel:WORD_1 src1_sel:DWORD
	v_and_b32_sdwa v157, v152, v248 dst_sel:DWORD dst_unused:UNUSED_PAD src0_sel:WORD_1 src1_sel:DWORD
	v_add3_u32 v153, v153, v156, s55
	v_add3_u32 v152, v152, v157, s55
	v_and_b32_sdwa v156, v138, v248 dst_sel:DWORD dst_unused:UNUSED_PAD src0_sel:WORD_1 src1_sel:DWORD
	v_and_b32_sdwa v157, v162, v248 dst_sel:DWORD dst_unused:UNUSED_PAD src0_sel:WORD_1 src1_sel:DWORD
; #define LAS __attribute__((address_space(3)))
; __device__ __forceinline__ unsigned f2bf(float f) { unsigned u = __builtin_bit_cast(unsigned, f); return (u + 0x7fffu + ((u >> 16) & 1u)) >> 16; }
; __device__ __forceinline__ unsigned pk2(float lo, float hi) { return f2bf(lo) | (f2bf(hi) << 16); }
; __global__ void __launch_bounds__(NWAVES * 64, 2) fwd(Args args) {
;     ...
;                         for (int j = 0; j < 4; ++j) { unsigned hh[4]; float rr[4];
; #pragma unroll
;                             for (int q = 0; q < 4; ++q) { hh[q] = f2bf(v[j][q]); rr[q] = v[j][q] - __builtin_bit_cast(float, hh[q] << 16); }
;                             const int o_ = (2 * wave + tk) * HP + (4 * lane + 256 * j) * 2;
;                             *(LAS v2u*)(hhi + o_) = (v2u){hh[0] | (hh[1] << 16), hh[2] | (hh[3] << 16)}; *(LAS v2u*)(hlo + o_) = (v2u){pk2(rr[0], rr[1]), pk2(rr[2], rr[3])}; } }
;                     if (rd + 1 < 4) {
; #pragma unroll
;                         for (int tk = 0; tk < 2; ++tk)
; #pragma unroll
;                             for (int j = 0; j < 4; ++j) raw[tk][j] = *(const v2u*)(Vf + (size_t)(m0 + 16 + tk) * D + 4 * lane + 256 * j); }
	v_add3_u32 v160, v138, v156, s55
	v_add3_u32 v161, v162, v157, s55
	v_and_b32_sdwa v156, v139, v248 dst_sel:DWORD dst_unused:UNUSED_PAD src0_sel:WORD_1 src1_sel:DWORD
	v_and_b32_sdwa v157, v163, v248 dst_sel:DWORD dst_unused:UNUSED_PAD src0_sel:WORD_1 src1_sel:DWORD
	v_add3_u32 v156, v139, v156, s55
	v_add3_u32 v158, v163, v157, s55
	v_and_b32_e32 v152, 0xffff0000, v152
	v_and_b32_e32 v157, 0xffff0000, v156
	v_and_b32_e32 v156, 0xffff0000, v158
	v_and_b32_e32 v153, 0xffff0000, v153
	v_or_b32_sdwa v150, v152, v150 dst_sel:DWORD dst_unused:UNUSED_PAD src0_sel:DWORD src1_sel:WORD_1
	v_mov_b32_e32 v152, v162
	v_or_b32_sdwa v159, v157, v160 dst_sel:DWORD dst_unused:UNUSED_PAD src0_sel:DWORD src1_sel:WORD_1
	v_or_b32_sdwa v158, v156, v161 dst_sel:DWORD dst_unused:UNUSED_PAD src0_sel:DWORD src1_sel:WORD_1
	v_add_u32_e32 v162, 16, v147
	v_or_b32_sdwa v151, v153, v151 dst_sel:DWORD dst_unused:UNUSED_PAD src0_sel:DWORD src1_sel:WORD_1
	v_mov_b32_e32 v153, v138
	ds_write2st64_b64 v162, v[154:155], v[158:159] offset0:4 offset1:5
	v_and_b32_e32 v155, 0xffff0000, v160
	v_and_b32_e32 v154, 0xffff0000, v161
	v_mov_b32_e32 v138, v163
	v_pk_add_f32 v[152:153], v[152:153], v[154:155] neg_lo:[0,1] neg_hi:[0,1]
	v_pk_add_f32 v[138:139], v[138:139], v[156:157] neg_lo:[0,1] neg_hi:[0,1]
	v_and_b32_sdwa v154, v153, v248 dst_sel:DWORD dst_unused:UNUSED_PAD src0_sel:WORD_1 src1_sel:DWORD
	v_and_b32_sdwa v155, v152, v248 dst_sel:DWORD dst_unused:UNUSED_PAD src0_sel:WORD_1 src1_sel:DWORD
	v_add3_u32 v152, v152, v155, s55
	v_add3_u32 v153, v153, v154, s55
	v_and_b32_sdwa v154, v139, v248 dst_sel:DWORD dst_unused:UNUSED_PAD src0_sel:WORD_1 src1_sel:DWORD
	v_and_b32_sdwa v155, v138, v248 dst_sel:DWORD dst_unused:UNUSED_PAD src0_sel:WORD_1 src1_sel:DWORD
	v_add3_u32 v139, v139, v154, s55
	v_add3_u32 v138, v138, v155, s55
	v_and_b32_e32 v139, 0xffff0000, v139
	v_and_b32_e32 v138, 0xffff0000, v138
	v_or_b32_sdwa v139, v139, v153 dst_sel:DWORD dst_unused:UNUSED_PAD src0_sel:DWORD src1_sel:WORD_1
	v_or_b32_sdwa v138, v138, v152 dst_sel:DWORD dst_unused:UNUSED_PAD src0_sel:DWORD src1_sel:WORD_1
	v_add_u32_e32 v154, 0x110, v147
	ds_write2st64_b64 v154, v[150:151], v[138:139] offset0:68 offset1:69
	v_and_b32_sdwa v151, v136, v248 dst_sel:DWORD dst_unused:UNUSED_PAD src0_sel:WORD_1 src1_sel:DWORD
	v_mov_b32_e32 v138, v136
	v_and_b32_sdwa v150, v134, v248 dst_sel:DWORD dst_unused:UNUSED_PAD src0_sel:WORD_1 src1_sel:DWORD
	v_add3_u32 v155, v136, v151, s55
	v_and_b32_sdwa v136, v135, v248 dst_sel:DWORD dst_unused:UNUSED_PAD src0_sel:WORD_1 src1_sel:DWORD
	v_add3_u32 v152, v134, v150, s55
	v_and_b32_sdwa v150, v137, v248 dst_sel:DWORD dst_unused:UNUSED_PAD src0_sel:WORD_1 src1_sel:DWORD
	v_add3_u32 v136, v135, v136, s55
	v_mov_b32_e32 v139, v134
	v_mov_b32_e32 v134, v137
	v_add3_u32 v150, v137, v150, s55
	v_and_b32_e32 v137, 0xffff0000, v136
	v_or_b32_sdwa v151, v137, v152 dst_sel:DWORD dst_unused:UNUSED_PAD src0_sel:DWORD src1_sel:WORD_1
	v_and_b32_e32 v153, 0xffff0000, v152
	v_and_b32_e32 v152, 0xffff0000, v155
	v_and_b32_e32 v136, 0xffff0000, v150
	v_pk_add_f32 v[138:139], v[138:139], v[152:153] neg_lo:[0,1] neg_hi:[0,1]
	v_pk_add_f32 v[134:135], v[134:135], v[136:137] neg_lo:[0,1] neg_hi:[0,1]
	v_and_b32_sdwa v137, v138, v248 dst_sel:DWORD dst_unused:UNUSED_PAD src0_sel:WORD_1 src1_sel:DWORD
	v_or_b32_sdwa v150, v136, v155 dst_sel:DWORD dst_unused:UNUSED_PAD src0_sel:DWORD src1_sel:WORD_1
	v_and_b32_sdwa v136, v139, v248 dst_sel:DWORD dst_unused:UNUSED_PAD src0_sel:WORD_1 src1_sel:DWORD
	v_add3_u32 v137, v138, v137, s55
	v_and_b32_sdwa v138, v135, v248 dst_sel:DWORD dst_unused:UNUSED_PAD src0_sel:WORD_1 src1_sel:DWORD
	v_add3_u32 v136, v139, v136, s55
	v_and_b32_sdwa v139, v134, v248 dst_sel:DWORD dst_unused:UNUSED_PAD src0_sel:WORD_1 src1_sel:DWORD
	v_add3_u32 v135, v135, v138, s55
	v_add3_u32 v134, v134, v139, s55
	v_and_b32_e32 v135, 0xffff0000, v135
	v_and_b32_sdwa v138, v96, v248 dst_sel:DWORD dst_unused:UNUSED_PAD src0_sel:WORD_1 src1_sel:DWORD
	v_and_b32_sdwa v139, v98, v248 dst_sel:DWORD dst_unused:UNUSED_PAD src0_sel:WORD_1 src1_sel:DWORD
	v_or_b32_sdwa v135, v135, v136 dst_sel:DWORD dst_unused:UNUSED_PAD src0_sel:DWORD src1_sel:WORD_1
	v_mov_b32_e32 v136, v98
	v_add3_u32 v152, v96, v138, s55
	v_add3_u32 v153, v98, v139, s55
	v_and_b32_sdwa v98, v97, v248 dst_sel:DWORD dst_unused:UNUSED_PAD src0_sel:WORD_1 src1_sel:DWORD
	v_and_b32_sdwa v138, v99, v248 dst_sel:DWORD dst_unused:UNUSED_PAD src0_sel:WORD_1 src1_sel:DWORD
	v_and_b32_e32 v134, 0xffff0000, v134
	v_add3_u32 v98, v97, v98, s55
	v_add3_u32 v138, v99, v138, s55
	v_or_b32_sdwa v134, v134, v137 dst_sel:DWORD dst_unused:UNUSED_PAD src0_sel:DWORD src1_sel:WORD_1
	v_mov_b32_e32 v137, v96
	v_mov_b32_e32 v96, v99
	v_and_b32_e32 v99, 0xffff0000, v98
	v_and_b32_e32 v98, 0xffff0000, v138
	v_or_b32_sdwa v139, v99, v152 dst_sel:DWORD dst_unused:UNUSED_PAD src0_sel:DWORD src1_sel:WORD_1
	v_or_b32_sdwa v138, v98, v153 dst_sel:DWORD dst_unused:UNUSED_PAD src0_sel:DWORD src1_sel:WORD_1
	ds_write2st64_b64 v162, v[150:151], v[138:139] offset0:6 offset1:7
	v_and_b32_e32 v139, 0xffff0000, v152
	v_and_b32_e32 v138, 0xffff0000, v153
	v_pk_add_f32 v[136:137], v[136:137], v[138:139] neg_lo:[0,1] neg_hi:[0,1]
	v_pk_add_f32 v[96:97], v[96:97], v[98:99] neg_lo:[0,1] neg_hi:[0,1]
	v_and_b32_sdwa v98, v137, v248 dst_sel:DWORD dst_unused:UNUSED_PAD src0_sel:WORD_1 src1_sel:DWORD
	v_and_b32_sdwa v99, v136, v248 dst_sel:DWORD dst_unused:UNUSED_PAD src0_sel:WORD_1 src1_sel:DWORD
	v_add3_u32 v99, v136, v99, s55
	v_add3_u32 v98, v137, v98, s55
	v_and_b32_sdwa v136, v97, v248 dst_sel:DWORD dst_unused:UNUSED_PAD src0_sel:WORD_1 src1_sel:DWORD
	v_and_b32_sdwa v137, v96, v248 dst_sel:DWORD dst_unused:UNUSED_PAD src0_sel:WORD_1 src1_sel:DWORD
	v_add3_u32 v97, v97, v136, s55
	v_add3_u32 v96, v96, v137, s55
	v_and_b32_e32 v97, 0xffff0000, v97
	v_and_b32_e32 v96, 0xffff0000, v96
	v_or_b32_sdwa v97, v97, v98 dst_sel:DWORD dst_unused:UNUSED_PAD src0_sel:DWORD src1_sel:WORD_1
	v_or_b32_sdwa v96, v96, v99 dst_sel:DWORD dst_unused:UNUSED_PAD src0_sel:DWORD src1_sel:WORD_1
	s_cmp_eq_u32 s19, 3
	ds_write2st64_b64 v154, v[134:135], v[96:97] offset0:70 offset1:71
	s_cbranch_scc1 .LBB0_3068
	v_lshl_add_u64 v[96:97], v[102:103], 0, s[20:21]
	s_mov_b64 s[12:13], 0x8000
	v_add_co_u32_e32 v124, vcc, 0x8000, v96
	v_lshl_add_u64 v[98:99], v[96:97], 0, s[12:13]
	s_nop 0
	v_addc_co_u32_e32 v125, vcc, 0, v97, vcc
	s_mov_b64 s[12:13], 0x8800
	global_load_dwordx2 v[116:117], v[124:125], off
	global_load_dwordx2 v[118:119], v[98:99], off offset:512
	global_load_dwordx2 v[120:121], v[98:99], off offset:1024
	global_load_dwordx2 v[122:123], v[98:99], off offset:1536
	v_lshl_add_u64 v[96:97], v[96:97], 0, s[12:13]
	global_load_dwordx2 v[124:125], v[124:125], off offset:2048
	s_nop 0
	global_load_dwordx2 v[126:127], v[96:97], off offset:512
	global_load_dwordx2 v[130:131], v[96:97], off offset:1024
	global_load_dwordx2 v[132:133], v[96:97], off offset:1536

; #define LAS __attribute__((address_space(3)))
; __device__ __forceinline__ int lane_op() { int l = (int)__builtin_amdgcn_mbcnt_hi(~0u, __builtin_amdgcn_mbcnt_lo(~0u, 0u)); asm volatile("" : "+v"(l)); return l; }
; #define SHX(v, m, l) bperm_((l) ^ (m), (v))
; __global__ void __launch_bounds__(NWAVES * 64, 2) fwd(Args args) {
;     ...
;                     const int eq = lane & 7; const int lopr_ = lane_op(); const f32x4 be4 = *(const f32x4*)(brt + 4 * eq);
; #pragma unroll 1
;                     for (int tk = 0; tk < 2; ++tk) { float cur[4] = {be4[0], be4[1], be4[2], be4[3]};
; #pragma unroll
;                         for (int w = 0; w < 8; ++w) { const f32x4 p = *(const LAS f32x4*)(part + (w * 16 + 2 * wave + tk) * 32 + 4 * eq);
; #pragma unroll
;                             for (int j = 0; j < 4; ++j) cur[j] += p[j]; }
;                         float val[4]; int idx[4];
; #pragma unroll
;                         for (int k = 0; k < 4; ++k) { float bv = cur[0]; int bi = 4 * eq;
; #pragma unroll
;                             for (int j = 1; j < 4; ++j) if (cur[j] > bv) { bv = cur[j]; bi = 4 * eq + j; }
; #pragma unroll
;                             for (int o = 1; o < 8; o <<= 1) { const float ov = SHX(bv, o, lopr_); const int oi = SHX(bi, o, lopr_); if (ov > bv || (ov == bv && oi < bi)) { bv = ov; bi = oi; } }
.LBB0_3070:
	s_or_b32 s12, s35, s46
	v_lshl_add_u32 v134, s12, 7, v141
	ds_read_b128 v[150:153], v134
	s_waitcnt vmcnt(0) lgkmcnt(0)
	v_add_f32_e32 v135, v152, v98
	v_add_f32_e32 v139, v153, v99
	ds_read_b128 v[152:155], v134 offset:2048
	s_waitcnt lgkmcnt(0)
	v_add_f32_e32 v135, v154, v135
	v_add_f32_e32 v139, v155, v139
	ds_read_b128 v[154:157], v134 offset:4096
	s_waitcnt lgkmcnt(0)
	v_add_f32_e32 v135, v156, v135
	v_add_f32_e32 v139, v157, v139
	ds_read_b128 v[156:159], v134 offset:6144
	s_waitcnt lgkmcnt(0)
	v_add_f32_e32 v135, v158, v135
	v_add_f32_e32 v139, v159, v139
	ds_read_b128 v[158:161], v134 offset:8192
	s_waitcnt lgkmcnt(0)
	v_add_f32_e32 v135, v160, v135
	v_add_f32_e32 v139, v161, v139
	ds_read_b128 v[160:163], v134 offset:10240
	s_waitcnt lgkmcnt(0)
	v_add_f32_e32 v135, v162, v135
	v_add_f32_e32 v139, v163, v139
	ds_read_b128 v[162:165], v134 offset:12288
	s_waitcnt lgkmcnt(0)
	v_add_f32_e32 v168, v164, v135
	v_add_f32_e32 v139, v165, v139
	ds_read_b128 v[164:167], v134 offset:14336
	v_pk_add_f32 v[134:135], v[150:151], v[96:97]
	s_waitcnt lgkmcnt(0)
	v_add_f32_e32 v151, v167, v139
	v_pk_add_f32 v[134:135], v[152:153], v[134:135]
	v_add_f32_e32 v152, v166, v168
	v_pk_add_f32 v[134:135], v[154:155], v[134:135]
	s_nop 0
	v_pk_add_f32 v[134:135], v[156:157], v[134:135]
	s_nop 0
	v_pk_add_f32 v[134:135], v[158:159], v[134:135]
	s_nop 0
	v_pk_add_f32 v[134:135], v[160:161], v[134:135]
	s_nop 0
	v_pk_add_f32 v[134:135], v[162:163], v[134:135]
	s_nop 0
	v_pk_add_f32 v[134:135], v[164:165], v[134:135]
	s_nop 0
	v_cmp_gt_f32_e32 vcc, v135, v134
	s_nop 1
	v_cndmask_b32_e32 v150, v134, v135, vcc
	v_cndmask_b32_e32 v139, v106, v101, vcc
	v_cmp_gt_f32_e32 vcc, v152, v150
	s_nop 1
	v_cndmask_b32_e32 v150, v150, v152, vcc
	v_cndmask_b32_e32 v139, v139, v145, vcc
	v_cmp_gt_f32_e32 vcc, v151, v150
	s_nop 1
	v_cndmask_b32_e32 v150, v150, v151, vcc
	v_cndmask_b32_e32 v139, v139, v146, vcc
	s_nop 1
	v_mov_b32_dpp v153, v150 quad_perm:[1,0,3,2] row_mask:0xf bank_mask:0xf
	s_nop 1
	v_mov_b32_dpp v154, v139 quad_perm:[1,0,3,2] row_mask:0xf bank_mask:0xf
	s_waitcnt lgkmcnt(1)
	v_cmp_lt_f32_e64 s[24:25], v150, v153
	v_cmp_nlt_f32_e32 vcc, v150, v153
	s_and_saveexec_b64 s[26:27], vcc
	s_cbranch_execz .LBB0_3072
	v_cmp_eq_f32_e32 vcc, v150, v153
	s_waitcnt lgkmcnt(0)
	v_cmp_lt_i32_e64 s[12:13], v154, v139
	s_and_b64 s[12:13], vcc, s[12:13]
	s_andn2_b64 s[24:25], s[24:25], exec
	s_and_b64 s[12:13], s[12:13], exec
	s_or_b64 s[24:25], s[24:25], s[12:13]

; #define SHX(v, m, l) bperm_((l) ^ (m), (v))
; __global__ void __launch_bounds__(NWAVES * 64, 2) fwd(Args args) {
;     ...
;                         for (int k = 0; k < 4; ++k) { float bv = cur[0]; int bi = 4 * eq;
; #pragma unroll
;                             for (int j = 1; j < 4; ++j) if (cur[j] > bv) { bv = cur[j]; bi = 4 * eq + j; }
; #pragma unroll
;                             for (int o = 1; o < 8; o <<= 1) { const float ov = SHX(bv, o, lopr_); const int oi = SHX(bi, o, lopr_); if (ov > bv || (ov == bv && oi < bi)) { bv = ov; bi = oi; } }
.LBB0_3074:
	s_or_b64 exec, exec, s[12:13]
	s_nop 1
	v_mov_b32_dpp v153, v150 quad_perm:[2,3,0,1] row_mask:0xf bank_mask:0xf
	s_waitcnt lgkmcnt(1)
	s_nop 1
	v_mov_b32_dpp v154, v139 quad_perm:[2,3,0,1] row_mask:0xf bank_mask:0xf
	s_waitcnt lgkmcnt(1)
	v_cmp_lt_f32_e64 s[24:25], v150, v153
	v_cmp_nlt_f32_e32 vcc, v150, v153
	s_and_saveexec_b64 s[26:27], vcc
	s_cbranch_execz .LBB0_3076
	v_cmp_eq_f32_e32 vcc, v150, v153
	s_waitcnt lgkmcnt(0)
	v_cmp_lt_i32_e64 s[12:13], v154, v139
	s_and_b64 s[12:13], vcc, s[12:13]
	s_andn2_b64 s[24:25], s[24:25], exec
	s_and_b64 s[12:13], s[12:13], exec
	s_or_b64 s[24:25], s[24:25], s[12:13]

; #define SHX(v, m, l) bperm_((l) ^ (m), (v))
; __global__ void __launch_bounds__(NWAVES * 64, 2) fwd(Args args) {
;     ...
;                         for (int k = 0; k < 4; ++k) { float bv = cur[0]; int bi = 4 * eq;
; #pragma unroll
;                             for (int j = 1; j < 4; ++j) if (cur[j] > bv) { bv = cur[j]; bi = 4 * eq + j; }
; #pragma unroll
;                             for (int o = 1; o < 8; o <<= 1) { const float ov = SHX(bv, o, lopr_); const int oi = SHX(bi, o, lopr_); if (ov > bv || (ov == bv && oi < bi)) { bv = ov; bi = oi; } }
.LBB0_3078:
	s_or_b64 exec, exec, s[12:13]
	s_nop 1
	v_mov_b32_dpp v153, v150 row_half_mirror row_mask:0xf bank_mask:0xf
	s_waitcnt lgkmcnt(1)
	s_nop 1
	v_mov_b32_dpp v154, v139 row_half_mirror row_mask:0xf bank_mask:0xf
	s_waitcnt lgkmcnt(1)
	v_cmp_lt_f32_e64 s[24:25], v150, v153
	v_cmp_nlt_f32_e32 vcc, v150, v153
	s_and_saveexec_b64 s[26:27], vcc
	s_cbranch_execz .LBB0_3080
	v_cmp_eq_f32_e32 vcc, v150, v153
	s_waitcnt lgkmcnt(0)
	v_cmp_lt_i32_e64 s[12:13], v154, v139
	s_and_b64 s[12:13], vcc, s[12:13]
	s_andn2_b64 s[24:25], s[24:25], exec
	s_and_b64 s[12:13], s[12:13], exec
	s_or_b64 s[24:25], s[24:25], s[12:13]

; #define SHX(v, m, l) bperm_((l) ^ (m), (v))
; __global__ void __launch_bounds__(NWAVES * 64, 2) fwd(Args args) {
;     ...
;                         for (int k = 0; k < 4; ++k) { float bv = cur[0]; int bi = 4 * eq;
; #pragma unroll
;                             for (int j = 1; j < 4; ++j) if (cur[j] > bv) { bv = cur[j]; bi = 4 * eq + j; }
; #pragma unroll
;                             for (int o = 1; o < 8; o <<= 1) { const float ov = SHX(bv, o, lopr_); const int oi = SHX(bi, o, lopr_); if (ov > bv || (ov == bv && oi < bi)) { bv = ov; bi = oi; } }
;                             val[k] = bv; idx[k] = bi;
; #pragma unroll
;                             for (int j = 0; j < 4; ++j) if (bi == 4 * eq + j) cur[j] = -INFINITY; }
.LBB0_3082:
	s_or_b64 exec, exec, s[12:13]
	v_cmp_ne_u32_e32 vcc, v139, v101
	s_nop 1
	v_cndmask_b32_e32 v153, v212, v135, vcc
	v_cmp_ne_u32_e32 vcc, v139, v106
	s_waitcnt lgkmcnt(0)
	s_nop 0
	v_cndmask_b32_e32 v154, v212, v134, vcc
	v_cmp_ne_u32_e32 vcc, v139, v145
	s_nop 1
	v_cndmask_b32_e32 v152, v212, v152, vcc
	v_cmp_ne_u32_e32 vcc, v139, v146
	s_nop 1
	v_cndmask_b32_e32 v151, v212, v151, vcc
	v_cmp_gt_f32_e32 vcc, v153, v154
	s_nop 1
	v_cndmask_b32_e32 v135, v154, v153, vcc
	v_cndmask_b32_e32 v134, v106, v101, vcc
	v_cmp_gt_f32_e32 vcc, v152, v135
	s_nop 1
	v_cndmask_b32_e32 v135, v135, v152, vcc
	v_cndmask_b32_e32 v134, v134, v145, vcc
	v_cmp_gt_f32_e32 vcc, v151, v135
	s_nop 1
	v_cndmask_b32_e32 v135, v135, v151, vcc
	v_cndmask_b32_e32 v134, v134, v146, vcc
	s_nop 1
	v_mov_b32_dpp v155, v135 quad_perm:[1,0,3,2] row_mask:0xf bank_mask:0xf
	s_nop 1
	v_mov_b32_dpp v156, v134 quad_perm:[1,0,3,2] row_mask:0xf bank_mask:0xf
	s_waitcnt lgkmcnt(1)
	v_cmp_lt_f32_e64 s[24:25], v135, v155
	v_cmp_nlt_f32_e32 vcc, v135, v155
	s_and_saveexec_b64 s[26:27], vcc
	s_cbranch_execz .LBB0_3084
	v_cmp_eq_f32_e32 vcc, v135, v155
	s_waitcnt lgkmcnt(0)
	v_cmp_lt_i32_e64 s[12:13], v156, v134
	s_and_b64 s[12:13], vcc, s[12:13]
	s_andn2_b64 s[24:25], s[24:25], exec
	s_and_b64 s[12:13], s[12:13], exec
	s_or_b64 s[24:25], s[24:25], s[12:13]

; #define SHX(v, m, l) bperm_((l) ^ (m), (v))
; __global__ void __launch_bounds__(NWAVES * 64, 2) fwd(Args args) {
;     ...
;                         for (int k = 0; k < 4; ++k) { float bv = cur[0]; int bi = 4 * eq;
; #pragma unroll
;                             for (int j = 1; j < 4; ++j) if (cur[j] > bv) { bv = cur[j]; bi = 4 * eq + j; }
; #pragma unroll
;                             for (int o = 1; o < 8; o <<= 1) { const float ov = SHX(bv, o, lopr_); const int oi = SHX(bi, o, lopr_); if (ov > bv || (ov == bv && oi < bi)) { bv = ov; bi = oi; } }
.LBB0_3086:
	s_or_b64 exec, exec, s[12:13]
	s_nop 1
	v_mov_b32_dpp v155, v135 quad_perm:[2,3,0,1] row_mask:0xf bank_mask:0xf
	s_waitcnt lgkmcnt(1)
	s_nop 1
	v_mov_b32_dpp v156, v134 quad_perm:[2,3,0,1] row_mask:0xf bank_mask:0xf
	s_waitcnt lgkmcnt(1)
	v_cmp_lt_f32_e64 s[24:25], v135, v155
	v_cmp_nlt_f32_e32 vcc, v135, v155
	s_and_saveexec_b64 s[26:27], vcc
	s_cbranch_execz .LBB0_3088
	v_cmp_eq_f32_e32 vcc, v135, v155
	s_waitcnt lgkmcnt(0)
	v_cmp_lt_i32_e64 s[12:13], v156, v134
	s_and_b64 s[12:13], vcc, s[12:13]
	s_andn2_b64 s[24:25], s[24:25], exec
	s_and_b64 s[12:13], s[12:13], exec
	s_or_b64 s[24:25], s[24:25], s[12:13]

; #define SHX(v, m, l) bperm_((l) ^ (m), (v))
; __global__ void __launch_bounds__(NWAVES * 64, 2) fwd(Args args) {
;     ...
;                         for (int k = 0; k < 4; ++k) { float bv = cur[0]; int bi = 4 * eq;
; #pragma unroll
;                             for (int j = 1; j < 4; ++j) if (cur[j] > bv) { bv = cur[j]; bi = 4 * eq + j; }
; #pragma unroll
;                             for (int o = 1; o < 8; o <<= 1) { const float ov = SHX(bv, o, lopr_); const int oi = SHX(bi, o, lopr_); if (ov > bv || (ov == bv && oi < bi)) { bv = ov; bi = oi; } }
.LBB0_3090:
	s_or_b64 exec, exec, s[12:13]
	s_nop 1
	v_mov_b32_dpp v155, v135 row_half_mirror row_mask:0xf bank_mask:0xf
	s_waitcnt lgkmcnt(1)
	s_nop 1
	v_mov_b32_dpp v156, v134 row_half_mirror row_mask:0xf bank_mask:0xf
	s_waitcnt lgkmcnt(1)
	v_cmp_lt_f32_e64 s[24:25], v135, v155
	v_cmp_nlt_f32_e32 vcc, v135, v155
	s_and_saveexec_b64 s[26:27], vcc
	s_cbranch_execz .LBB0_3092
	v_cmp_eq_f32_e32 vcc, v135, v155
	s_waitcnt lgkmcnt(0)
	v_cmp_lt_i32_e64 s[12:13], v156, v134
	s_and_b64 s[12:13], vcc, s[12:13]
	s_andn2_b64 s[24:25], s[24:25], exec
	s_and_b64 s[12:13], s[12:13], exec
	s_or_b64 s[24:25], s[24:25], s[12:13]

; #define SHX(v, m, l) bperm_((l) ^ (m), (v))
; __global__ void __launch_bounds__(NWAVES * 64, 2) fwd(Args args) {
;     ...
;                         for (int k = 0; k < 4; ++k) { float bv = cur[0]; int bi = 4 * eq;
; #pragma unroll
;                             for (int j = 1; j < 4; ++j) if (cur[j] > bv) { bv = cur[j]; bi = 4 * eq + j; }
; #pragma unroll
;                             for (int o = 1; o < 8; o <<= 1) { const float ov = SHX(bv, o, lopr_); const int oi = SHX(bi, o, lopr_); if (ov > bv || (ov == bv && oi < bi)) { bv = ov; bi = oi; } }
;                             val[k] = bv; idx[k] = bi;
; #pragma unroll
;                             for (int j = 0; j < 4; ++j) if (bi == 4 * eq + j) cur[j] = -INFINITY; }
.LBB0_3094:
	s_or_b64 exec, exec, s[12:13]
	v_cmp_ne_u32_e32 vcc, v134, v101
	s_nop 1
	v_cndmask_b32_e32 v153, v212, v153, vcc
	v_cmp_ne_u32_e32 vcc, v134, v106
	s_waitcnt lgkmcnt(0)
	s_nop 0
	v_cndmask_b32_e32 v156, v212, v154, vcc
	v_cmp_ne_u32_e32 vcc, v134, v145
	s_nop 1
	v_cndmask_b32_e32 v154, v212, v152, vcc
	v_cmp_ne_u32_e32 vcc, v134, v146
	s_nop 1
	v_cndmask_b32_e32 v155, v212, v151, vcc
	v_cmp_gt_f32_e32 vcc, v153, v156
	s_nop 1
	v_cndmask_b32_e32 v152, v156, v153, vcc
	v_cndmask_b32_e32 v151, v106, v101, vcc
	v_cmp_gt_f32_e32 vcc, v154, v152
	s_nop 1
	v_cndmask_b32_e32 v152, v152, v154, vcc
	v_cndmask_b32_e32 v151, v151, v145, vcc
	v_cmp_gt_f32_e32 vcc, v155, v152
	s_nop 1
	v_cndmask_b32_e32 v152, v152, v155, vcc
	v_cndmask_b32_e32 v151, v151, v146, vcc
	s_nop 1
	v_mov_b32_dpp v157, v152 quad_perm:[1,0,3,2] row_mask:0xf bank_mask:0xf
	s_nop 1
	v_mov_b32_dpp v158, v151 quad_perm:[1,0,3,2] row_mask:0xf bank_mask:0xf
	s_waitcnt lgkmcnt(1)
	v_cmp_lt_f32_e64 s[24:25], v152, v157
	v_cmp_nlt_f32_e32 vcc, v152, v157
	s_and_saveexec_b64 s[26:27], vcc
	s_cbranch_execz .LBB0_3096
	v_cmp_eq_f32_e32 vcc, v152, v157
	s_waitcnt lgkmcnt(0)
	v_cmp_lt_i32_e64 s[12:13], v158, v151
	s_and_b64 s[12:13], vcc, s[12:13]
	s_andn2_b64 s[24:25], s[24:25], exec
	s_and_b64 s[12:13], s[12:13], exec
	s_or_b64 s[24:25], s[24:25], s[12:13]

; #define SHX(v, m, l) bperm_((l) ^ (m), (v))
; __global__ void __launch_bounds__(NWAVES * 64, 2) fwd(Args args) {
;     ...
;                         for (int k = 0; k < 4; ++k) { float bv = cur[0]; int bi = 4 * eq;
; #pragma unroll
;                             for (int j = 1; j < 4; ++j) if (cur[j] > bv) { bv = cur[j]; bi = 4 * eq + j; }
; #pragma unroll
;                             for (int o = 1; o < 8; o <<= 1) { const float ov = SHX(bv, o, lopr_); const int oi = SHX(bi, o, lopr_); if (ov > bv || (ov == bv && oi < bi)) { bv = ov; bi = oi; } }
.LBB0_3098:
	s_or_b64 exec, exec, s[12:13]
	s_nop 1
	v_mov_b32_dpp v157, v152 quad_perm:[2,3,0,1] row_mask:0xf bank_mask:0xf
	s_waitcnt lgkmcnt(1)
	s_nop 1
	v_mov_b32_dpp v158, v151 quad_perm:[2,3,0,1] row_mask:0xf bank_mask:0xf
	s_waitcnt lgkmcnt(1)
	v_cmp_lt_f32_e64 s[24:25], v152, v157
	v_cmp_nlt_f32_e32 vcc, v152, v157
	s_and_saveexec_b64 s[26:27], vcc
	s_cbranch_execz .LBB0_3100
	v_cmp_eq_f32_e32 vcc, v152, v157
	s_waitcnt lgkmcnt(0)
	v_cmp_lt_i32_e64 s[12:13], v158, v151
	s_and_b64 s[12:13], vcc, s[12:13]
	s_andn2_b64 s[24:25], s[24:25], exec
	s_and_b64 s[12:13], s[12:13], exec
	s_or_b64 s[24:25], s[24:25], s[12:13]

; #define SHX(v, m, l) bperm_((l) ^ (m), (v))
; __global__ void __launch_bounds__(NWAVES * 64, 2) fwd(Args args) {
;     ...
;                         for (int k = 0; k < 4; ++k) { float bv = cur[0]; int bi = 4 * eq;
; #pragma unroll
;                             for (int j = 1; j < 4; ++j) if (cur[j] > bv) { bv = cur[j]; bi = 4 * eq + j; }
; #pragma unroll
;                             for (int o = 1; o < 8; o <<= 1) { const float ov = SHX(bv, o, lopr_); const int oi = SHX(bi, o, lopr_); if (ov > bv || (ov == bv && oi < bi)) { bv = ov; bi = oi; } }
.LBB0_3102:
	s_or_b64 exec, exec, s[12:13]
	s_nop 1
	v_mov_b32_dpp v157, v152 row_half_mirror row_mask:0xf bank_mask:0xf
	s_waitcnt lgkmcnt(1)
	s_nop 1
	v_mov_b32_dpp v158, v151 row_half_mirror row_mask:0xf bank_mask:0xf
	s_waitcnt lgkmcnt(1)
	v_cmp_lt_f32_e64 s[24:25], v152, v157
	v_cmp_nlt_f32_e32 vcc, v152, v157
	s_and_saveexec_b64 s[26:27], vcc
	s_cbranch_execz .LBB0_3104
	v_cmp_eq_f32_e32 vcc, v152, v157
	s_waitcnt lgkmcnt(0)
	v_cmp_lt_i32_e64 s[12:13], v158, v151
	s_and_b64 s[12:13], vcc, s[12:13]
	s_andn2_b64 s[24:25], s[24:25], exec
	s_and_b64 s[12:13], s[12:13], exec
	s_or_b64 s[24:25], s[24:25], s[12:13]

; #define SHX(v, m, l) bperm_((l) ^ (m), (v))
; __global__ void __launch_bounds__(NWAVES * 64, 2) fwd(Args args) {
;     ...
;                         for (int k = 0; k < 4; ++k) { float bv = cur[0]; int bi = 4 * eq;
; #pragma unroll
;                             for (int j = 1; j < 4; ++j) if (cur[j] > bv) { bv = cur[j]; bi = 4 * eq + j; }
; #pragma unroll
;                             for (int o = 1; o < 8; o <<= 1) { const float ov = SHX(bv, o, lopr_); const int oi = SHX(bi, o, lopr_); if (ov > bv || (ov == bv && oi < bi)) { bv = ov; bi = oi; } }
;                             val[k] = bv; idx[k] = bi;
; #pragma unroll
;                             for (int j = 0; j < 4; ++j) if (bi == 4 * eq + j) cur[j] = -INFINITY; }
.LBB0_3106:
	s_or_b64 exec, exec, s[12:13]
	v_cmp_ne_u32_e32 vcc, v151, v106
	s_nop 1
	v_cndmask_b32_e32 v156, v212, v156, vcc
	v_cmp_ne_u32_e32 vcc, v151, v101
	s_nop 1
	v_cndmask_b32_e32 v153, v212, v153, vcc
	v_cmp_ne_u32_e32 vcc, v151, v145
	s_nop 1
	v_cndmask_b32_e32 v154, v212, v154, vcc
	v_cmp_ne_u32_e32 vcc, v151, v146
	s_nop 1
	v_cndmask_b32_e32 v155, v212, v155, vcc
	v_cmp_gt_f32_e32 vcc, v153, v156
	s_nop 1
	v_cndmask_b32_e32 v153, v156, v153, vcc
	v_cndmask_b32_e32 v157, v106, v101, vcc
	v_cmp_gt_f32_e32 vcc, v154, v153
	s_nop 1
	v_cndmask_b32_e32 v154, v153, v154, vcc
	v_cndmask_b32_e32 v156, v157, v145, vcc
	v_cmp_gt_f32_e32 vcc, v155, v154
	s_nop 1
	v_cndmask_b32_e32 v154, v154, v155, vcc
	v_cndmask_b32_e32 v153, v156, v146, vcc
	s_nop 1
	v_mov_b32_dpp v155, v154 quad_perm:[1,0,3,2] row_mask:0xf bank_mask:0xf
	s_nop 1
	v_mov_b32_dpp v156, v153 quad_perm:[1,0,3,2] row_mask:0xf bank_mask:0xf
	s_waitcnt lgkmcnt(1)
	v_cmp_lt_f32_e64 s[24:25], v154, v155
	v_cmp_nlt_f32_e32 vcc, v154, v155
	s_and_saveexec_b64 s[26:27], vcc
	s_cbranch_execz .LBB0_3108
	v_cmp_eq_f32_e32 vcc, v154, v155
	s_waitcnt lgkmcnt(0)
	v_cmp_lt_i32_e64 s[12:13], v156, v153
	s_and_b64 s[12:13], vcc, s[12:13]
	s_andn2_b64 s[24:25], s[24:25], exec
	s_and_b64 s[12:13], s[12:13], exec
	s_or_b64 s[24:25], s[24:25], s[12:13]

; #define SHX(v, m, l) bperm_((l) ^ (m), (v))
; __global__ void __launch_bounds__(NWAVES * 64, 2) fwd(Args args) {
;     ...
;                         for (int k = 0; k < 4; ++k) { float bv = cur[0]; int bi = 4 * eq;
; #pragma unroll
;                             for (int j = 1; j < 4; ++j) if (cur[j] > bv) { bv = cur[j]; bi = 4 * eq + j; }
; #pragma unroll
;                             for (int o = 1; o < 8; o <<= 1) { const float ov = SHX(bv, o, lopr_); const int oi = SHX(bi, o, lopr_); if (ov > bv || (ov == bv && oi < bi)) { bv = ov; bi = oi; } }
;                             val[k] = bv; idx[k] = bi;
.LBB0_3110:
	s_or_b64 exec, exec, s[12:13]
	s_nop 1
	v_mov_b32_dpp v155, v154 quad_perm:[2,3,0,1] row_mask:0xf bank_mask:0xf
	s_waitcnt lgkmcnt(1)
	s_nop 1
	v_mov_b32_dpp v156, v153 quad_perm:[2,3,0,1] row_mask:0xf bank_mask:0xf
	s_waitcnt lgkmcnt(1)
	v_cmp_lt_f32_e64 s[24:25], v154, v155
	v_cmp_nlt_f32_e32 vcc, v154, v155
	s_and_saveexec_b64 s[26:27], vcc
	s_cbranch_execz .LBB0_3112
	v_cmp_eq_f32_e32 vcc, v154, v155
	s_waitcnt lgkmcnt(0)
	v_cmp_lt_i32_e64 s[12:13], v156, v153
	s_and_b64 s[12:13], vcc, s[12:13]
	s_andn2_b64 s[24:25], s[24:25], exec
	s_and_b64 s[12:13], s[12:13], exec
	s_or_b64 s[24:25], s[24:25], s[12:13]

; #define SHX(v, m, l) bperm_((l) ^ (m), (v))
; __global__ void __launch_bounds__(NWAVES * 64, 2) fwd(Args args) {
;     ...
;                         for (int k = 0; k < 4; ++k) { float bv = cur[0]; int bi = 4 * eq;
; #pragma unroll
;                             for (int j = 1; j < 4; ++j) if (cur[j] > bv) { bv = cur[j]; bi = 4 * eq + j; }
; #pragma unroll
;                             for (int o = 1; o < 8; o <<= 1) { const float ov = SHX(bv, o, lopr_); const int oi = SHX(bi, o, lopr_); if (ov > bv || (ov == bv && oi < bi)) { bv = ov; bi = oi; } }
;                             val[k] = bv; idx[k] = bi;
.LBB0_3114:
	s_or_b64 exec, exec, s[12:13]
	s_nop 1
	v_mov_b32_dpp v155, v154 row_half_mirror row_mask:0xf bank_mask:0xf
	s_waitcnt lgkmcnt(1)
	s_nop 1
	v_mov_b32_dpp v156, v153 row_half_mirror row_mask:0xf bank_mask:0xf
	s_waitcnt lgkmcnt(1)
	v_cmp_lt_f32_e64 s[24:25], v154, v155
	v_cmp_nlt_f32_e32 vcc, v154, v155
	s_and_saveexec_b64 s[26:27], vcc
	s_cbranch_execnz .LBB0_3117
	s_or_b64 exec, exec, s[26:27]
	s_and_saveexec_b64 s[12:13], s[24:25]
	s_cbranch_execnz .LBB0_3118

.LBB0_3565:
	s_waitcnt vmcnt(39)
	v_lshlrev_b32_e32 v130, 16, v40
	v_and_b32_e32 v131, 0xffff0000, v40
	v_lshlrev_b32_e32 v132, 16, v41
	v_and_b32_e32 v133, 0xffff0000, v41
	s_waitcnt vmcnt(35)
	v_lshlrev_b32_e32 v40, 16, v44
	v_and_b32_e32 v41, 0xffff0000, v44
	s_mov_b32 s0, 0x3fd744fd
	v_lshlrev_b32_e32 v44, 16, v45
	v_and_b32_e32 v45, 0xffff0000, v45
	v_pk_fma_f32 v[40:41], v[130:131], s[0:1], v[40:41] op_sel_hi:[1,0,1]
	s_waitcnt vmcnt(31)
	v_lshlrev_b32_e32 v130, 16, v120
	v_and_b32_e32 v131, 0xffff0000, v120
	v_pk_fma_f32 v[44:45], v[132:133], s[0:1], v[44:45] op_sel_hi:[1,0,1]
	v_lshlrev_b32_e32 v120, 16, v121
	v_and_b32_e32 v121, 0xffff0000, v121
	v_pk_add_f32 v[44:45], v[44:45], v[120:121]
	s_waitcnt vmcnt(27)
	v_lshlrev_b32_e32 v120, 16, v123
	v_and_b32_e32 v121, 0xffff0000, v123
	v_pk_add_f32 v[44:45], v[44:45], v[120:121]
	s_waitcnt vmcnt(23)
	v_lshlrev_b32_e32 v120, 16, v125
	v_and_b32_e32 v121, 0xffff0000, v125
	v_pk_add_f32 v[40:41], v[40:41], v[130:131]
	v_lshlrev_b32_e32 v130, 16, v122
	v_and_b32_e32 v131, 0xffff0000, v122
	v_pk_add_f32 v[44:45], v[44:45], v[120:121]
	v_lshlrev_b32_e32 v120, 16, v108
	v_and_b32_e32 v121, 0xffff0000, v108
	v_lshlrev_b32_e32 v122, 16, v109
	v_and_b32_e32 v123, 0xffff0000, v109
	v_lshlrev_b32_e32 v108, 16, v112
	v_and_b32_e32 v109, 0xffff0000, v112
	v_lshlrev_b32_e32 v112, 16, v113
	v_and_b32_e32 v113, 0xffff0000, v113
	v_pk_fma_f32 v[108:109], v[120:121], s[0:1], v[108:109] op_sel_hi:[1,0,1]
	v_lshlrev_b32_e32 v120, 16, v114
	v_and_b32_e32 v121, 0xffff0000, v114
	v_pk_fma_f32 v[112:113], v[122:123], s[0:1], v[112:113] op_sel_hi:[1,0,1]
	v_lshlrev_b32_e32 v114, 16, v115
	v_and_b32_e32 v115, 0xffff0000, v115
	v_pk_add_f32 v[112:113], v[112:113], v[114:115]
	v_lshlrev_b32_e32 v114, 16, v117
	v_and_b32_e32 v115, 0xffff0000, v117
	v_pk_add_f32 v[112:113], v[112:113], v[114:115]
	s_waitcnt vmcnt(22)
	v_lshlrev_b32_e32 v114, 16, v119
	v_and_b32_e32 v115, 0xffff0000, v119
	v_pk_add_f32 v[108:109], v[108:109], v[120:121]
	v_lshlrev_b32_e32 v120, 16, v116
	v_and_b32_e32 v121, 0xffff0000, v116
	v_pk_add_f32 v[112:113], v[112:113], v[114:115]
	v_lshlrev_b32_e32 v114, 16, v110
	v_and_b32_e32 v115, 0xffff0000, v110
	v_lshlrev_b32_e32 v116, 16, v111
	v_and_b32_e32 v117, 0xffff0000, v111
	v_lshlrev_b32_e32 v110, 16, v46
	v_and_b32_e32 v111, 0xffff0000, v46
	v_lshlrev_b32_e32 v46, 16, v47
	v_and_b32_e32 v47, 0xffff0000, v47
	v_pk_fma_f32 v[110:111], v[114:115], s[0:1], v[110:111] op_sel_hi:[1,0,1]
	v_lshlrev_b32_e32 v114, 16, v102
	v_and_b32_e32 v115, 0xffff0000, v102
	v_pk_fma_f32 v[46:47], v[116:117], s[0:1], v[46:47] op_sel_hi:[1,0,1]
	v_lshlrev_b32_e32 v102, 16, v103
	v_and_b32_e32 v103, 0xffff0000, v103
	v_pk_add_f32 v[46:47], v[46:47], v[102:103]
	v_lshlrev_b32_e32 v102, 16, v105
	v_and_b32_e32 v103, 0xffff0000, v105
	v_pk_add_f32 v[46:47], v[46:47], v[102:103]
	s_waitcnt vmcnt(21)
	v_lshlrev_b32_e32 v102, 16, v107
	v_and_b32_e32 v103, 0xffff0000, v107
	v_pk_add_f32 v[110:111], v[110:111], v[114:115]
	v_lshlrev_b32_e32 v114, 16, v104
	v_and_b32_e32 v115, 0xffff0000, v104
	v_pk_add_f32 v[46:47], v[46:47], v[102:103]
	v_lshlrev_b32_e32 v102, 16, v42
	v_and_b32_e32 v103, 0xffff0000, v42
	v_lshlrev_b32_e32 v42, 16, v43
	v_and_b32_e32 v43, 0xffff0000, v43
	v_lshlrev_b32_e32 v104, 16, v38
	v_and_b32_e32 v105, 0xffff0000, v38
	v_lshlrev_b32_e32 v38, 16, v39
	v_and_b32_e32 v39, 0xffff0000, v39
	v_pk_fma_f32 v[102:103], v[102:103], s[0:1], v[104:105] op_sel_hi:[1,0,1]
	v_lshlrev_b32_e32 v104, 16, v32
	v_and_b32_e32 v105, 0xffff0000, v32
	v_pk_fma_f32 v[38:39], v[42:43], s[0:1], v[38:39] op_sel_hi:[1,0,1]
	v_lshlrev_b32_e32 v32, 16, v33
	v_and_b32_e32 v33, 0xffff0000, v33
	v_pk_add_f32 v[40:41], v[40:41], v[130:131]
	v_lshlrev_b32_e32 v130, 16, v124
	v_and_b32_e32 v131, 0xffff0000, v124
	v_pk_add_f32 v[102:103], v[102:103], v[104:105]
	v_lshlrev_b32_e32 v104, 16, v34
	v_and_b32_e32 v105, 0xffff0000, v34
	v_pk_add_f32 v[32:33], v[38:39], v[32:33]
	v_lshlrev_b32_e32 v34, 16, v35
	v_and_b32_e32 v35, 0xffff0000, v35
	v_pk_add_f32 v[40:41], v[40:41], v[130:131]
	v_pk_add_f32 v[108:109], v[108:109], v[120:121]
	v_lshlrev_b32_e32 v120, 16, v118
	v_and_b32_e32 v121, 0xffff0000, v118
	v_pk_add_f32 v[102:103], v[102:103], v[104:105]
	s_waitcnt vmcnt(20)
; __device__ __forceinline__ void ln_rows_pre(f32x4 (&v)[4], const LnAff& a) {
;     float s = 0.f;
; #pragma unroll
;     for (int j = 0; j < 4; ++j) s += (v[j][0] + v[j][1]) + (v[j][2] + v[j][3]);
;     const float mean = wave_sum(s) * (1.f / D); float s2 = 0.f;
; #pragma unroll
;     for (int j = 0; j < 4; ++j) { v[j] = v[j] - mean; s2 += (v[j][0] * v[j][0] + v[j][1] * v[j][1]) + (v[j][2] * v[j][2] + v[j][3] * v[j][3]); }
;     const float rstd = 1.f / sqrtf(wave_sum(s2) * (1.f / D) + LN_EPS);
; #pragma unroll
;     for (int j = 0; j < 4; ++j) v[j] = v[j] * rstd * a.g[j] + a.b[j];
; }
	v_lshlrev_b32_e32 v104, 16, v36
	v_and_b32_e32 v105, 0xffff0000, v36
	v_pk_add_f32 v[32:33], v[32:33], v[34:35]
	v_lshlrev_b32_e32 v34, 16, v37
	v_and_b32_e32 v35, 0xffff0000, v37
	v_pk_add_f32 v[108:109], v[108:109], v[120:121]
	v_pk_add_f32 v[102:103], v[102:103], v[104:105]
	v_pk_add_f32 v[104:105], v[32:33], v[34:35]
	v_mov_b32_e32 v32, v40
	v_mov_b32_e32 v33, v44
	v_mov_b32_e32 v34, v41
	v_mov_b32_e32 v35, v45
	v_pk_add_f32 v[110:111], v[110:111], v[114:115]
	v_lshlrev_b32_e32 v114, 16, v106
	v_and_b32_e32 v115, 0xffff0000, v106
	v_pk_add_f32 v[32:33], v[32:33], v[34:35]
	v_mov_b32_e32 v34, v108
	v_mov_b32_e32 v35, v112
	v_mov_b32_e32 v36, v109
	v_mov_b32_e32 v37, v113
	v_pk_add_f32 v[110:111], v[110:111], v[114:115]
	v_pk_add_f32 v[34:35], v[34:35], v[36:37]
	v_add_f32_e32 v32, v32, v33
	v_pk_add_f32 v[34:35], v[34:35], v[34:35] op_sel_hi:[0,1]
	v_pk_add_f32 v[36:37], v[110:111], v[110:111] op_sel_hi:[0,1]
	v_pk_add_f32 v[38:39], v[46:47], v[46:47] op_sel_hi:[0,1]
	v_add_f32_e32 v33, 0, v32
	v_mov_b32_e32 v36, v102
	v_mov_b32_e32 v38, v103
	v_mov_b32_e32 v34, v104
	v_mov_b32_e32 v32, v105
	v_pk_add_f32 v[36:37], v[36:37], v[38:39]
	v_pk_add_f32 v[32:33], v[34:35], v[32:33]
	s_nop 0
	v_pk_add_f32 v[32:33], v[36:37], v[32:33]
	s_nop 0
	v_add_f32_e32 v32, v32, v33
	v_mov_b32_e32 v33, v251
	s_nop 0
	v_lshlrev_b32_e32 v33, 2, v33
	v_xor_b32_e32 v34, 4, v33
	v_xor_b32_e32 v34, 8, v33
	v_xor_b32_e32 v34, 16, v33
	v_xor_b32_e32 v34, 32, v33
	v_xor_b32_e32 v34, 64, v33
	v_xor_b32_e32 v33, 0x80, v33
	s_nop 1
	v_add_f32_dpp v32, v32, v32 quad_perm:[1,0,3,2] row_mask:0xf bank_mask:0xf
	s_nop 1
	v_add_f32_dpp v32, v32, v32 quad_perm:[2,3,0,1] row_mask:0xf bank_mask:0xf
	s_nop 1
	v_add_f32_dpp v32, v32, v32 row_half_mirror row_mask:0xf bank_mask:0xf
	s_nop 1
	v_add_f32_dpp v32, v32, v32 row_mirror row_mask:0xf bank_mask:0xf
	v_mov_b32_e32 v33, v32
	v_mov_b32_e32 v34, v32
	s_nop 1
	v_permlane16_swap_b32 v33, v34
	v_add_f32_e32 v32, v33, v34
	v_mov_b32_e32 v33, v32
	v_mov_b32_e32 v34, v32
	s_nop 1
	v_permlane32_swap_b32 v33, v34
	v_add_f32_e32 v42, v33, v34
	v_fmamk_f32 v41, v42, 0xba800000, v41
	v_fmac_f32_e32 v40, 0xba800000, v42
	v_fmamk_f32 v45, v42, 0xba800000, v45
	v_fmac_f32_e32 v44, 0xba800000, v42
	v_pk_mul_f32 v[32:33], v[44:45], v[44:45]
	v_pk_mul_f32 v[34:35], v[40:41], v[40:41]
	v_fmamk_f32 v109, v42, 0xba800000, v109
	v_pk_mov_b32 v[36:37], v[34:35], v[32:33] op_sel:[1,0]
	v_mov_b32_e32 v35, v33
	v_pk_add_f32 v[32:33], v[36:37], v[34:35]
	v_fmac_f32_e32 v108, 0xba800000, v42
	v_fmamk_f32 v113, v42, 0xba800000, v113
	v_fmac_f32_e32 v112, 0xba800000, v42
	v_pk_add_f32 v[32:33], v[32:33], v[32:33] op_sel_hi:[0,1]
	v_pk_mul_f32 v[34:35], v[112:113], v[112:113]
	v_pk_mul_f32 v[36:37], v[108:109], v[108:109]
	v_fmac_f32_e32 v110, 0xba800000, v42
	v_pk_mov_b32 v[38:39], v[36:37], v[34:35] op_sel:[1,0]
	v_mov_b32_e32 v37, v35
	v_fmamk_f32 v111, v42, 0xba800000, v111
	v_fmac_f32_e32 v46, 0xba800000, v42
	v_mul_f32_e32 v32, v110, v110
	v_pk_add_f32 v[34:35], v[38:39], v[36:37]
	v_fmamk_f32 v47, v42, 0xba800000, v47
	v_pk_fma_f32 v[36:37], v[110:111], v[110:111], v[32:33] op_sel_hi:[1,1,0]
	v_mul_f32_e32 v32, v46, v46
	v_pk_add_f32 v[34:35], v[34:35], v[34:35] op_sel_hi:[0,1]
	v_pk_fma_f32 v[38:39], v[46:47], v[46:47], v[32:33] op_sel_hi:[1,1,0]
	v_fmamk_f32 v105, v42, 0xba800000, v105
	v_fmac_f32_e32 v104, 0xba800000, v42
	v_fmamk_f32 v103, v42, 0xba800000, v103
	v_fmac_f32_e32 v102, 0xba800000, v42
	v_mul_f32_e32 v36, v102, v102
	v_mul_f32_e32 v38, v103, v103
	v_mul_f32_e32 v32, v104, v104
	v_mul_f32_e32 v34, v105, v105
	v_pk_add_f32 v[36:37], v[36:37], v[38:39]
	v_pk_add_f32 v[32:33], v[32:33], v[34:35]
	s_nop 0
	v_pk_add_f32 v[32:33], v[36:37], v[32:33]
	s_nop 0
	v_add_f32_e32 v32, v32, v33
	v_mov_b32_e32 v33, v251
	s_nop 0
	v_lshlrev_b32_e32 v33, 2, v33
	v_xor_b32_e32 v34, 4, v33
	v_xor_b32_e32 v34, 8, v33
	v_xor_b32_e32 v34, 16, v33
	v_xor_b32_e32 v34, 32, v33
	v_xor_b32_e32 v34, 64, v33
	v_xor_b32_e32 v33, 0x80, v33
	s_nop 1
	v_add_f32_dpp v32, v32, v32 quad_perm:[1,0,3,2] row_mask:0xf bank_mask:0xf
	s_nop 1
	v_add_f32_dpp v32, v32, v32 quad_perm:[2,3,0,1] row_mask:0xf bank_mask:0xf
	s_nop 1
	v_add_f32_dpp v32, v32, v32 row_half_mirror row_mask:0xf bank_mask:0xf
	s_nop 1
	v_add_f32_dpp v32, v32, v32 row_mirror row_mask:0xf bank_mask:0xf
	v_mov_b32_e32 v33, v32
	v_mov_b32_e32 v34, v32
	s_nop 1
	v_permlane16_swap_b32 v33, v34
	v_add_f32_e32 v32, v33, v34
	v_mov_b32_e32 v33, v32
	v_mov_b32_e32 v34, v32
	s_nop 1
	v_permlane32_swap_b32 v33, v34
	v_add_f32_e32 v32, v33, v34
	v_fmamk_f32 v32, v32, 0x3a800000, v249
	v_mul_f32_e32 v33, 0x4f800000, v32
	v_cmp_gt_f32_e32 vcc, s52, v32
	s_nop 1
	v_cndmask_b32_e32 v32, v32, v33, vcc
	v_sqrt_f32_e32 v33, v32
	s_nop 0
	v_add_u32_e32 v34, -1, v33
	v_fma_f32 v35, -v34, v33, v32
	v_cmp_ge_f32_e64 s[0:1], 0, v35
	v_add_u32_e32 v35, 1, v33
	s_nop 0
	v_cndmask_b32_e64 v34, v33, v34, s[0:1]
	v_fma_f32 v33, -v35, v33, v32
	v_cmp_lt_f32_e64 s[0:1], 0, v33
	s_nop 1
	v_cndmask_b32_e64 v33, v34, v35, s[0:1]
	v_mul_f32_e32 v34, 0x37800000, v33
	v_cndmask_b32_e32 v33, v33, v34, vcc
	v_cmp_class_f32_e32 vcc, v32, v250
	s_nop 1
	v_cndmask_b32_e32 v32, v33, v32, vcc
	v_div_scale_f32 v33, s[0:1], v32, v32, 1.0
	v_rcp_f32_e32 v34, v33
	s_mov_b64 s[0:1], -1
	v_fma_f32 v35, -v33, v34, 1.0
	v_fmac_f32_e32 v34, v35, v34
	v_div_scale_f32 v35, vcc, 1.0, v32, 1.0
	v_mul_f32_e32 v36, v35, v34
	v_fma_f32 v37, -v33, v36, v35
	v_fmac_f32_e32 v36, v37, v34
	v_fma_f32 v33, -v33, v36, v35
	v_div_fmas_f32 v33, v33, v34, v36
	v_div_fixup_f32 v106, v33, v32, 1.0
	v_pk_mul_f32 v[32:33], v[40:41], v[106:107] op_sel_hi:[1,0]
	v_pk_mul_f32 v[34:35], v[44:45], v[106:107] op_sel_hi:[1,0]
	v_pk_mul_f32 v[36:37], v[108:109], v[106:107] op_sel_hi:[1,0]
	v_pk_mul_f32 v[38:39], v[112:113], v[106:107] op_sel_hi:[1,0]
	v_pk_mul_f32 v[40:41], v[110:111], v[106:107] op_sel_hi:[1,0]
	v_pk_mul_f32 v[42:43], v[46:47], v[106:107] op_sel_hi:[1,0]
	v_pk_mul_f32 v[44:45], v[102:103], v[106:107] op_sel_hi:[1,0]
	v_pk_mul_f32 v[46:47], v[104:105], v[106:107] op_sel_hi:[1,0]
	v_pk_fma_f32 v[34:35], v[2:3], v[34:35], v[6:7]
	v_pk_fma_f32 v[32:33], v[0:1], v[32:33], v[4:5]
	v_pk_fma_f32 v[38:39], v[10:11], v[38:39], v[14:15]
	v_pk_fma_f32 v[36:37], v[8:9], v[36:37], v[12:13]
	v_pk_fma_f32 v[42:43], v[18:19], v[42:43], v[22:23]
	v_pk_fma_f32 v[40:41], v[16:17], v[40:41], v[20:21]
	v_pk_fma_f32 v[46:47], v[26:27], v[46:47], v[30:31]
	v_pk_fma_f32 v[44:45], v[24:25], v[44:45], v[28:29]
	s_and_b64 vcc, exec, s[10:11]
	s_cbranch_vccz .LBB0_3567
; __device__ __forceinline__ unsigned pk2(float lo, float hi) { return f2bf(lo) | (f2bf(hi) << 16); }
; __device__ __forceinline__ unsigned q8x4(float a, float b, float c, float d, float s) { return q8_(a, s) | (q8_(b, s) << 8) | (q8_(c, s) << 16) | (q8_(d, s) << 24); }
; __device__ __forceinline__ void store_row_f32_bf16(const f32x4 (&v)[4], float* of, bf16* ob, int lane) {
; #pragma unroll
;     for (int j = 0; j < 4; ++j) { if (of) *(f32x4*)(of + 4 * lane + 256 * j) = v[j];
;         if (ob) { v2u w; w.x = pk2(v[j][0], v[j][1]); w.y = pk2(v[j][2], v[j][3]); *(v2u*)(ob + 4 * lane + 256 * j) = w; } }
; }
; __device__ __forceinline__ void store_row_fp8(const f32x4 (&v)[4], unsigned char* o8, int lane) {
; #pragma unroll
;     for (int j = 0; j < 4; ++j) *(unsigned*)(o8 + 4 * lane + 256 * j) = q8x4(v[j][0], v[j][1], v[j][2], v[j][3], QS_H);
; }
	v_bfe_u32 v49, v32, 16, 1
	v_add3_u32 v49, v32, v49, s55
	v_bfe_u32 v104, v33, 16, 1
	v_lshrrev_b32_e32 v49, 16, v49
	v_add3_u32 v104, v33, v104, s55
	v_and_or_b32 v104, v104, s53, v49
	v_bfe_u32 v49, v34, 16, 1
	v_lshl_add_u64 v[102:103], s[2:3], 0, v[58:59]
	v_add3_u32 v49, v34, v49, s55
	v_bfe_u32 v105, v35, 16, 1
	s_mov_b32 s0, 0x36e00000
	v_lshrrev_b32_e32 v49, 16, v49
	v_add3_u32 v105, v35, v105, s55
	v_add_co_u32_e32 v102, vcc, s0, v102
	v_and_or_b32 v105, v105, s53, v49
	s_nop 0
	v_addc_co_u32_e32 v103, vcc, 0, v103, vcc
	v_bfe_u32 v49, v36, 16, 1
	global_store_dwordx2 v[102:103], v[104:105], off
	v_add3_u32 v49, v36, v49, s55
	v_bfe_u32 v104, v37, 16, 1
	v_lshrrev_b32_e32 v49, 16, v49
	v_add3_u32 v104, v37, v104, s55
	v_and_or_b32 v104, v104, s53, v49
	v_bfe_u32 v49, v38, 16, 1
	v_add3_u32 v49, v38, v49, s55
	v_bfe_u32 v105, v39, 16, 1
	v_lshrrev_b32_e32 v49, 16, v49
	v_add3_u32 v105, v39, v105, s55
	v_and_or_b32 v105, v105, s53, v49
	v_bfe_u32 v49, v40, 16, 1
	global_store_dwordx2 v[102:103], v[104:105], off offset:512
	v_add3_u32 v49, v40, v49, s55
	v_bfe_u32 v104, v41, 16, 1
	v_lshrrev_b32_e32 v49, 16, v49
	v_add3_u32 v104, v41, v104, s55
	v_and_or_b32 v104, v104, s53, v49
	v_bfe_u32 v49, v42, 16, 1
	v_add3_u32 v49, v42, v49, s55
	v_bfe_u32 v105, v43, 16, 1
	v_lshrrev_b32_e32 v49, 16, v49
	v_add3_u32 v105, v43, v105, s55
	v_and_or_b32 v105, v105, s53, v49
	v_bfe_u32 v49, v44, 16, 1
	global_store_dwordx2 v[102:103], v[104:105], off offset:1024
	v_add3_u32 v49, v44, v49, s55
	v_bfe_u32 v104, v45, 16, 1
	v_lshrrev_b32_e32 v49, 16, v49
	v_add3_u32 v104, v45, v104, s55
	v_and_or_b32 v104, v104, s53, v49
	v_bfe_u32 v49, v46, 16, 1
	v_add3_u32 v49, v46, v49, s55
	v_bfe_u32 v105, v47, 16, 1
	v_lshrrev_b32_e32 v49, 16, v49
	v_add3_u32 v105, v47, v105, s55
	v_and_or_b32 v105, v105, s53, v49
	global_store_dwordx2 v[102:103], v[104:105], off offset:1536
	v_mul_f32_e32 v104, 0x41cb3333, v33
	v_mul_f32_e32 v49, 0x41cb3333, v32
	v_med3_f32 v104, v104, s54, v213
	v_mul_f32_e32 v105, 0x41cb3333, v34
	v_mul_f32_e32 v106, 0x41cb3333, v35
	v_med3_f32 v49, v49, s54, v213
	v_rndne_f32_e32 v104, v104
	v_med3_f32 v105, v105, s54, v213
	v_med3_f32 v106, v106, s54, v213
	v_rndne_f32_e32 v49, v49
	v_cvt_i32_f32_e32 v104, v104
	v_rndne_f32_e32 v105, v105
	v_rndne_f32_e32 v106, v106
	v_cvt_i32_f32_e32 v49, v49
	v_cvt_i32_f32_sdwa v105, v105 dst_sel:WORD_1 dst_unused:UNUSED_PAD src0_sel:DWORD
	v_cvt_i32_f32_e32 v106, v106
	v_lshl_add_u64 v[102:103], s[2:3], 0, v[56:57]
	v_lshlrev_b32_e32 v104, 8, v104
	s_mov_b32 s0, 0x3ae00000
	v_and_b32_e32 v104, 0xff00, v104
	v_and_b32_e32 v105, 0xff0000, v105
	v_perm_b32 v49, v106, v49, s65
	v_add_co_u32_e32 v102, vcc, s0, v102
	v_or3_b32 v49, v49, v104, v105
	s_nop 0
	v_addc_co_u32_e32 v103, vcc, 0, v103, vcc
	v_mul_f32_e32 v104, 0x41cb3333, v37
	global_store_dword v[102:103], v49, off
	v_mul_f32_e32 v49, 0x41cb3333, v36
	v_med3_f32 v104, v104, s54, v213
	v_mul_f32_e32 v105, 0x41cb3333, v38
	v_mul_f32_e32 v106, 0x41cb3333, v39
	v_med3_f32 v49, v49, s54, v213
	v_rndne_f32_e32 v104, v104
	v_med3_f32 v105, v105, s54, v213
	v_med3_f32 v106, v106, s54, v213
	v_rndne_f32_e32 v49, v49
	v_cvt_i32_f32_e32 v104, v104
	v_rndne_f32_e32 v105, v105
	v_rndne_f32_e32 v106, v106
	v_cvt_i32_f32_e32 v49, v49
	v_cvt_i32_f32_sdwa v105, v105 dst_sel:WORD_1 dst_unused:UNUSED_PAD src0_sel:DWORD
	v_cvt_i32_f32_e32 v106, v106
	v_lshlrev_b32_e32 v104, 8, v104
	v_and_b32_e32 v104, 0xff00, v104
	v_and_b32_e32 v105, 0xff0000, v105
	v_perm_b32 v49, v106, v49, s65
	v_or3_b32 v49, v49, v104, v105
	v_mul_f32_e32 v104, 0x41cb3333, v41
	global_store_dword v[102:103], v49, off offset:256
	v_mul_f32_e32 v49, 0x41cb3333, v40
	v_med3_f32 v104, v104, s54, v213
	v_mul_f32_e32 v105, 0x41cb3333, v42
	v_mul_f32_e32 v106, 0x41cb3333, v43
	v_med3_f32 v49, v49, s54, v213
	v_rndne_f32_e32 v104, v104
	v_med3_f32 v105, v105, s54, v213
	v_med3_f32 v106, v106, s54, v213
	v_rndne_f32_e32 v49, v49
	v_cvt_i32_f32_e32 v104, v104
	v_rndne_f32_e32 v105, v105
	v_rndne_f32_e32 v106, v106
	v_cvt_i32_f32_e32 v49, v49
	v_cvt_i32_f32_sdwa v105, v105 dst_sel:WORD_1 dst_unused:UNUSED_PAD src0_sel:DWORD
	v_cvt_i32_f32_e32 v106, v106
	v_lshlrev_b32_e32 v104, 8, v104
	v_and_b32_e32 v104, 0xff00, v104
	v_and_b32_e32 v105, 0xff0000, v105
	v_perm_b32 v49, v106, v49, s65
	v_or3_b32 v49, v49, v104, v105
	v_mul_f32_e32 v104, 0x41cb3333, v45
	global_store_dword v[102:103], v49, off offset:512
	v_mul_f32_e32 v49, 0x41cb3333, v44
	v_med3_f32 v104, v104, s54, v213
	v_mul_f32_e32 v105, 0x41cb3333, v46
	v_mul_f32_e32 v106, 0x41cb3333, v47
	v_med3_f32 v49, v49, s54, v213
	v_rndne_f32_e32 v104, v104
	v_med3_f32 v105, v105, s54, v213
	v_med3_f32 v106, v106, s54, v213
	v_rndne_f32_e32 v49, v49
	v_cvt_i32_f32_e32 v104, v104
	v_rndne_f32_e32 v105, v105
	v_rndne_f32_e32 v106, v106
	v_cvt_i32_f32_e32 v49, v49
	v_cvt_i32_f32_sdwa v105, v105 dst_sel:WORD_1 dst_unused:UNUSED_PAD src0_sel:DWORD
	v_cvt_i32_f32_e32 v106, v106
	v_lshlrev_b32_e32 v104, 8, v104
	v_and_b32_e32 v104, 0xff00, v104
	v_and_b32_e32 v105, 0xff0000, v105
	v_perm_b32 v49, v106, v49, s65
	v_or3_b32 v49, v49, v104, v105
	global_store_dword v[102:103], v49, off offset:768
	s_mov_b64 s[0:1], 0

; __global__ void __launch_bounds__(NWAVES * 64, 2) fwd(Args args) {
;     ...
;               for (; m < M; m += 2 * st) { const bool two = m + st < M; const int m1 = two ? m + st : m; v2u hA[4], yA[4][4], hB[4], yB[4][4];
;                   LL_ISSUE(m, sa, hA, yA); LL_ISSUE(m1, sb, hB, yB);
;                   { const int n0 = m + 2 * st; if (n0 < M) { sa = *(const v4u*)(SLOT + (size_t)n0 * 4); sb = *(const v4u*)(SLOT + (size_t)(n0 + st < M ? n0 + st : n0) * 4); } }
;                   LL_FIN(m, hA, yA)
;                   if (two) LL_FIN(m1, hB, yB) } }
.LBB0_3570:
	s_andn2_b64 vcc, exec, s[20:21]
	s_cbranch_vccnz .LBB0_3562
	s_waitcnt vmcnt(19)
	v_lshlrev_b32_e32 v32, 16, v92
	v_and_b32_e32 v33, 0xffff0000, v92
	s_waitcnt vmcnt(15)
	v_lshlrev_b32_e32 v36, 16, v94
	v_and_b32_e32 v37, 0xffff0000, v94
	s_mov_b32 s0, 0x3fd744fd
	v_pk_fma_f32 v[32:33], v[32:33], s[0:1], v[36:37] op_sel_hi:[1,0,1]
	s_waitcnt vmcnt(11)
	v_lshlrev_b32_e32 v36, 16, v96
	v_and_b32_e32 v37, 0xffff0000, v96
	v_pk_add_f32 v[32:33], v[32:33], v[36:37]
	s_waitcnt vmcnt(7)
	v_lshlrev_b32_e32 v36, 16, v98
	v_and_b32_e32 v37, 0xffff0000, v98
	v_pk_add_f32 v[32:33], v[32:33], v[36:37]
	s_waitcnt vmcnt(3)
	v_lshlrev_b32_e32 v36, 16, v100
	v_and_b32_e32 v37, 0xffff0000, v100
	v_lshlrev_b32_e32 v34, 16, v93
	v_and_b32_e32 v35, 0xffff0000, v93
	v_pk_add_f32 v[32:33], v[32:33], v[36:37]
	v_lshlrev_b32_e32 v36, 16, v95
	v_and_b32_e32 v37, 0xffff0000, v95
	v_pk_fma_f32 v[34:35], v[34:35], s[0:1], v[36:37] op_sel_hi:[1,0,1]
	v_lshlrev_b32_e32 v36, 16, v97
	v_and_b32_e32 v37, 0xffff0000, v97
	v_pk_add_f32 v[34:35], v[34:35], v[36:37]
	v_lshlrev_b32_e32 v36, 16, v99
	v_and_b32_e32 v37, 0xffff0000, v99
	v_pk_add_f32 v[34:35], v[34:35], v[36:37]
	v_lshlrev_b32_e32 v36, 16, v101
	v_and_b32_e32 v37, 0xffff0000, v101
	v_pk_add_f32 v[34:35], v[34:35], v[36:37]
	v_lshlrev_b32_e32 v36, 16, v82
	v_and_b32_e32 v37, 0xffff0000, v82
	v_lshlrev_b32_e32 v40, 16, v84
	v_and_b32_e32 v41, 0xffff0000, v84
	v_pk_fma_f32 v[36:37], v[36:37], s[0:1], v[40:41] op_sel_hi:[1,0,1]
	v_lshlrev_b32_e32 v40, 16, v86
	v_and_b32_e32 v41, 0xffff0000, v86
	v_pk_add_f32 v[36:37], v[36:37], v[40:41]
	v_lshlrev_b32_e32 v40, 16, v88
	v_and_b32_e32 v41, 0xffff0000, v88
	v_pk_add_f32 v[36:37], v[36:37], v[40:41]
	s_waitcnt vmcnt(2)
	v_lshlrev_b32_e32 v40, 16, v90
	v_and_b32_e32 v41, 0xffff0000, v90
	v_lshlrev_b32_e32 v38, 16, v83
	v_and_b32_e32 v39, 0xffff0000, v83
	v_pk_add_f32 v[36:37], v[36:37], v[40:41]
	v_lshlrev_b32_e32 v40, 16, v85
	v_and_b32_e32 v41, 0xffff0000, v85
	v_pk_fma_f32 v[38:39], v[38:39], s[0:1], v[40:41] op_sel_hi:[1,0,1]
	v_lshlrev_b32_e32 v40, 16, v87
	v_and_b32_e32 v41, 0xffff0000, v87
	v_pk_add_f32 v[38:39], v[38:39], v[40:41]
	v_lshlrev_b32_e32 v40, 16, v89
	v_and_b32_e32 v41, 0xffff0000, v89
	v_pk_add_f32 v[38:39], v[38:39], v[40:41]
	v_lshlrev_b32_e32 v40, 16, v91
	v_and_b32_e32 v41, 0xffff0000, v91
	v_pk_add_f32 v[38:39], v[38:39], v[40:41]
	v_lshlrev_b32_e32 v40, 16, v72
	v_and_b32_e32 v41, 0xffff0000, v72
	v_lshlrev_b32_e32 v44, 16, v74
	v_and_b32_e32 v45, 0xffff0000, v74
	v_pk_fma_f32 v[40:41], v[40:41], s[0:1], v[44:45] op_sel_hi:[1,0,1]
	v_lshlrev_b32_e32 v44, 16, v76
	v_and_b32_e32 v45, 0xffff0000, v76
	v_pk_add_f32 v[40:41], v[40:41], v[44:45]
	v_lshlrev_b32_e32 v44, 16, v78
	v_and_b32_e32 v45, 0xffff0000, v78
	v_pk_add_f32 v[40:41], v[40:41], v[44:45]
	s_waitcnt vmcnt(1)
	v_lshlrev_b32_e32 v44, 16, v80
	v_and_b32_e32 v45, 0xffff0000, v80
	v_lshlrev_b32_e32 v42, 16, v73
	v_and_b32_e32 v43, 0xffff0000, v73
	v_pk_add_f32 v[40:41], v[40:41], v[44:45]
	v_lshlrev_b32_e32 v44, 16, v75
	v_and_b32_e32 v45, 0xffff0000, v75
	v_pk_fma_f32 v[42:43], v[42:43], s[0:1], v[44:45] op_sel_hi:[1,0,1]
	v_lshlrev_b32_e32 v44, 16, v77
	v_and_b32_e32 v45, 0xffff0000, v77
	v_pk_add_f32 v[42:43], v[42:43], v[44:45]
	v_lshlrev_b32_e32 v44, 16, v79
	v_and_b32_e32 v45, 0xffff0000, v79
	v_pk_add_f32 v[42:43], v[42:43], v[44:45]
	v_lshlrev_b32_e32 v44, 16, v81
	v_and_b32_e32 v45, 0xffff0000, v81
	v_pk_add_f32 v[42:43], v[42:43], v[44:45]
	v_lshlrev_b32_e32 v44, 16, v62
	v_and_b32_e32 v45, 0xffff0000, v62
	v_lshlrev_b32_e32 v46, 16, v63
	v_and_b32_e32 v47, 0xffff0000, v63
	v_lshlrev_b32_e32 v62, 16, v64
	v_and_b32_e32 v63, 0xffff0000, v64
	v_pk_fma_f32 v[44:45], v[44:45], s[0:1], v[62:63] op_sel_hi:[1,0,1]
	v_lshlrev_b32_e32 v62, 16, v66
	v_and_b32_e32 v63, 0xffff0000, v66
	v_pk_add_f32 v[44:45], v[44:45], v[62:63]
	v_lshlrev_b32_e32 v62, 16, v68
	v_and_b32_e32 v63, 0xffff0000, v68
	v_pk_add_f32 v[44:45], v[44:45], v[62:63]
	s_waitcnt vmcnt(0)
	v_lshlrev_b32_e32 v62, 16, v70
	v_and_b32_e32 v63, 0xffff0000, v70
	v_pk_add_f32 v[44:45], v[44:45], v[62:63]
	v_lshlrev_b32_e32 v62, 16, v65
	v_and_b32_e32 v63, 0xffff0000, v65
	v_pk_fma_f32 v[46:47], v[46:47], s[0:1], v[62:63] op_sel_hi:[1,0,1]
	v_lshlrev_b32_e32 v62, 16, v67
	v_and_b32_e32 v63, 0xffff0000, v67
	v_pk_add_f32 v[46:47], v[46:47], v[62:63]
	v_lshlrev_b32_e32 v62, 16, v69
	v_and_b32_e32 v63, 0xffff0000, v69
	v_pk_add_f32 v[46:47], v[46:47], v[62:63]
	v_lshlrev_b32_e32 v62, 16, v71
	v_and_b32_e32 v63, 0xffff0000, v71
	v_pk_add_f32 v[46:47], v[46:47], v[62:63]
	v_mov_b32_e32 v62, v32
	v_mov_b32_e32 v63, v34
	v_mov_b32_e32 v64, v33
	v_mov_b32_e32 v65, v35
	v_pk_add_f32 v[62:63], v[62:63], v[64:65]
	v_mov_b32_e32 v64, v36
	v_mov_b32_e32 v65, v38
	v_mov_b32_e32 v66, v37
	v_mov_b32_e32 v67, v39
	v_pk_add_f32 v[64:65], v[64:65], v[66:67]
	v_add_f32_e32 v49, v62, v63
	v_pk_add_f32 v[64:65], v[64:65], v[64:65] op_sel_hi:[0,1]
	v_pk_add_f32 v[66:67], v[40:41], v[40:41] op_sel_hi:[0,1]
	v_pk_add_f32 v[68:69], v[42:43], v[42:43] op_sel_hi:[0,1]
	v_add_f32_e32 v63, 0, v49
	v_mov_b32_e32 v66, v44
	v_mov_b32_e32 v68, v45
	v_mov_b32_e32 v64, v46
	v_mov_b32_e32 v62, v47
	v_pk_add_f32 v[66:67], v[66:67], v[68:69]
	v_pk_add_f32 v[62:63], v[64:65], v[62:63]
	s_nop 0
	v_pk_add_f32 v[62:63], v[66:67], v[62:63]
	s_nop 0
	v_add_f32_e32 v49, v62, v63
	v_mov_b32_e32 v62, v251
	s_nop 0
	v_lshlrev_b32_e32 v62, 2, v62
	v_xor_b32_e32 v63, 4, v62
	v_xor_b32_e32 v63, 8, v62
	v_xor_b32_e32 v63, 16, v62
	v_xor_b32_e32 v63, 32, v62
	v_xor_b32_e32 v63, 64, v62
	v_xor_b32_e32 v62, 0x80, v62
	s_nop 1
	v_add_f32_dpp v49, v49, v49 quad_perm:[1,0,3,2] row_mask:0xf bank_mask:0xf
; __device__ __forceinline__ void ln_rows_pre(f32x4 (&v)[4], const LnAff& a) {
;     float s = 0.f;
; #pragma unroll
;     for (int j = 0; j < 4; ++j) s += (v[j][0] + v[j][1]) + (v[j][2] + v[j][3]);
;     const float mean = wave_sum(s) * (1.f / D); float s2 = 0.f;
; #pragma unroll
;     for (int j = 0; j < 4; ++j) { v[j] = v[j] - mean; s2 += (v[j][0] * v[j][0] + v[j][1] * v[j][1]) + (v[j][2] * v[j][2] + v[j][3] * v[j][3]); }
;     const float rstd = 1.f / sqrtf(wave_sum(s2) * (1.f / D) + LN_EPS);
; #pragma unroll
;     for (int j = 0; j < 4; ++j) v[j] = v[j] * rstd * a.g[j] + a.b[j];
; }
	s_nop 1
	v_add_f32_dpp v49, v49, v49 quad_perm:[2,3,0,1] row_mask:0xf bank_mask:0xf
	s_nop 1
	v_add_f32_dpp v49, v49, v49 row_half_mirror row_mask:0xf bank_mask:0xf
	s_nop 1
	v_add_f32_dpp v49, v49, v49 row_mirror row_mask:0xf bank_mask:0xf
	v_mov_b32_e32 v62, v49
	v_mov_b32_e32 v63, v49
	s_nop 1
	v_permlane16_swap_b32 v62, v63
	v_add_f32_e32 v49, v62, v63
	v_mov_b32_e32 v62, v49
	v_mov_b32_e32 v63, v49
	s_nop 1
	v_permlane32_swap_b32 v62, v63
	v_add_f32_e32 v49, v62, v63
	v_fmamk_f32 v33, v49, 0xba800000, v33
	v_fmac_f32_e32 v32, 0xba800000, v49
	v_fmamk_f32 v35, v49, 0xba800000, v35
	v_fmac_f32_e32 v34, 0xba800000, v49
	v_pk_mul_f32 v[62:63], v[34:35], v[34:35]
	v_pk_mul_f32 v[64:65], v[32:33], v[32:33]
	v_fmamk_f32 v37, v49, 0xba800000, v37
	v_pk_mov_b32 v[66:67], v[64:65], v[62:63] op_sel:[1,0]
	v_mov_b32_e32 v65, v63
	v_pk_add_f32 v[62:63], v[66:67], v[64:65]
	v_fmac_f32_e32 v36, 0xba800000, v49
	v_fmamk_f32 v39, v49, 0xba800000, v39
	v_fmac_f32_e32 v38, 0xba800000, v49
	v_pk_add_f32 v[62:63], v[62:63], v[62:63] op_sel_hi:[0,1]
	v_pk_mul_f32 v[64:65], v[38:39], v[38:39]
	v_pk_mul_f32 v[66:67], v[36:37], v[36:37]
	v_fmac_f32_e32 v40, 0xba800000, v49
	v_pk_mov_b32 v[68:69], v[66:67], v[64:65] op_sel:[1,0]
	v_mov_b32_e32 v67, v65
	v_fmamk_f32 v41, v49, 0xba800000, v41
	v_fmac_f32_e32 v42, 0xba800000, v49
	v_mul_f32_e32 v62, v40, v40
	v_pk_add_f32 v[64:65], v[68:69], v[66:67]
	v_fmamk_f32 v43, v49, 0xba800000, v43
	v_pk_fma_f32 v[66:67], v[40:41], v[40:41], v[62:63] op_sel_hi:[1,1,0]
	v_mul_f32_e32 v62, v42, v42
	v_pk_add_f32 v[64:65], v[64:65], v[64:65] op_sel_hi:[0,1]
	v_pk_fma_f32 v[68:69], v[42:43], v[42:43], v[62:63] op_sel_hi:[1,1,0]
	v_fmamk_f32 v47, v49, 0xba800000, v47
	v_fmac_f32_e32 v46, 0xba800000, v49
	v_fmamk_f32 v45, v49, 0xba800000, v45
	v_fmac_f32_e32 v44, 0xba800000, v49
	v_mul_f32_e32 v66, v44, v44
	v_mul_f32_e32 v68, v45, v45
	v_mul_f32_e32 v62, v46, v46
	v_mul_f32_e32 v64, v47, v47
	v_pk_add_f32 v[66:67], v[66:67], v[68:69]
	v_pk_add_f32 v[62:63], v[62:63], v[64:65]
	s_nop 0
	v_pk_add_f32 v[62:63], v[66:67], v[62:63]
	s_nop 0
	v_add_f32_e32 v49, v62, v63
	v_mov_b32_e32 v62, v251
	s_nop 0
	v_lshlrev_b32_e32 v62, 2, v62
	v_xor_b32_e32 v63, 4, v62
	v_xor_b32_e32 v63, 8, v62
	v_xor_b32_e32 v63, 16, v62
	v_xor_b32_e32 v63, 32, v62
	v_xor_b32_e32 v63, 64, v62
	v_xor_b32_e32 v62, 0x80, v62
	s_nop 1
	v_add_f32_dpp v49, v49, v49 quad_perm:[1,0,3,2] row_mask:0xf bank_mask:0xf
	s_nop 1
	v_add_f32_dpp v49, v49, v49 quad_perm:[2,3,0,1] row_mask:0xf bank_mask:0xf
	s_nop 1
	v_add_f32_dpp v49, v49, v49 row_half_mirror row_mask:0xf bank_mask:0xf
	s_nop 1
	v_add_f32_dpp v49, v49, v49 row_mirror row_mask:0xf bank_mask:0xf
	v_mov_b32_e32 v62, v49
	v_mov_b32_e32 v63, v49
	s_nop 1
	v_permlane16_swap_b32 v62, v63
	v_add_f32_e32 v49, v62, v63
	v_mov_b32_e32 v62, v49
	v_mov_b32_e32 v63, v49
	s_nop 1
	v_permlane32_swap_b32 v62, v63
	v_add_f32_e32 v49, v62, v63
	v_fmamk_f32 v49, v49, 0x3a800000, v249
	v_mul_f32_e32 v62, 0x4f800000, v49
	v_cmp_gt_f32_e32 vcc, s52, v49
	s_nop 1
	v_cndmask_b32_e32 v49, v49, v62, vcc
	v_sqrt_f32_e32 v62, v49
	s_nop 0
	v_add_u32_e32 v63, -1, v62
	v_fma_f32 v64, -v63, v62, v49
	v_cmp_ge_f32_e64 s[0:1], 0, v64
	v_add_u32_e32 v64, 1, v62
	s_nop 0
	v_cndmask_b32_e64 v63, v62, v63, s[0:1]
	v_fma_f32 v62, -v64, v62, v49
	v_cmp_lt_f32_e64 s[0:1], 0, v62
	s_nop 1
	v_cndmask_b32_e64 v62, v63, v64, s[0:1]
	v_mul_f32_e32 v63, 0x37800000, v62
	v_cndmask_b32_e32 v62, v62, v63, vcc
	v_cmp_class_f32_e32 vcc, v49, v250
	s_nop 1
	v_cndmask_b32_e32 v49, v62, v49, vcc
	v_div_scale_f32 v62, s[0:1], v49, v49, 1.0
	v_rcp_f32_e32 v63, v62
	s_mov_b64 s[0:1], -1
	v_fma_f32 v64, -v62, v63, 1.0
	v_fmac_f32_e32 v63, v64, v63
	v_div_scale_f32 v64, vcc, 1.0, v49, 1.0
	v_mul_f32_e32 v65, v64, v63
	v_fma_f32 v66, -v62, v65, v64
	v_fmac_f32_e32 v65, v66, v63
	v_fma_f32 v62, -v62, v65, v64
	v_div_fmas_f32 v62, v62, v63, v65
	v_div_fixup_f32 v62, v62, v49, 1.0
	v_pk_mul_f32 v[32:33], v[32:33], v[62:63] op_sel_hi:[1,0]
	v_pk_mul_f32 v[34:35], v[34:35], v[62:63] op_sel_hi:[1,0]
	v_pk_mul_f32 v[36:37], v[36:37], v[62:63] op_sel_hi:[1,0]
	v_pk_mul_f32 v[38:39], v[38:39], v[62:63] op_sel_hi:[1,0]
	v_pk_mul_f32 v[40:41], v[40:41], v[62:63] op_sel_hi:[1,0]
	v_pk_mul_f32 v[42:43], v[42:43], v[62:63] op_sel_hi:[1,0]
	v_pk_mul_f32 v[44:45], v[44:45], v[62:63] op_sel_hi:[1,0]
	v_pk_mul_f32 v[46:47], v[46:47], v[62:63] op_sel_hi:[1,0]
	v_pk_fma_f32 v[34:35], v[2:3], v[34:35], v[6:7]
	v_pk_fma_f32 v[32:33], v[0:1], v[32:33], v[4:5]
	v_pk_fma_f32 v[38:39], v[10:11], v[38:39], v[14:15]
	v_pk_fma_f32 v[36:37], v[8:9], v[36:37], v[12:13]
	v_pk_fma_f32 v[42:43], v[18:19], v[42:43], v[22:23]
	v_pk_fma_f32 v[40:41], v[16:17], v[40:41], v[20:21]
	v_pk_fma_f32 v[46:47], v[26:27], v[46:47], v[30:31]
	v_pk_fma_f32 v[44:45], v[24:25], v[44:45], v[28:29]
	s_and_b64 vcc, exec, s[10:11]
	s_cbranch_vccz .LBB0_3573
; __device__ __forceinline__ unsigned pk2(float lo, float hi) { return f2bf(lo) | (f2bf(hi) << 16); }
; __device__ __forceinline__ unsigned q8x4(float a, float b, float c, float d, float s) { return q8_(a, s) | (q8_(b, s) << 8) | (q8_(c, s) << 16) | (q8_(d, s) << 24); }
; __device__ __forceinline__ void store_row_f32_bf16(const f32x4 (&v)[4], float* of, bf16* ob, int lane) {
; #pragma unroll
;     for (int j = 0; j < 4; ++j) { if (of) *(f32x4*)(of + 4 * lane + 256 * j) = v[j];
;         if (ob) { v2u w; w.x = pk2(v[j][0], v[j][1]); w.y = pk2(v[j][2], v[j][3]); *(v2u*)(ob + 4 * lane + 256 * j) = w; } }
; }
; __device__ __forceinline__ void store_row_fp8(const f32x4 (&v)[4], unsigned char* o8, int lane) {
; #pragma unroll
;     for (int j = 0; j < 4; ++j) *(unsigned*)(o8 + 4 * lane + 256 * j) = q8x4(v[j][0], v[j][1], v[j][2], v[j][3], QS_H);
; }
	v_bfe_u32 v49, v32, 16, 1
	v_add3_u32 v49, v32, v49, s55
	v_bfe_u32 v64, v33, 16, 1
	v_lshrrev_b32_e32 v49, 16, v49
	v_add3_u32 v64, v33, v64, s55
	v_and_or_b32 v64, v64, s53, v49
	v_bfe_u32 v49, v34, 16, 1
	s_ashr_i32 s69, s68, 31
	v_add3_u32 v49, v34, v49, s55
	v_bfe_u32 v65, v35, 16, 1
	s_lshl_b64 s[20:21], s[68:69], 11
	v_lshrrev_b32_e32 v49, 16, v49
	v_add3_u32 v65, v35, v65, s55
	v_lshl_add_u64 v[62:63], v[50:51], 0, s[20:21]
	v_and_or_b32 v65, v65, s53, v49
	v_bfe_u32 v49, v36, 16, 1
	global_store_dwordx2 v[62:63], v[64:65], off
	v_add3_u32 v49, v36, v49, s55
	v_bfe_u32 v64, v37, 16, 1
	v_lshrrev_b32_e32 v49, 16, v49
	v_add3_u32 v64, v37, v64, s55
	v_and_or_b32 v64, v64, s53, v49
	v_bfe_u32 v49, v38, 16, 1
	v_add3_u32 v49, v38, v49, s55
	v_bfe_u32 v65, v39, 16, 1
	v_lshrrev_b32_e32 v49, 16, v49
	v_add3_u32 v65, v39, v65, s55
	v_and_or_b32 v65, v65, s53, v49
	v_bfe_u32 v49, v40, 16, 1
	global_store_dwordx2 v[62:63], v[64:65], off offset:512
	v_add3_u32 v49, v40, v49, s55
	v_bfe_u32 v64, v41, 16, 1
	v_lshrrev_b32_e32 v49, 16, v49
	v_add3_u32 v64, v41, v64, s55
	v_and_or_b32 v64, v64, s53, v49
	v_bfe_u32 v49, v42, 16, 1
	v_add3_u32 v49, v42, v49, s55
	v_bfe_u32 v65, v43, 16, 1
	v_lshrrev_b32_e32 v49, 16, v49
	v_add3_u32 v65, v43, v65, s55
	v_and_or_b32 v65, v65, s53, v49
	v_bfe_u32 v49, v44, 16, 1
	global_store_dwordx2 v[62:63], v[64:65], off offset:1024
	v_add3_u32 v49, v44, v49, s55
	v_bfe_u32 v64, v45, 16, 1
	v_lshrrev_b32_e32 v49, 16, v49
	v_add3_u32 v64, v45, v64, s55
	v_and_or_b32 v64, v64, s53, v49
	v_bfe_u32 v49, v46, 16, 1
	v_add3_u32 v49, v46, v49, s55
	v_bfe_u32 v65, v47, 16, 1
	v_lshrrev_b32_e32 v49, 16, v49
	v_add3_u32 v65, v47, v65, s55
	v_and_or_b32 v65, v65, s53, v49
	global_store_dwordx2 v[62:63], v[64:65], off offset:1536
	v_mul_f32_e32 v64, 0x41cb3333, v33
	v_mul_f32_e32 v49, 0x41cb3333, v32
	v_med3_f32 v64, v64, s54, v213
	v_mul_f32_e32 v65, 0x41cb3333, v34
	v_mul_f32_e32 v66, 0x41cb3333, v35
	v_med3_f32 v49, v49, s54, v213
	v_rndne_f32_e32 v64, v64
	v_med3_f32 v65, v65, s54, v213
	v_med3_f32 v66, v66, s54, v213
	v_rndne_f32_e32 v49, v49
	v_cvt_i32_f32_e32 v64, v64
	v_rndne_f32_e32 v65, v65
	v_rndne_f32_e32 v66, v66
	v_cvt_i32_f32_e32 v49, v49
	v_cvt_i32_f32_sdwa v65, v65 dst_sel:WORD_1 dst_unused:UNUSED_PAD src0_sel:DWORD
	v_cvt_i32_f32_e32 v66, v66
	v_lshlrev_b32_e32 v64, 8, v64
	s_lshl_b64 s[0:1], s[68:69], 10
	v_and_b32_e32 v64, 0xff00, v64
	v_and_b32_e32 v65, 0xff0000, v65
	v_perm_b32 v49, v66, v49, s65
	v_lshl_add_u64 v[62:63], v[52:53], 0, s[0:1]
	v_or3_b32 v49, v49, v64, v65
	v_mul_f32_e32 v64, 0x41cb3333, v37
	global_store_dword v[62:63], v49, off
	v_mul_f32_e32 v49, 0x41cb3333, v36
	v_med3_f32 v64, v64, s54, v213
	v_mul_f32_e32 v65, 0x41cb3333, v38
	v_mul_f32_e32 v66, 0x41cb3333, v39
	v_med3_f32 v49, v49, s54, v213
	v_rndne_f32_e32 v64, v64
	v_med3_f32 v65, v65, s54, v213
	v_med3_f32 v66, v66, s54, v213
	v_rndne_f32_e32 v49, v49
	v_cvt_i32_f32_e32 v64, v64
	v_rndne_f32_e32 v65, v65
	v_rndne_f32_e32 v66, v66
	v_cvt_i32_f32_e32 v49, v49
	v_cvt_i32_f32_sdwa v65, v65 dst_sel:WORD_1 dst_unused:UNUSED_PAD src0_sel:DWORD
	v_cvt_i32_f32_e32 v66, v66
	v_lshlrev_b32_e32 v64, 8, v64
	v_and_b32_e32 v64, 0xff00, v64
	v_and_b32_e32 v65, 0xff0000, v65
	v_perm_b32 v49, v66, v49, s65
	v_or3_b32 v49, v49, v64, v65
	v_mul_f32_e32 v64, 0x41cb3333, v41
	global_store_dword v[62:63], v49, off offset:256
	v_mul_f32_e32 v49, 0x41cb3333, v40
	v_med3_f32 v64, v64, s54, v213
	v_mul_f32_e32 v65, 0x41cb3333, v42
	v_mul_f32_e32 v66, 0x41cb3333, v43
	v_med3_f32 v49, v49, s54, v213
	v_rndne_f32_e32 v64, v64
	v_med3_f32 v65, v65, s54, v213
	v_med3_f32 v66, v66, s54, v213
	v_rndne_f32_e32 v49, v49
	v_cvt_i32_f32_e32 v64, v64
	v_rndne_f32_e32 v65, v65
	v_rndne_f32_e32 v66, v66
	v_cvt_i32_f32_e32 v49, v49
	v_cvt_i32_f32_sdwa v65, v65 dst_sel:WORD_1 dst_unused:UNUSED_PAD src0_sel:DWORD
	v_cvt_i32_f32_e32 v66, v66
	v_lshlrev_b32_e32 v64, 8, v64
	v_and_b32_e32 v64, 0xff00, v64
	v_and_b32_e32 v65, 0xff0000, v65
	v_perm_b32 v49, v66, v49, s65
	v_or3_b32 v49, v49, v64, v65
	v_mul_f32_e32 v64, 0x41cb3333, v45
	global_store_dword v[62:63], v49, off offset:512
	v_mul_f32_e32 v49, 0x41cb3333, v44
	v_med3_f32 v64, v64, s54, v213
	v_mul_f32_e32 v65, 0x41cb3333, v46
	v_mul_f32_e32 v66, 0x41cb3333, v47
	v_med3_f32 v49, v49, s54, v213
	v_rndne_f32_e32 v64, v64
	v_med3_f32 v65, v65, s54, v213
	v_med3_f32 v66, v66, s54, v213
	v_rndne_f32_e32 v49, v49
	v_cvt_i32_f32_e32 v64, v64
	v_rndne_f32_e32 v65, v65
	v_rndne_f32_e32 v66, v66
	v_cvt_i32_f32_e32 v49, v49
	v_cvt_i32_f32_sdwa v65, v65 dst_sel:WORD_1 dst_unused:UNUSED_PAD src0_sel:DWORD
	v_cvt_i32_f32_e32 v66, v66
	v_lshlrev_b32_e32 v64, 8, v64
	v_and_b32_e32 v64, 0xff00, v64
	v_and_b32_e32 v65, 0xff0000, v65
	v_perm_b32 v49, v66, v49, s65
	v_or3_b32 v49, v49, v64, v65
	global_store_dword v[62:63], v49, off offset:768
	s_mov_b64 s[0:1], 0
